# in-projection epilogue: tile types 2,3,5,6 run straight-line copies without the per-element scalar type tests (on top of v12)
# speedup vs baseline: 1.0115x; 1.0034x over previous
.LBB0_304:
	v_lshl_add_u32 v106, s10, 8, v160
	v_ashrrev_i32_e32 v107, 31, v106
	v_lshl_add_u64 v[108:109], v[106:107], 2, s[30:31]
	v_add_u32_e32 v110, 0x80, v106
	v_add_u32_e32 v112, 0x90, v106
	v_add_u32_e32 v126, 0xa0, v106
	v_add_u32_e32 v106, 0xb0, v106
	v_ashrrev_i32_e32 v111, 31, v110
	v_ashrrev_i32_e32 v113, 31, v112
	v_ashrrev_i32_e32 v127, 31, v126
	v_ashrrev_i32_e32 v107, 31, v106
	v_lshl_add_u64 v[110:111], v[110:111], 2, s[30:31]
	v_lshl_add_u64 v[112:113], v[112:113], 2, s[30:31]
	v_lshl_add_u64 v[126:127], v[126:127], 2, s[30:31]
	v_lshl_add_u64 v[106:107], v[106:107], 2, s[30:31]
	global_load_dword v194, v[108:109], off
	global_load_dword v192, v[108:109], off offset:64
	global_load_dword v190, v[108:109], off offset:128
	global_load_dword v188, v[108:109], off offset:192
	global_load_dword v186, v[110:111], off
	global_load_dword v184, v[112:113], off
	global_load_dword v182, v[126:127], off
	global_load_dword v180, v[106:107], off
	s_lshl_b32 s66, s64, 8
	s_ashr_i32 s67, s66, 31
	v_lshl_add_u64 v[110:111], s[66:67], 2, v[164:165]
	global_load_dwordx4 v[126:129], v[110:111], off offset:16
	global_load_dwordx4 v[130:133], v[110:111], off
	global_load_dwordx4 v[106:109], v[110:111], off offset:528
	s_nop 0
	global_load_dwordx4 v[110:113], v[110:111], off offset:512
	s_lshl_b32 s11, s64, 1
	s_and_b32 s57, s11, 14
	s_ashr_i32 s11, s10, 31
	s_ashr_i32 s59, s64, 3
	s_lshl_b64 s[10:11], s[10:11], 8
	v_lshl_add_u64 v[178:179], s[10:11], 0, v[160:161]
	s_cmp_gt_i32 s59, 1
	s_mov_b64 s[10:11], -1
	s_cbranch_scc0 .LBB0_320
	s_cmp_eq_u32 s59, 4
	s_cbranch_scc0 .Lepi_spec
	s_cmp_lt_i32 s59, 4
	s_cbranch_scc1 .LBB0_311
	s_cmp_gt_i32 s59, 4
	s_cbranch_scc0 .LBB0_357
	s_mov_b64 s[66:67], -1
	s_mov_b64 s[68:69], 0
	s_cmp_eq_u32 s59, 5
	s_mov_b64 s[10:11], 0
	s_cbranch_scc0 .LBB0_309
	s_mov_b64 s[66:67], 0
	s_mov_b64 s[10:11], -1

.Lepi_spec:
	s_cmp_lt_i32 s59, 4
	s_cbranch_scc1 .Lepi_lo
	s_cmp_eq_u32 s59, 5
	s_cbranch_scc1 .Lepi_t5
	s_mov_b64 s[68:69], s[24:25]
	s_mov_b64 s[68:69], s[28:29]
	v_mov_b64_e32 v[196:197], v[166:167]
	s_cmp_eq_u32 s59, 3
	s_cselect_b64 s[10:11], -1, 0
	v_cvt_f32_i32_e32 v147, v143
	v_cvt_f32_i32_e32 v146, v142
	s_waitcnt vmcnt(0)
	v_pk_mul_f32 v[148:149], v[194:195], v[130:131] op_sel_hi:[0,1]
	v_cndmask_b32_e64 v219, 1.0, v217, s[10:11]
	v_pk_mul_f32 v[146:147], v[148:149], v[146:147]
	v_mul_f32_e32 v148, 0xbfb8aa3b, v146
	v_exp_f32_e32 v148, v148
	v_mul_f32_e32 v146, v219, v146
	v_add_f32_e32 v148, 1.0, v148
	v_rcp_f32_e32 v148, v148
	s_nop 0
	v_mul_f32_e32 v146, v146, v148
	v_cvt_f32_i32_e32 v149, v145
	v_cvt_f32_i32_e32 v148, v144
	v_mov_b32_e32 v195, v194
	v_pk_mul_f32 v[196:197], v[194:195], v[132:133] op_sel_hi:[0,1]
	v_pk_mul_f32 v[148:149], v[196:197], v[148:149]
	v_mul_f32_e32 v158, 0xbfb8aa3b, v147
	v_exp_f32_e32 v158, v158
	v_mul_f32_e32 v147, v219, v147
	v_add_f32_e32 v158, 1.0, v158
	v_rcp_f32_e32 v158, v158
	s_nop 0
	v_mul_f32_e32 v147, v147, v158
	v_mul_f32_e32 v158, 0xbfb8aa3b, v148
	v_exp_f32_e32 v158, v158
	v_mul_f32_e32 v148, v219, v148
	v_add_f32_e32 v158, 1.0, v158
	v_rcp_f32_e32 v158, v158
	s_nop 0
	v_mul_f32_e32 v148, v148, v158
	v_mul_f32_e32 v158, 0xbfb8aa3b, v149
	v_exp_f32_e32 v158, v158
	v_mul_f32_e32 v149, v219, v149
	v_add_f32_e32 v158, 1.0, v158
	v_rcp_f32_e32 v158, v158
	s_nop 0
	v_mul_f32_e32 v149, v149, v158
	v_cvt_f32_i32_e32 v197, v139
	v_cvt_f32_i32_e32 v196, v138
	v_pk_mul_f32 v[198:199], v[194:195], v[126:127]
	v_pk_mul_f32 v[198:199], v[198:199], v[196:197]
	v_mul_f32_e32 v158, 0xbfb8aa3b, v198
	v_exp_f32_e32 v158, v158
	v_mul_f32_e32 v181, v219, v198
	v_add_f32_e32 v158, 1.0, v158
	v_rcp_f32_e32 v158, v158
	s_nop 0
	v_mul_f32_e32 v198, v181, v158
	v_cvt_f32_i32_e32 v197, v141
	v_cvt_f32_i32_e32 v196, v140
	v_mov_b32_e32 v200, v194
	v_mov_b32_e32 v201, v194
	v_pk_mul_f32 v[200:201], v[200:201], v[128:129]
	v_pk_mul_f32 v[200:201], v[200:201], v[196:197]
	v_mul_f32_e32 v158, 0xbfb8aa3b, v199
	v_exp_f32_e32 v158, v158
	v_mul_f32_e32 v181, v219, v199
	v_add_f32_e32 v158, 1.0, v158
	v_rcp_f32_e32 v158, v158
	s_nop 0
	v_mul_f32_e32 v199, v181, v158
	v_mul_f32_e32 v158, 0xbfb8aa3b, v200
	v_exp_f32_e32 v158, v158
	v_mul_f32_e32 v181, v219, v200
	v_add_f32_e32 v158, 1.0, v158
	v_rcp_f32_e32 v158, v158
	s_nop 0
	v_mul_f32_e32 v200, v181, v158
	v_mul_f32_e32 v158, 0xbfb8aa3b, v201
	v_exp_f32_e32 v158, v158
	v_mul_f32_e32 v181, v219, v201
	v_add_f32_e32 v158, 1.0, v158
	v_rcp_f32_e32 v158, v158
	s_nop 0
	v_mul_f32_e32 v201, v181, v158
	s_lshl_b32 s16, s57, 13
	v_lshlrev_b32_e32 v158, 1, v162
	v_cvt_pk_bf16_f32 v146, v146, v147
	v_cvt_pk_bf16_f32 v147, v148, v149
	v_cvt_pk_bf16_f32 v148, v198, v199
	v_lshl_add_u64 v[198:199], v[178:179], 0, s[16:17]
	v_lshl_add_u64 v[196:197], s[68:69], 0, v[158:159]
	v_lshlrev_b64 v[198:199], 8, v[198:199]
	v_lshl_add_u64 v[198:199], v[196:197], 0, v[198:199]
	v_cvt_pk_bf16_f32 v149, v200, v201
	global_store_dwordx4 v[198:199], v[146:149], off
	s_nop 1
	v_cvt_f32_i32_e32 v147, v135
	v_cvt_f32_i32_e32 v146, v134
	v_pk_mul_f32 v[148:149], v[194:195], v[110:111]
	v_pk_mul_f32 v[146:147], v[148:149], v[146:147]
	v_mul_f32_e32 v148, 0xbfb8aa3b, v146
	v_exp_f32_e32 v148, v148
	v_mul_f32_e32 v146, v219, v146
	v_add_f32_e32 v148, 1.0, v148
	v_rcp_f32_e32 v148, v148
	s_nop 0
	v_mul_f32_e32 v146, v146, v148
	v_cvt_f32_i32_e32 v149, v137
	v_cvt_f32_i32_e32 v148, v136
	v_mov_b32_e32 v198, v194
	v_mov_b32_e32 v199, v194
	v_pk_mul_f32 v[198:199], v[198:199], v[112:113]
	v_pk_mul_f32 v[148:149], v[198:199], v[148:149]
	v_mul_f32_e32 v158, 0xbfb8aa3b, v147
	v_exp_f32_e32 v158, v158
	v_mul_f32_e32 v147, v219, v147
	v_add_f32_e32 v158, 1.0, v158
	v_rcp_f32_e32 v158, v158
	s_nop 0
	v_mul_f32_e32 v147, v147, v158
	v_mul_f32_e32 v158, 0xbfb8aa3b, v148
	v_exp_f32_e32 v158, v158
	v_mul_f32_e32 v148, v219, v148
	v_add_f32_e32 v158, 1.0, v158
	v_rcp_f32_e32 v158, v158
	s_nop 0
	v_mul_f32_e32 v148, v148, v158
	v_mul_f32_e32 v158, 0xbfb8aa3b, v149
	v_exp_f32_e32 v158, v158
	v_mul_f32_e32 v149, v219, v149
	v_add_f32_e32 v158, 1.0, v158
	v_rcp_f32_e32 v158, v158
	s_nop 0
	v_mul_f32_e32 v149, v149, v158
	v_cvt_f32_i32_e32 v199, v123
	v_cvt_f32_i32_e32 v198, v122
	v_pk_mul_f32 v[200:201], v[194:195], v[106:107]
	v_pk_mul_f32 v[198:199], v[200:201], v[198:199]
	v_mul_f32_e32 v158, 0xbfb8aa3b, v198
	v_exp_f32_e32 v158, v158
	v_mul_f32_e32 v181, v219, v198
	v_add_f32_e32 v158, 1.0, v158
	v_rcp_f32_e32 v158, v158
	s_nop 0
	v_mul_f32_e32 v198, v181, v158
	v_cvt_f32_i32_e32 v201, v125
	v_cvt_f32_i32_e32 v200, v124
	v_mov_b32_e32 v195, v194
	v_pk_mul_f32 v[202:203], v[194:195], v[108:109]
	v_pk_mul_f32 v[200:201], v[202:203], v[200:201]
	v_mul_f32_e32 v158, 0xbfb8aa3b, v199
	v_exp_f32_e32 v158, v158
	v_mul_f32_e32 v181, v219, v199
	v_add_f32_e32 v158, 1.0, v158
	v_rcp_f32_e32 v158, v158
	s_nop 0
	v_mul_f32_e32 v199, v181, v158
	v_mul_f32_e32 v158, 0xbfb8aa3b, v200
	v_exp_f32_e32 v158, v158
	v_mul_f32_e32 v181, v219, v200
	v_add_f32_e32 v158, 1.0, v158
	v_rcp_f32_e32 v158, v158
	s_nop 0
	v_mul_f32_e32 v200, v181, v158
	v_mul_f32_e32 v158, 0xbfb8aa3b, v201
	v_exp_f32_e32 v158, v158
	v_mul_f32_e32 v181, v219, v201
	v_add_f32_e32 v158, 1.0, v158
	v_rcp_f32_e32 v158, v158
	s_nop 0
	v_mul_f32_e32 v201, v181, v158
	s_or_b32 s10, s16, 0x2000
	s_mov_b32 s11, s17
	v_cvt_pk_bf16_f32 v146, v146, v147
	v_cvt_pk_bf16_f32 v147, v148, v149
	v_cvt_pk_bf16_f32 v148, v198, v199
	v_lshl_add_u64 v[198:199], v[178:179], 0, s[10:11]
	v_lshlrev_b64 v[198:199], 8, v[198:199]
	v_lshl_add_u64 v[198:199], v[196:197], 0, v[198:199]
	v_cvt_pk_bf16_f32 v149, v200, v201
	global_store_dwordx4 v[198:199], v[146:149], off
	s_nop 1
	v_cvt_f32_i32_e32 v147, v119
	v_cvt_f32_i32_e32 v146, v118
	v_pk_mul_f32 v[148:149], v[192:193], v[130:131] op_sel_hi:[0,1]
	v_pk_mul_f32 v[148:149], v[148:149], v[146:147]
	v_mul_f32_e32 v146, 0xbfb8aa3b, v148
	v_exp_f32_e32 v146, v146
	v_mul_f32_e32 v147, v219, v148
	v_add_f32_e32 v146, 1.0, v146
	v_rcp_f32_e32 v146, v146
	s_nop 0
	v_mul_f32_e32 v148, v147, v146
	v_cvt_f32_i32_e32 v147, v121
	v_cvt_f32_i32_e32 v146, v120
	v_mov_b32_e32 v193, v192
	v_pk_mul_f32 v[198:199], v[192:193], v[132:133] op_sel_hi:[0,1]
	v_pk_mul_f32 v[198:199], v[198:199], v[146:147]
	v_mul_f32_e32 v146, 0xbfb8aa3b, v149
	v_exp_f32_e32 v146, v146
	v_mul_f32_e32 v147, v219, v149
	v_add_f32_e32 v146, 1.0, v146
	v_rcp_f32_e32 v146, v146
	s_nop 0
	v_mul_f32_e32 v149, v147, v146
	v_mul_f32_e32 v146, 0xbfb8aa3b, v198
	v_exp_f32_e32 v146, v146
	v_mul_f32_e32 v147, v219, v198
	v_add_f32_e32 v146, 1.0, v146
	v_rcp_f32_e32 v146, v146
	s_nop 0
	v_mul_f32_e32 v198, v147, v146
	v_mul_f32_e32 v146, 0xbfb8aa3b, v199
	v_exp_f32_e32 v146, v146
	v_mul_f32_e32 v147, v219, v199
	v_add_f32_e32 v146, 1.0, v146
	v_rcp_f32_e32 v146, v146
	s_nop 0
	v_mul_f32_e32 v199, v147, v146
	v_cvt_f32_i32_e32 v147, v115
	v_cvt_f32_i32_e32 v146, v114
	v_pk_mul_f32 v[200:201], v[192:193], v[126:127]
	v_pk_mul_f32 v[200:201], v[200:201], v[146:147]
	v_mul_f32_e32 v146, 0xbfb8aa3b, v200
	v_exp_f32_e32 v146, v146
	v_mul_f32_e32 v147, v219, v200
	v_add_f32_e32 v146, 1.0, v146
	v_rcp_f32_e32 v146, v146
	s_nop 0
	v_mul_f32_e32 v200, v147, v146
	v_cvt_f32_i32_e32 v147, v117
	v_cvt_f32_i32_e32 v146, v116
	v_mov_b32_e32 v202, v192
	v_mov_b32_e32 v203, v192
	v_pk_mul_f32 v[202:203], v[202:203], v[128:129]
	v_pk_mul_f32 v[202:203], v[202:203], v[146:147]
	v_mul_f32_e32 v146, 0xbfb8aa3b, v201
	v_exp_f32_e32 v146, v146
	v_mul_f32_e32 v147, v219, v201
	v_add_f32_e32 v146, 1.0, v146
	v_rcp_f32_e32 v146, v146
	s_nop 0
	v_mul_f32_e32 v201, v147, v146
	v_mul_f32_e32 v146, 0xbfb8aa3b, v202
	v_exp_f32_e32 v146, v146
	v_mul_f32_e32 v147, v219, v202
	v_add_f32_e32 v146, 1.0, v146
	v_rcp_f32_e32 v146, v146
	s_nop 0
	v_mul_f32_e32 v202, v147, v146
	v_mul_f32_e32 v146, 0xbfb8aa3b, v203
	v_exp_f32_e32 v146, v146
	v_mul_f32_e32 v147, v219, v203
	v_add_f32_e32 v146, 1.0, v146
	v_rcp_f32_e32 v146, v146
	s_nop 0
	v_mul_f32_e32 v203, v147, v146
	v_or_b32_e32 v146, 16, v178
	v_mov_b32_e32 v147, v179
	v_cvt_pk_bf16_f32 v220, v148, v149
	v_lshl_add_u64 v[148:149], v[146:147], 0, s[16:17]
	v_lshlrev_b64 v[148:149], 8, v[148:149]
	v_lshl_add_u64 v[148:149], v[196:197], 0, v[148:149]
	v_cvt_pk_bf16_f32 v221, v198, v199
	v_cvt_pk_bf16_f32 v222, v200, v201
	v_cvt_pk_bf16_f32 v223, v202, v203
	global_store_dwordx4 v[148:149], v[220:223], off
	s_nop 1
	v_cvt_f32_i32_e32 v149, v103
	v_cvt_f32_i32_e32 v148, v102
	v_pk_mul_f32 v[198:199], v[192:193], v[110:111]
	v_pk_mul_f32 v[148:149], v[198:199], v[148:149]
	v_mul_f32_e32 v158, 0xbfb8aa3b, v148
	v_exp_f32_e32 v158, v158
	v_mul_f32_e32 v148, v219, v148
	v_add_f32_e32 v158, 1.0, v158
	v_rcp_f32_e32 v158, v158
	s_nop 0
	v_mul_f32_e32 v148, v148, v158
	v_cvt_f32_i32_e32 v199, v105
	v_cvt_f32_i32_e32 v198, v104
	v_mov_b32_e32 v200, v192
	v_mov_b32_e32 v201, v192
	v_pk_mul_f32 v[200:201], v[200:201], v[112:113]
	v_pk_mul_f32 v[198:199], v[200:201], v[198:199]
	v_mul_f32_e32 v158, 0xbfb8aa3b, v149
	v_exp_f32_e32 v158, v158
	v_mul_f32_e32 v149, v219, v149
	v_add_f32_e32 v158, 1.0, v158
	v_rcp_f32_e32 v158, v158
	s_nop 0
	v_mul_f32_e32 v149, v149, v158
	v_mul_f32_e32 v158, 0xbfb8aa3b, v198
	v_exp_f32_e32 v158, v158
	v_mul_f32_e32 v181, v219, v198
	v_add_f32_e32 v158, 1.0, v158
	v_rcp_f32_e32 v158, v158
	s_nop 0
	v_mul_f32_e32 v198, v181, v158
	v_mul_f32_e32 v158, 0xbfb8aa3b, v199
	v_exp_f32_e32 v158, v158
	v_mul_f32_e32 v181, v219, v199
	v_add_f32_e32 v158, 1.0, v158
	v_rcp_f32_e32 v158, v158
	s_nop 0
	v_mul_f32_e32 v199, v181, v158
	v_cvt_f32_i32_e32 v201, v99
	v_cvt_f32_i32_e32 v200, v98
	v_pk_mul_f32 v[202:203], v[192:193], v[106:107]
	v_pk_mul_f32 v[200:201], v[202:203], v[200:201]
	v_mul_f32_e32 v158, 0xbfb8aa3b, v200
	v_exp_f32_e32 v158, v158
	v_mul_f32_e32 v181, v219, v200
	v_add_f32_e32 v158, 1.0, v158
	v_rcp_f32_e32 v158, v158
	s_nop 0
	v_mul_f32_e32 v200, v181, v158
	v_cvt_f32_i32_e32 v203, v101
	v_cvt_f32_i32_e32 v202, v100
	v_mov_b32_e32 v193, v192
	v_pk_mul_f32 v[220:221], v[192:193], v[108:109]
	v_pk_mul_f32 v[202:203], v[220:221], v[202:203]
	v_mul_f32_e32 v158, 0xbfb8aa3b, v201
	v_exp_f32_e32 v158, v158
	v_mul_f32_e32 v181, v219, v201
	v_add_f32_e32 v158, 1.0, v158
	v_rcp_f32_e32 v158, v158
	s_nop 0
	v_mul_f32_e32 v201, v181, v158
	v_mul_f32_e32 v158, 0xbfb8aa3b, v202
	v_exp_f32_e32 v158, v158
	v_mul_f32_e32 v181, v219, v202
	v_add_f32_e32 v158, 1.0, v158
	v_rcp_f32_e32 v158, v158
	s_nop 0
	v_mul_f32_e32 v202, v181, v158
	v_mul_f32_e32 v158, 0xbfb8aa3b, v203
	v_exp_f32_e32 v158, v158
	v_mul_f32_e32 v181, v219, v203
	v_add_f32_e32 v158, 1.0, v158
	v_rcp_f32_e32 v158, v158
	s_nop 0
	v_mul_f32_e32 v203, v181, v158
	v_lshl_add_u64 v[146:147], v[146:147], 0, s[10:11]
	v_lshlrev_b64 v[146:147], 8, v[146:147]
	v_lshl_add_u64 v[146:147], v[196:197], 0, v[146:147]
	v_cvt_pk_bf16_f32 v220, v148, v149
	v_cvt_pk_bf16_f32 v221, v198, v199
	v_cvt_pk_bf16_f32 v222, v200, v201
	v_cvt_pk_bf16_f32 v223, v202, v203
	global_store_dwordx4 v[146:147], v[220:223], off
	s_nop 1
	v_cvt_f32_i32_e32 v147, v95
	v_cvt_f32_i32_e32 v146, v94
	v_pk_mul_f32 v[148:149], v[190:191], v[130:131] op_sel_hi:[0,1]
	v_pk_mul_f32 v[148:149], v[148:149], v[146:147]
	v_mul_f32_e32 v146, 0xbfb8aa3b, v148
	v_exp_f32_e32 v146, v146
	v_mul_f32_e32 v147, v219, v148
	v_add_f32_e32 v146, 1.0, v146
	v_rcp_f32_e32 v146, v146
	s_nop 0
	v_mul_f32_e32 v148, v147, v146
	v_cvt_f32_i32_e32 v147, v97
	v_cvt_f32_i32_e32 v146, v96
	v_mov_b32_e32 v191, v190
	v_pk_mul_f32 v[198:199], v[190:191], v[132:133] op_sel_hi:[0,1]
	v_pk_mul_f32 v[198:199], v[198:199], v[146:147]
	v_mul_f32_e32 v146, 0xbfb8aa3b, v149
	v_exp_f32_e32 v146, v146
	v_mul_f32_e32 v147, v219, v149
	v_add_f32_e32 v146, 1.0, v146
	v_rcp_f32_e32 v146, v146
	s_nop 0
	v_mul_f32_e32 v149, v147, v146
	v_mul_f32_e32 v146, 0xbfb8aa3b, v198
	v_exp_f32_e32 v146, v146
	v_mul_f32_e32 v147, v219, v198
	v_add_f32_e32 v146, 1.0, v146
	v_rcp_f32_e32 v146, v146
	s_nop 0
	v_mul_f32_e32 v198, v147, v146
	v_mul_f32_e32 v146, 0xbfb8aa3b, v199
	v_exp_f32_e32 v146, v146
	v_mul_f32_e32 v147, v219, v199
	v_add_f32_e32 v146, 1.0, v146
	v_rcp_f32_e32 v146, v146
	s_nop 0
	v_mul_f32_e32 v199, v147, v146
	v_cvt_f32_i32_e32 v147, v91
	v_cvt_f32_i32_e32 v146, v90
	v_pk_mul_f32 v[200:201], v[190:191], v[126:127]
	v_pk_mul_f32 v[200:201], v[200:201], v[146:147]
	v_mul_f32_e32 v146, 0xbfb8aa3b, v200
	v_exp_f32_e32 v146, v146
	v_mul_f32_e32 v147, v219, v200
	v_add_f32_e32 v146, 1.0, v146
	v_rcp_f32_e32 v146, v146
	s_nop 0
	v_mul_f32_e32 v200, v147, v146
	v_cvt_f32_i32_e32 v147, v93
	v_cvt_f32_i32_e32 v146, v92
	v_mov_b32_e32 v202, v190
	v_mov_b32_e32 v203, v190
	v_pk_mul_f32 v[202:203], v[202:203], v[128:129]
	v_pk_mul_f32 v[202:203], v[202:203], v[146:147]
	v_mul_f32_e32 v146, 0xbfb8aa3b, v201
	v_exp_f32_e32 v146, v146
	v_mul_f32_e32 v147, v219, v201
	v_add_f32_e32 v146, 1.0, v146
	v_rcp_f32_e32 v146, v146
	s_nop 0
	v_mul_f32_e32 v201, v147, v146
	v_mul_f32_e32 v146, 0xbfb8aa3b, v202
	v_exp_f32_e32 v146, v146
	v_mul_f32_e32 v147, v219, v202
	v_add_f32_e32 v146, 1.0, v146
	v_rcp_f32_e32 v146, v146
	s_nop 0
	v_mul_f32_e32 v202, v147, v146
	v_mul_f32_e32 v146, 0xbfb8aa3b, v203
	v_exp_f32_e32 v146, v146
	v_mul_f32_e32 v147, v219, v203
	v_add_f32_e32 v146, 1.0, v146
	v_rcp_f32_e32 v146, v146
	s_nop 0
	v_mul_f32_e32 v203, v147, v146
	v_or_b32_e32 v146, 32, v178
	v_mov_b32_e32 v147, v179
	v_cvt_pk_bf16_f32 v220, v148, v149
	v_lshl_add_u64 v[148:149], v[146:147], 0, s[16:17]
	v_lshlrev_b64 v[148:149], 8, v[148:149]
	v_lshl_add_u64 v[148:149], v[196:197], 0, v[148:149]
	v_cvt_pk_bf16_f32 v221, v198, v199
	v_cvt_pk_bf16_f32 v222, v200, v201
	v_cvt_pk_bf16_f32 v223, v202, v203
	global_store_dwordx4 v[148:149], v[220:223], off
	s_nop 1
	v_cvt_f32_i32_e32 v149, v87
	v_cvt_f32_i32_e32 v148, v86
	v_pk_mul_f32 v[198:199], v[190:191], v[110:111]
	v_pk_mul_f32 v[148:149], v[198:199], v[148:149]
	v_mul_f32_e32 v158, 0xbfb8aa3b, v148
	v_exp_f32_e32 v158, v158
	v_mul_f32_e32 v148, v219, v148
	v_add_f32_e32 v158, 1.0, v158
	v_rcp_f32_e32 v158, v158
	s_nop 0
	v_mul_f32_e32 v148, v148, v158
	v_cvt_f32_i32_e32 v199, v89
	v_cvt_f32_i32_e32 v198, v88
	v_mov_b32_e32 v200, v190
	v_mov_b32_e32 v201, v190
	v_pk_mul_f32 v[200:201], v[200:201], v[112:113]
	v_pk_mul_f32 v[198:199], v[200:201], v[198:199]
	v_mul_f32_e32 v158, 0xbfb8aa3b, v149
	v_exp_f32_e32 v158, v158
	v_mul_f32_e32 v149, v219, v149
	v_add_f32_e32 v158, 1.0, v158
	v_rcp_f32_e32 v158, v158
	s_nop 0
	v_mul_f32_e32 v149, v149, v158
	v_mul_f32_e32 v158, 0xbfb8aa3b, v198
	v_exp_f32_e32 v158, v158
	v_mul_f32_e32 v181, v219, v198
	v_add_f32_e32 v158, 1.0, v158
	v_rcp_f32_e32 v158, v158
	s_nop 0
	v_mul_f32_e32 v198, v181, v158
	v_mul_f32_e32 v158, 0xbfb8aa3b, v199
	v_exp_f32_e32 v158, v158
	v_mul_f32_e32 v181, v219, v199
	v_add_f32_e32 v158, 1.0, v158
	v_rcp_f32_e32 v158, v158
	s_nop 0
	v_mul_f32_e32 v199, v181, v158
	v_cvt_f32_i32_e32 v201, v83
	v_cvt_f32_i32_e32 v200, v82
	v_pk_mul_f32 v[202:203], v[190:191], v[106:107]
	v_pk_mul_f32 v[200:201], v[202:203], v[200:201]
	v_mul_f32_e32 v158, 0xbfb8aa3b, v200
	v_exp_f32_e32 v158, v158
	v_mul_f32_e32 v181, v219, v200
	v_add_f32_e32 v158, 1.0, v158
	v_rcp_f32_e32 v158, v158
	s_nop 0
	v_mul_f32_e32 v200, v181, v158
	v_cvt_f32_i32_e32 v203, v85
	v_cvt_f32_i32_e32 v202, v84
	v_mov_b32_e32 v191, v190
	v_pk_mul_f32 v[220:221], v[190:191], v[108:109]
	v_pk_mul_f32 v[202:203], v[220:221], v[202:203]
	v_mul_f32_e32 v158, 0xbfb8aa3b, v201
	v_exp_f32_e32 v158, v158
	v_mul_f32_e32 v181, v219, v201
	v_add_f32_e32 v158, 1.0, v158
	v_rcp_f32_e32 v158, v158
	s_nop 0
	v_mul_f32_e32 v201, v181, v158
	v_mul_f32_e32 v158, 0xbfb8aa3b, v202
	v_exp_f32_e32 v158, v158
	v_mul_f32_e32 v181, v219, v202
	v_add_f32_e32 v158, 1.0, v158
	v_rcp_f32_e32 v158, v158
	s_nop 0
	v_mul_f32_e32 v202, v181, v158
	v_mul_f32_e32 v158, 0xbfb8aa3b, v203
	v_exp_f32_e32 v158, v158
	v_mul_f32_e32 v181, v219, v203
	v_add_f32_e32 v158, 1.0, v158
	v_rcp_f32_e32 v158, v158
	s_nop 0
	v_mul_f32_e32 v203, v181, v158
	v_lshl_add_u64 v[146:147], v[146:147], 0, s[10:11]
	v_lshlrev_b64 v[146:147], 8, v[146:147]
	v_lshl_add_u64 v[146:147], v[196:197], 0, v[146:147]
	v_cvt_pk_bf16_f32 v220, v148, v149
	v_cvt_pk_bf16_f32 v221, v198, v199
	v_cvt_pk_bf16_f32 v222, v200, v201
	v_cvt_pk_bf16_f32 v223, v202, v203
	global_store_dwordx4 v[146:147], v[220:223], off
	s_nop 1
	v_cvt_f32_i32_e32 v147, v79
	v_cvt_f32_i32_e32 v146, v78
	v_pk_mul_f32 v[148:149], v[188:189], v[130:131] op_sel_hi:[0,1]
	v_pk_mul_f32 v[148:149], v[148:149], v[146:147]
	v_mul_f32_e32 v146, 0xbfb8aa3b, v148
	v_exp_f32_e32 v146, v146
	v_mul_f32_e32 v147, v219, v148
	v_add_f32_e32 v146, 1.0, v146
	v_rcp_f32_e32 v146, v146
	s_nop 0
	v_mul_f32_e32 v148, v147, v146
	v_cvt_f32_i32_e32 v147, v81
	v_cvt_f32_i32_e32 v146, v80
	v_mov_b32_e32 v189, v188
	v_pk_mul_f32 v[198:199], v[188:189], v[132:133] op_sel_hi:[0,1]
	v_pk_mul_f32 v[198:199], v[198:199], v[146:147]
	v_mul_f32_e32 v146, 0xbfb8aa3b, v149
	v_exp_f32_e32 v146, v146
	v_mul_f32_e32 v147, v219, v149
	v_add_f32_e32 v146, 1.0, v146
	v_rcp_f32_e32 v146, v146
	s_nop 0
	v_mul_f32_e32 v149, v147, v146
	v_mul_f32_e32 v146, 0xbfb8aa3b, v198
	v_exp_f32_e32 v146, v146
	v_mul_f32_e32 v147, v219, v198
	v_add_f32_e32 v146, 1.0, v146
	v_rcp_f32_e32 v146, v146
	s_nop 0
	v_mul_f32_e32 v198, v147, v146
	v_mul_f32_e32 v146, 0xbfb8aa3b, v199
	v_exp_f32_e32 v146, v146
	v_mul_f32_e32 v147, v219, v199
	v_add_f32_e32 v146, 1.0, v146
	v_rcp_f32_e32 v146, v146
	s_nop 0
	v_mul_f32_e32 v199, v147, v146
	v_cvt_f32_i32_e32 v147, v75
	v_cvt_f32_i32_e32 v146, v74
	v_pk_mul_f32 v[200:201], v[188:189], v[126:127]
	v_pk_mul_f32 v[200:201], v[200:201], v[146:147]
	v_mul_f32_e32 v146, 0xbfb8aa3b, v200
	v_exp_f32_e32 v146, v146
	v_mul_f32_e32 v147, v219, v200
	v_add_f32_e32 v146, 1.0, v146
	v_rcp_f32_e32 v146, v146
	s_nop 0
	v_mul_f32_e32 v200, v147, v146
	v_cvt_f32_i32_e32 v147, v77
	v_cvt_f32_i32_e32 v146, v76
	v_mov_b32_e32 v202, v188
	v_mov_b32_e32 v203, v188
	v_pk_mul_f32 v[202:203], v[202:203], v[128:129]
	v_pk_mul_f32 v[202:203], v[202:203], v[146:147]
	v_mul_f32_e32 v146, 0xbfb8aa3b, v201
	v_exp_f32_e32 v146, v146
	v_mul_f32_e32 v147, v219, v201
	v_add_f32_e32 v146, 1.0, v146
	v_rcp_f32_e32 v146, v146
	s_nop 0
	v_mul_f32_e32 v201, v147, v146
	v_mul_f32_e32 v146, 0xbfb8aa3b, v202
	v_exp_f32_e32 v146, v146
	v_mul_f32_e32 v147, v219, v202
	v_add_f32_e32 v146, 1.0, v146
	v_rcp_f32_e32 v146, v146
	s_nop 0
	v_mul_f32_e32 v202, v147, v146
	v_mul_f32_e32 v146, 0xbfb8aa3b, v203
	v_exp_f32_e32 v146, v146
	v_mul_f32_e32 v147, v219, v203
	v_add_f32_e32 v146, 1.0, v146
	v_rcp_f32_e32 v146, v146
	s_nop 0
	v_mul_f32_e32 v203, v147, v146
	v_or_b32_e32 v146, 48, v178
	v_mov_b32_e32 v147, v179
	v_cvt_pk_bf16_f32 v220, v148, v149
	v_lshl_add_u64 v[148:149], v[146:147], 0, s[16:17]
	v_lshlrev_b64 v[148:149], 8, v[148:149]
	v_lshl_add_u64 v[148:149], v[196:197], 0, v[148:149]
	v_cvt_pk_bf16_f32 v221, v198, v199
	v_cvt_pk_bf16_f32 v222, v200, v201
	v_cvt_pk_bf16_f32 v223, v202, v203
	global_store_dwordx4 v[148:149], v[220:223], off
	s_nop 1
	v_cvt_f32_i32_e32 v149, v71
	v_cvt_f32_i32_e32 v148, v70
	v_pk_mul_f32 v[198:199], v[188:189], v[110:111]
	v_pk_mul_f32 v[148:149], v[198:199], v[148:149]
	v_mul_f32_e32 v158, 0xbfb8aa3b, v148
	v_exp_f32_e32 v158, v158
	v_mul_f32_e32 v148, v219, v148
	v_add_f32_e32 v158, 1.0, v158
	v_rcp_f32_e32 v158, v158
	s_nop 0
	v_mul_f32_e32 v148, v148, v158
	v_cvt_f32_i32_e32 v199, v73
	v_cvt_f32_i32_e32 v198, v72
	v_mov_b32_e32 v200, v188
	v_mov_b32_e32 v201, v188
	v_pk_mul_f32 v[200:201], v[200:201], v[112:113]
	v_pk_mul_f32 v[198:199], v[200:201], v[198:199]
	v_mul_f32_e32 v158, 0xbfb8aa3b, v149
	v_exp_f32_e32 v158, v158
	v_mul_f32_e32 v149, v219, v149
	v_add_f32_e32 v158, 1.0, v158
	v_rcp_f32_e32 v158, v158
	s_nop 0
	v_mul_f32_e32 v149, v149, v158
	v_mul_f32_e32 v158, 0xbfb8aa3b, v198
	v_exp_f32_e32 v158, v158
	v_mul_f32_e32 v181, v219, v198
	v_add_f32_e32 v158, 1.0, v158
	v_rcp_f32_e32 v158, v158
	s_nop 0
	v_mul_f32_e32 v198, v181, v158
	v_mul_f32_e32 v158, 0xbfb8aa3b, v199
	v_exp_f32_e32 v158, v158
	v_mul_f32_e32 v181, v219, v199
	v_add_f32_e32 v158, 1.0, v158
	v_rcp_f32_e32 v158, v158
	s_nop 0
	v_mul_f32_e32 v199, v181, v158
	v_cvt_f32_i32_e32 v201, v67
	v_cvt_f32_i32_e32 v200, v66
	v_pk_mul_f32 v[202:203], v[188:189], v[106:107]
	v_pk_mul_f32 v[200:201], v[202:203], v[200:201]
	v_mul_f32_e32 v158, 0xbfb8aa3b, v200
	v_exp_f32_e32 v158, v158
	v_mul_f32_e32 v181, v219, v200
	v_add_f32_e32 v158, 1.0, v158
	v_rcp_f32_e32 v158, v158
	s_nop 0
	v_mul_f32_e32 v200, v181, v158
	v_cvt_f32_i32_e32 v203, v69
	v_cvt_f32_i32_e32 v202, v68
	v_mov_b32_e32 v189, v188
	v_pk_mul_f32 v[220:221], v[188:189], v[108:109]
	v_pk_mul_f32 v[202:203], v[220:221], v[202:203]
	v_mul_f32_e32 v158, 0xbfb8aa3b, v201
	v_exp_f32_e32 v158, v158
	v_mul_f32_e32 v181, v219, v201
	v_add_f32_e32 v158, 1.0, v158
	v_rcp_f32_e32 v158, v158
	s_nop 0
	v_mul_f32_e32 v201, v181, v158
	v_mul_f32_e32 v158, 0xbfb8aa3b, v202
	v_exp_f32_e32 v158, v158
	v_mul_f32_e32 v181, v219, v202
	v_add_f32_e32 v158, 1.0, v158
	v_rcp_f32_e32 v158, v158
	s_nop 0
	v_mul_f32_e32 v202, v181, v158
	v_mul_f32_e32 v158, 0xbfb8aa3b, v203
	v_exp_f32_e32 v158, v158
	v_mul_f32_e32 v181, v219, v203
	v_add_f32_e32 v158, 1.0, v158
	v_rcp_f32_e32 v158, v158
	s_nop 0
	v_mul_f32_e32 v203, v181, v158
	v_lshl_add_u64 v[146:147], v[146:147], 0, s[10:11]
	v_lshlrev_b64 v[146:147], 8, v[146:147]
	v_lshl_add_u64 v[146:147], v[196:197], 0, v[146:147]
	v_cvt_pk_bf16_f32 v220, v148, v149
	v_cvt_pk_bf16_f32 v221, v198, v199
	v_cvt_pk_bf16_f32 v222, v200, v201
	v_cvt_pk_bf16_f32 v223, v202, v203
	global_store_dwordx4 v[146:147], v[220:223], off
	s_nop 1
	v_cvt_f32_i32_e32 v147, v63
	v_cvt_f32_i32_e32 v146, v62
	v_pk_mul_f32 v[148:149], v[186:187], v[130:131] op_sel_hi:[0,1]
	v_pk_mul_f32 v[148:149], v[148:149], v[146:147]
	v_mul_f32_e32 v146, 0xbfb8aa3b, v148
	v_exp_f32_e32 v146, v146
	v_mul_f32_e32 v147, v219, v148
	v_add_f32_e32 v146, 1.0, v146
	v_rcp_f32_e32 v146, v146
	s_nop 0
	v_mul_f32_e32 v148, v147, v146
	v_cvt_f32_i32_e32 v147, v65
	v_cvt_f32_i32_e32 v146, v64
	v_mov_b32_e32 v187, v186
	v_pk_mul_f32 v[198:199], v[186:187], v[132:133] op_sel_hi:[0,1]
	v_pk_mul_f32 v[198:199], v[198:199], v[146:147]
	v_mul_f32_e32 v146, 0xbfb8aa3b, v149
	v_exp_f32_e32 v146, v146
	v_mul_f32_e32 v147, v219, v149
	v_add_f32_e32 v146, 1.0, v146
	v_rcp_f32_e32 v146, v146
	s_nop 0
	v_mul_f32_e32 v149, v147, v146
	v_mul_f32_e32 v146, 0xbfb8aa3b, v198
	v_exp_f32_e32 v146, v146
	v_mul_f32_e32 v147, v219, v198
	v_add_f32_e32 v146, 1.0, v146
	v_rcp_f32_e32 v146, v146
	s_nop 0
	v_mul_f32_e32 v198, v147, v146
	v_mul_f32_e32 v146, 0xbfb8aa3b, v199
	v_exp_f32_e32 v146, v146
	v_mul_f32_e32 v147, v219, v199
	v_add_f32_e32 v146, 1.0, v146
	v_rcp_f32_e32 v146, v146
	s_nop 0
	v_mul_f32_e32 v199, v147, v146
	v_cvt_f32_i32_e32 v147, v59
	v_cvt_f32_i32_e32 v146, v58
	v_pk_mul_f32 v[200:201], v[186:187], v[126:127]
	v_pk_mul_f32 v[200:201], v[200:201], v[146:147]
	v_mul_f32_e32 v146, 0xbfb8aa3b, v200
	v_exp_f32_e32 v146, v146
	v_mul_f32_e32 v147, v219, v200
	v_add_f32_e32 v146, 1.0, v146
	v_rcp_f32_e32 v146, v146
	s_nop 0
	v_mul_f32_e32 v200, v147, v146
	v_cvt_f32_i32_e32 v147, v61
	v_cvt_f32_i32_e32 v146, v60
	v_mov_b32_e32 v202, v186
	v_mov_b32_e32 v203, v186
	v_pk_mul_f32 v[202:203], v[202:203], v[128:129]
	v_pk_mul_f32 v[202:203], v[202:203], v[146:147]
	v_mul_f32_e32 v146, 0xbfb8aa3b, v201
	v_exp_f32_e32 v146, v146
	v_mul_f32_e32 v147, v219, v201
	v_add_f32_e32 v146, 1.0, v146
	v_rcp_f32_e32 v146, v146
	s_nop 0
	v_mul_f32_e32 v201, v147, v146
	v_mul_f32_e32 v146, 0xbfb8aa3b, v202
	v_exp_f32_e32 v146, v146
	v_mul_f32_e32 v147, v219, v202
	v_add_f32_e32 v146, 1.0, v146
	v_rcp_f32_e32 v146, v146
	s_nop 0
	v_mul_f32_e32 v202, v147, v146
	v_mul_f32_e32 v146, 0xbfb8aa3b, v203
	v_exp_f32_e32 v146, v146
	v_mul_f32_e32 v147, v219, v203
	v_add_f32_e32 v146, 1.0, v146
	v_rcp_f32_e32 v146, v146
	s_nop 0
	v_mul_f32_e32 v203, v147, v146
	v_lshl_add_u64 v[146:147], v[178:179], 0, s[34:35]
	v_cvt_pk_bf16_f32 v220, v148, v149
	v_lshl_add_u64 v[148:149], v[146:147], 0, s[16:17]
	v_lshlrev_b64 v[148:149], 8, v[148:149]
	v_lshl_add_u64 v[148:149], v[196:197], 0, v[148:149]
	v_cvt_pk_bf16_f32 v221, v198, v199
	v_cvt_pk_bf16_f32 v222, v200, v201
	v_cvt_pk_bf16_f32 v223, v202, v203
	global_store_dwordx4 v[148:149], v[220:223], off
	s_nop 1
	v_cvt_f32_i32_e32 v149, v55
	v_cvt_f32_i32_e32 v148, v54
	v_pk_mul_f32 v[198:199], v[186:187], v[110:111]
	v_pk_mul_f32 v[148:149], v[198:199], v[148:149]
	v_mul_f32_e32 v158, 0xbfb8aa3b, v148
	v_exp_f32_e32 v158, v158
	v_mul_f32_e32 v148, v219, v148
	v_add_f32_e32 v158, 1.0, v158
	v_rcp_f32_e32 v158, v158
	s_nop 0
	v_mul_f32_e32 v148, v148, v158
	v_cvt_f32_i32_e32 v199, v57
	v_cvt_f32_i32_e32 v198, v56
	v_mov_b32_e32 v200, v186
	v_mov_b32_e32 v201, v186
	v_pk_mul_f32 v[200:201], v[200:201], v[112:113]
	v_pk_mul_f32 v[198:199], v[200:201], v[198:199]
	v_mul_f32_e32 v158, 0xbfb8aa3b, v149
	v_exp_f32_e32 v158, v158
	v_mul_f32_e32 v149, v219, v149
	v_add_f32_e32 v158, 1.0, v158
	v_rcp_f32_e32 v158, v158
	s_nop 0
	v_mul_f32_e32 v149, v149, v158
	v_mul_f32_e32 v158, 0xbfb8aa3b, v198
	v_exp_f32_e32 v158, v158
	v_mul_f32_e32 v181, v219, v198
	v_add_f32_e32 v158, 1.0, v158
	v_rcp_f32_e32 v158, v158
	s_nop 0
	v_mul_f32_e32 v198, v181, v158
	v_mul_f32_e32 v158, 0xbfb8aa3b, v199
	v_exp_f32_e32 v158, v158
	v_mul_f32_e32 v181, v219, v199
	v_add_f32_e32 v158, 1.0, v158
	v_rcp_f32_e32 v158, v158
	s_nop 0
	v_mul_f32_e32 v199, v181, v158
	v_cvt_f32_i32_e32 v201, v51
	v_cvt_f32_i32_e32 v200, v50
	v_pk_mul_f32 v[202:203], v[186:187], v[106:107]
	v_pk_mul_f32 v[200:201], v[202:203], v[200:201]
	v_mul_f32_e32 v158, 0xbfb8aa3b, v200
	v_exp_f32_e32 v158, v158
	v_mul_f32_e32 v181, v219, v200
	v_add_f32_e32 v158, 1.0, v158
	v_rcp_f32_e32 v158, v158
	s_nop 0
	v_mul_f32_e32 v200, v181, v158
	v_cvt_f32_i32_e32 v203, v53
	v_cvt_f32_i32_e32 v202, v52
	v_mov_b32_e32 v187, v186
	v_pk_mul_f32 v[220:221], v[186:187], v[108:109]
	v_pk_mul_f32 v[202:203], v[220:221], v[202:203]
	v_mul_f32_e32 v158, 0xbfb8aa3b, v201
	v_exp_f32_e32 v158, v158
	v_mul_f32_e32 v181, v219, v201
	v_add_f32_e32 v158, 1.0, v158
	v_rcp_f32_e32 v158, v158
	s_nop 0
	v_mul_f32_e32 v201, v181, v158
	v_mul_f32_e32 v158, 0xbfb8aa3b, v202
	v_exp_f32_e32 v158, v158
	v_mul_f32_e32 v181, v219, v202
	v_add_f32_e32 v158, 1.0, v158
	v_rcp_f32_e32 v158, v158
	s_nop 0
	v_mul_f32_e32 v202, v181, v158
	v_mul_f32_e32 v158, 0xbfb8aa3b, v203
	v_exp_f32_e32 v158, v158
	v_mul_f32_e32 v181, v219, v203
	v_add_f32_e32 v158, 1.0, v158
	v_rcp_f32_e32 v158, v158
	s_nop 0
	v_mul_f32_e32 v203, v181, v158
	v_lshl_add_u64 v[146:147], v[146:147], 0, s[10:11]
	v_lshlrev_b64 v[146:147], 8, v[146:147]
	v_lshl_add_u64 v[146:147], v[196:197], 0, v[146:147]
	v_cvt_pk_bf16_f32 v220, v148, v149
	v_cvt_pk_bf16_f32 v221, v198, v199
	v_cvt_pk_bf16_f32 v222, v200, v201
	v_cvt_pk_bf16_f32 v223, v202, v203
	global_store_dwordx4 v[146:147], v[220:223], off
	s_nop 1
	v_cvt_f32_i32_e32 v147, v47
	v_cvt_f32_i32_e32 v146, v46
	v_pk_mul_f32 v[148:149], v[184:185], v[130:131] op_sel_hi:[0,1]
	v_pk_mul_f32 v[148:149], v[148:149], v[146:147]
	v_mul_f32_e32 v146, 0xbfb8aa3b, v148
	v_exp_f32_e32 v146, v146
	v_mul_f32_e32 v147, v219, v148
	v_add_f32_e32 v146, 1.0, v146
	v_rcp_f32_e32 v146, v146
	s_nop 0
	v_mul_f32_e32 v148, v147, v146
	v_cvt_f32_i32_e32 v147, v49
	v_cvt_f32_i32_e32 v146, v48
	v_mov_b32_e32 v185, v184
	v_pk_mul_f32 v[198:199], v[184:185], v[132:133] op_sel_hi:[0,1]
	v_pk_mul_f32 v[198:199], v[198:199], v[146:147]
	v_mul_f32_e32 v146, 0xbfb8aa3b, v149
	v_exp_f32_e32 v146, v146
	v_mul_f32_e32 v147, v219, v149
	v_add_f32_e32 v146, 1.0, v146
	v_rcp_f32_e32 v146, v146
	s_nop 0
	v_mul_f32_e32 v149, v147, v146
	v_mul_f32_e32 v146, 0xbfb8aa3b, v198
	v_exp_f32_e32 v146, v146
	v_mul_f32_e32 v147, v219, v198
	v_add_f32_e32 v146, 1.0, v146
	v_rcp_f32_e32 v146, v146
	s_nop 0
	v_mul_f32_e32 v198, v147, v146
	v_mul_f32_e32 v146, 0xbfb8aa3b, v199
	v_exp_f32_e32 v146, v146
	v_mul_f32_e32 v147, v219, v199
	v_add_f32_e32 v146, 1.0, v146
	v_rcp_f32_e32 v146, v146
	s_nop 0
	v_mul_f32_e32 v199, v147, v146
	v_cvt_f32_i32_e32 v147, v43
	v_cvt_f32_i32_e32 v146, v42
	v_pk_mul_f32 v[200:201], v[184:185], v[126:127]
	v_pk_mul_f32 v[200:201], v[200:201], v[146:147]
	v_mul_f32_e32 v146, 0xbfb8aa3b, v200
	v_exp_f32_e32 v146, v146
	v_mul_f32_e32 v147, v219, v200
	v_add_f32_e32 v146, 1.0, v146
	v_rcp_f32_e32 v146, v146
	s_nop 0
	v_mul_f32_e32 v200, v147, v146
	v_cvt_f32_i32_e32 v147, v45
	v_cvt_f32_i32_e32 v146, v44
	v_mov_b32_e32 v202, v184
	v_mov_b32_e32 v203, v184
	v_pk_mul_f32 v[202:203], v[202:203], v[128:129]
	v_pk_mul_f32 v[202:203], v[202:203], v[146:147]
	v_mul_f32_e32 v146, 0xbfb8aa3b, v201
	v_exp_f32_e32 v146, v146
	v_mul_f32_e32 v147, v219, v201
	v_add_f32_e32 v146, 1.0, v146
	v_rcp_f32_e32 v146, v146
	s_nop 0
	v_mul_f32_e32 v201, v147, v146
	v_mul_f32_e32 v146, 0xbfb8aa3b, v202
	v_exp_f32_e32 v146, v146
	v_mul_f32_e32 v147, v219, v202
	v_add_f32_e32 v146, 1.0, v146
	v_rcp_f32_e32 v146, v146
	s_nop 0
	v_mul_f32_e32 v202, v147, v146
	v_mul_f32_e32 v146, 0xbfb8aa3b, v203
	v_exp_f32_e32 v146, v146
	v_mul_f32_e32 v147, v219, v203
	v_add_f32_e32 v146, 1.0, v146
	v_rcp_f32_e32 v146, v146
	s_nop 0
	v_mul_f32_e32 v203, v147, v146
	v_lshl_add_u64 v[146:147], v[178:179], 0, s[42:43]
	v_cvt_pk_bf16_f32 v220, v148, v149
	v_lshl_add_u64 v[148:149], v[146:147], 0, s[16:17]
	v_lshlrev_b64 v[148:149], 8, v[148:149]
	v_lshl_add_u64 v[148:149], v[196:197], 0, v[148:149]
	v_cvt_pk_bf16_f32 v221, v198, v199
	v_cvt_pk_bf16_f32 v222, v200, v201
	v_cvt_pk_bf16_f32 v223, v202, v203
	global_store_dwordx4 v[148:149], v[220:223], off
	s_nop 1
	v_cvt_f32_i32_e32 v149, v39
	v_cvt_f32_i32_e32 v148, v38
	v_pk_mul_f32 v[198:199], v[184:185], v[110:111]
	v_pk_mul_f32 v[148:149], v[198:199], v[148:149]
	v_mul_f32_e32 v158, 0xbfb8aa3b, v148
	v_exp_f32_e32 v158, v158
	v_mul_f32_e32 v148, v219, v148
	v_add_f32_e32 v158, 1.0, v158
	v_rcp_f32_e32 v158, v158
	s_nop 0
	v_mul_f32_e32 v148, v148, v158
	v_cvt_f32_i32_e32 v199, v41
	v_cvt_f32_i32_e32 v198, v40
	v_mov_b32_e32 v200, v184
	v_mov_b32_e32 v201, v184
	v_pk_mul_f32 v[200:201], v[200:201], v[112:113]
	v_pk_mul_f32 v[198:199], v[200:201], v[198:199]
	v_mul_f32_e32 v158, 0xbfb8aa3b, v149
	v_exp_f32_e32 v158, v158
	v_mul_f32_e32 v149, v219, v149
	v_add_f32_e32 v158, 1.0, v158
	v_rcp_f32_e32 v158, v158
	s_nop 0
	v_mul_f32_e32 v149, v149, v158
	v_mul_f32_e32 v158, 0xbfb8aa3b, v198
	v_exp_f32_e32 v158, v158
	v_mul_f32_e32 v181, v219, v198
	v_add_f32_e32 v158, 1.0, v158
	v_rcp_f32_e32 v158, v158
	s_nop 0
	v_mul_f32_e32 v198, v181, v158
	v_mul_f32_e32 v158, 0xbfb8aa3b, v199
	v_exp_f32_e32 v158, v158
	v_mul_f32_e32 v181, v219, v199
	v_add_f32_e32 v158, 1.0, v158
	v_rcp_f32_e32 v158, v158
	s_nop 0
	v_mul_f32_e32 v199, v181, v158
	v_cvt_f32_i32_e32 v201, v35
	v_cvt_f32_i32_e32 v200, v34
	v_pk_mul_f32 v[202:203], v[184:185], v[106:107]
	v_pk_mul_f32 v[200:201], v[202:203], v[200:201]
	v_mul_f32_e32 v158, 0xbfb8aa3b, v200
	v_exp_f32_e32 v158, v158
	v_mul_f32_e32 v181, v219, v200
	v_add_f32_e32 v158, 1.0, v158
	v_rcp_f32_e32 v158, v158
	s_nop 0
	v_mul_f32_e32 v200, v181, v158
	v_cvt_f32_i32_e32 v203, v37
	v_cvt_f32_i32_e32 v202, v36
	v_mov_b32_e32 v185, v184
	v_pk_mul_f32 v[220:221], v[184:185], v[108:109]
	v_pk_mul_f32 v[202:203], v[220:221], v[202:203]
	v_mul_f32_e32 v158, 0xbfb8aa3b, v201
	v_exp_f32_e32 v158, v158
	v_mul_f32_e32 v181, v219, v201
	v_add_f32_e32 v158, 1.0, v158
	v_rcp_f32_e32 v158, v158
	s_nop 0
	v_mul_f32_e32 v201, v181, v158
	v_mul_f32_e32 v158, 0xbfb8aa3b, v202
	v_exp_f32_e32 v158, v158
	v_mul_f32_e32 v181, v219, v202
	v_add_f32_e32 v158, 1.0, v158
	v_rcp_f32_e32 v158, v158
	s_nop 0
	v_mul_f32_e32 v202, v181, v158
	v_mul_f32_e32 v158, 0xbfb8aa3b, v203
	v_exp_f32_e32 v158, v158
	v_mul_f32_e32 v181, v219, v203
	v_add_f32_e32 v158, 1.0, v158
	v_rcp_f32_e32 v158, v158
	s_nop 0
	v_mul_f32_e32 v203, v181, v158
	v_lshl_add_u64 v[146:147], v[146:147], 0, s[10:11]
	v_lshlrev_b64 v[146:147], 8, v[146:147]
	v_lshl_add_u64 v[146:147], v[196:197], 0, v[146:147]
	v_cvt_pk_bf16_f32 v220, v148, v149
	v_cvt_pk_bf16_f32 v221, v198, v199
	v_cvt_pk_bf16_f32 v222, v200, v201
	v_cvt_pk_bf16_f32 v223, v202, v203
	global_store_dwordx4 v[146:147], v[220:223], off
	s_nop 1
	v_cvt_f32_i32_e32 v147, v31
	v_cvt_f32_i32_e32 v146, v30
	v_pk_mul_f32 v[148:149], v[182:183], v[130:131] op_sel_hi:[0,1]
	v_pk_mul_f32 v[148:149], v[148:149], v[146:147]
	v_mul_f32_e32 v146, 0xbfb8aa3b, v148
	v_exp_f32_e32 v146, v146
	v_mul_f32_e32 v147, v219, v148
	v_add_f32_e32 v146, 1.0, v146
	v_rcp_f32_e32 v146, v146
	s_nop 0
	v_mul_f32_e32 v148, v147, v146
	v_cvt_f32_i32_e32 v147, v33
	v_cvt_f32_i32_e32 v146, v32
	v_mov_b32_e32 v183, v182
	v_pk_mul_f32 v[198:199], v[182:183], v[132:133] op_sel_hi:[0,1]
	v_pk_mul_f32 v[198:199], v[198:199], v[146:147]
	v_mul_f32_e32 v146, 0xbfb8aa3b, v149
	v_exp_f32_e32 v146, v146
	v_mul_f32_e32 v147, v219, v149
	v_add_f32_e32 v146, 1.0, v146
	v_rcp_f32_e32 v146, v146
	s_nop 0
	v_mul_f32_e32 v149, v147, v146
	v_mul_f32_e32 v146, 0xbfb8aa3b, v198
	v_exp_f32_e32 v146, v146
	v_mul_f32_e32 v147, v219, v198
	v_add_f32_e32 v146, 1.0, v146
	v_rcp_f32_e32 v146, v146
	s_nop 0
	v_mul_f32_e32 v198, v147, v146
	v_mul_f32_e32 v146, 0xbfb8aa3b, v199
	v_exp_f32_e32 v146, v146
	v_mul_f32_e32 v147, v219, v199
	v_add_f32_e32 v146, 1.0, v146
	v_rcp_f32_e32 v146, v146
	s_nop 0
	v_mul_f32_e32 v199, v147, v146
	v_cvt_f32_i32_e32 v147, v27
	v_cvt_f32_i32_e32 v146, v26
	v_pk_mul_f32 v[200:201], v[182:183], v[126:127]
	v_pk_mul_f32 v[200:201], v[200:201], v[146:147]
	v_mul_f32_e32 v146, 0xbfb8aa3b, v200
	v_exp_f32_e32 v146, v146
	v_mul_f32_e32 v147, v219, v200
	v_add_f32_e32 v146, 1.0, v146
	v_rcp_f32_e32 v146, v146
	s_nop 0
	v_mul_f32_e32 v200, v147, v146
	v_cvt_f32_i32_e32 v147, v29
	v_cvt_f32_i32_e32 v146, v28
	v_mov_b32_e32 v202, v182
	v_mov_b32_e32 v203, v182
	v_pk_mul_f32 v[202:203], v[202:203], v[128:129]
	v_pk_mul_f32 v[202:203], v[202:203], v[146:147]
	v_mul_f32_e32 v146, 0xbfb8aa3b, v201
	v_exp_f32_e32 v146, v146
	v_mul_f32_e32 v147, v219, v201
	v_add_f32_e32 v146, 1.0, v146
	v_rcp_f32_e32 v146, v146
	s_nop 0
	v_mul_f32_e32 v201, v147, v146
	v_mul_f32_e32 v146, 0xbfb8aa3b, v202
	v_exp_f32_e32 v146, v146
	v_mul_f32_e32 v147, v219, v202
	v_add_f32_e32 v146, 1.0, v146
	v_rcp_f32_e32 v146, v146
	s_nop 0
	v_mul_f32_e32 v202, v147, v146
	v_mul_f32_e32 v146, 0xbfb8aa3b, v203
	v_exp_f32_e32 v146, v146
	v_mul_f32_e32 v147, v219, v203
	v_add_f32_e32 v146, 1.0, v146
	v_rcp_f32_e32 v146, v146
	s_nop 0
	v_mul_f32_e32 v203, v147, v146
	v_lshl_add_u64 v[146:147], v[178:179], 0, s[52:53]
	v_cvt_pk_bf16_f32 v220, v148, v149
	v_lshl_add_u64 v[148:149], v[146:147], 0, s[16:17]
	v_lshlrev_b64 v[148:149], 8, v[148:149]
	v_lshl_add_u64 v[148:149], v[196:197], 0, v[148:149]
	v_cvt_pk_bf16_f32 v221, v198, v199
	v_cvt_pk_bf16_f32 v222, v200, v201
	v_cvt_pk_bf16_f32 v223, v202, v203
	global_store_dwordx4 v[148:149], v[220:223], off
	s_nop 1
	v_cvt_f32_i32_e32 v149, v23
	v_cvt_f32_i32_e32 v148, v22
	v_pk_mul_f32 v[198:199], v[182:183], v[110:111]
	v_pk_mul_f32 v[148:149], v[198:199], v[148:149]
	v_mul_f32_e32 v158, 0xbfb8aa3b, v148
	v_exp_f32_e32 v158, v158
	v_mul_f32_e32 v148, v219, v148
	v_add_f32_e32 v158, 1.0, v158
	v_rcp_f32_e32 v158, v158
	s_nop 0
	v_mul_f32_e32 v148, v148, v158
	v_cvt_f32_i32_e32 v199, v25
	v_cvt_f32_i32_e32 v198, v24
	v_mov_b32_e32 v200, v182
	v_mov_b32_e32 v201, v182
	v_pk_mul_f32 v[200:201], v[200:201], v[112:113]
	v_pk_mul_f32 v[198:199], v[200:201], v[198:199]
	v_mul_f32_e32 v158, 0xbfb8aa3b, v149
	v_exp_f32_e32 v158, v158
	v_mul_f32_e32 v149, v219, v149
	v_add_f32_e32 v158, 1.0, v158
	v_rcp_f32_e32 v158, v158
	s_nop 0
	v_mul_f32_e32 v149, v149, v158
	v_mul_f32_e32 v158, 0xbfb8aa3b, v198
	v_exp_f32_e32 v158, v158
	v_mul_f32_e32 v181, v219, v198
	v_add_f32_e32 v158, 1.0, v158
	v_rcp_f32_e32 v158, v158
	s_nop 0
	v_mul_f32_e32 v198, v181, v158
	v_mul_f32_e32 v158, 0xbfb8aa3b, v199
	v_exp_f32_e32 v158, v158
	v_mul_f32_e32 v181, v219, v199
	v_add_f32_e32 v158, 1.0, v158
	v_rcp_f32_e32 v158, v158
	s_nop 0
	v_mul_f32_e32 v199, v181, v158
	v_cvt_f32_i32_e32 v201, v19
	v_cvt_f32_i32_e32 v200, v18
	v_pk_mul_f32 v[202:203], v[182:183], v[106:107]
	v_pk_mul_f32 v[200:201], v[202:203], v[200:201]
	v_mul_f32_e32 v158, 0xbfb8aa3b, v200
	v_exp_f32_e32 v158, v158
	v_mul_f32_e32 v181, v219, v200
	v_add_f32_e32 v158, 1.0, v158
	v_rcp_f32_e32 v158, v158
	s_nop 0
	v_mul_f32_e32 v200, v181, v158
	v_cvt_f32_i32_e32 v203, v21
	v_cvt_f32_i32_e32 v202, v20
	v_mov_b32_e32 v183, v182
	v_pk_mul_f32 v[220:221], v[182:183], v[108:109]
	v_pk_mul_f32 v[202:203], v[220:221], v[202:203]
	v_mul_f32_e32 v158, 0xbfb8aa3b, v201
	v_exp_f32_e32 v158, v158
	v_mul_f32_e32 v181, v219, v201
	v_add_f32_e32 v158, 1.0, v158
	v_rcp_f32_e32 v158, v158
	s_nop 0
	v_mul_f32_e32 v201, v181, v158
	v_mul_f32_e32 v158, 0xbfb8aa3b, v202
	v_exp_f32_e32 v158, v158
	v_mul_f32_e32 v181, v219, v202
	v_add_f32_e32 v158, 1.0, v158
	v_rcp_f32_e32 v158, v158
	s_nop 0
	v_mul_f32_e32 v202, v181, v158
	v_mul_f32_e32 v158, 0xbfb8aa3b, v203
	v_exp_f32_e32 v158, v158
	v_mul_f32_e32 v181, v219, v203
	v_add_f32_e32 v158, 1.0, v158
	v_rcp_f32_e32 v158, v158
	s_nop 0
	v_mul_f32_e32 v203, v181, v158
	v_lshl_add_u64 v[146:147], v[146:147], 0, s[10:11]
	v_lshlrev_b64 v[146:147], 8, v[146:147]
	v_lshl_add_u64 v[146:147], v[196:197], 0, v[146:147]
	v_cvt_pk_bf16_f32 v220, v148, v149
	v_cvt_pk_bf16_f32 v221, v198, v199
	v_cvt_pk_bf16_f32 v222, v200, v201
	v_cvt_pk_bf16_f32 v223, v202, v203
	global_store_dwordx4 v[146:147], v[220:223], off
	s_nop 1
	v_cvt_f32_i32_e32 v147, v15
	v_cvt_f32_i32_e32 v146, v14
	v_pk_mul_f32 v[148:149], v[130:131], v[180:181] op_sel_hi:[1,0]
	v_pk_mul_f32 v[146:147], v[148:149], v[146:147]
	v_mul_f32_e32 v148, 0xbfb8aa3b, v146
	v_exp_f32_e32 v148, v148
	v_mul_f32_e32 v146, v219, v146
	v_add_f32_e32 v148, 1.0, v148
	v_rcp_f32_e32 v148, v148
	s_nop 0
	v_mul_f32_e32 v146, v146, v148
	v_cvt_f32_i32_e32 v149, v17
	v_cvt_f32_i32_e32 v148, v16
	v_mov_b32_e32 v181, v180
	v_pk_mul_f32 v[198:199], v[132:133], v[180:181] op_sel_hi:[1,0]
	v_pk_mul_f32 v[148:149], v[198:199], v[148:149]
	v_mul_f32_e32 v158, 0xbfb8aa3b, v147
	v_exp_f32_e32 v158, v158
	v_mul_f32_e32 v147, v219, v147
	v_add_f32_e32 v158, 1.0, v158
	v_rcp_f32_e32 v158, v158
	s_nop 0
	v_mul_f32_e32 v147, v147, v158
	v_mul_f32_e32 v158, 0xbfb8aa3b, v148
	v_exp_f32_e32 v158, v158
	v_mul_f32_e32 v148, v219, v148
	v_add_f32_e32 v158, 1.0, v158
	v_rcp_f32_e32 v158, v158
	s_nop 0
	v_mul_f32_e32 v148, v148, v158
	v_mul_f32_e32 v158, 0xbfb8aa3b, v149
	v_exp_f32_e32 v158, v158
	v_mul_f32_e32 v149, v219, v149
	v_add_f32_e32 v158, 1.0, v158
	v_rcp_f32_e32 v158, v158
	s_nop 0
	v_mul_f32_e32 v149, v149, v158
	v_cvt_f32_i32_e32 v199, v11
	v_cvt_f32_i32_e32 v198, v10
	v_pk_mul_f32 v[200:201], v[180:181], v[126:127]
	v_pk_mul_f32 v[200:201], v[200:201], v[198:199]
	v_mul_f32_e32 v158, 0xbfb8aa3b, v200
	v_exp_f32_e32 v158, v158
	v_mul_f32_e32 v183, v219, v200
	v_add_f32_e32 v158, 1.0, v158
	v_rcp_f32_e32 v158, v158
	s_nop 0
	v_mul_f32_e32 v200, v183, v158
	v_cvt_f32_i32_e32 v199, v13
	v_cvt_f32_i32_e32 v198, v12
	v_mov_b32_e32 v202, v180
	v_mov_b32_e32 v203, v180
	v_pk_mul_f32 v[202:203], v[202:203], v[128:129]
	v_pk_mul_f32 v[202:203], v[202:203], v[198:199]
	v_mul_f32_e32 v158, 0xbfb8aa3b, v201
	v_exp_f32_e32 v158, v158
	v_mul_f32_e32 v183, v219, v201
	v_add_f32_e32 v158, 1.0, v158
	v_rcp_f32_e32 v158, v158
	s_nop 0
	v_mul_f32_e32 v201, v183, v158
	v_mul_f32_e32 v158, 0xbfb8aa3b, v202
	v_exp_f32_e32 v158, v158
	v_mul_f32_e32 v183, v219, v202
	v_add_f32_e32 v158, 1.0, v158
	v_rcp_f32_e32 v158, v158
	s_nop 0
	v_mul_f32_e32 v202, v183, v158
	v_mul_f32_e32 v158, 0xbfb8aa3b, v203
	v_exp_f32_e32 v158, v158
	v_mul_f32_e32 v183, v219, v203
	v_add_f32_e32 v158, 1.0, v158
	v_rcp_f32_e32 v158, v158
	s_nop 0
	v_mul_f32_e32 v203, v183, v158
	v_lshl_add_u64 v[198:199], v[178:179], 0, s[54:55]
	v_cvt_pk_bf16_f32 v146, v146, v147
	v_cvt_pk_bf16_f32 v147, v148, v149
	v_cvt_pk_bf16_f32 v148, v200, v201
	v_lshl_add_u64 v[200:201], v[198:199], 0, s[16:17]
	v_lshlrev_b64 v[200:201], 8, v[200:201]
	v_lshl_add_u64 v[200:201], v[196:197], 0, v[200:201]
	v_cvt_pk_bf16_f32 v149, v202, v203
	global_store_dwordx4 v[200:201], v[146:149], off
	s_nop 1
	v_cvt_f32_i32_e32 v147, v7
	v_cvt_f32_i32_e32 v146, v6
	v_pk_mul_f32 v[148:149], v[180:181], v[110:111]
	v_pk_mul_f32 v[146:147], v[148:149], v[146:147]
	v_mul_f32_e32 v148, 0xbfb8aa3b, v146
	v_exp_f32_e32 v148, v148
	v_mul_f32_e32 v146, v219, v146
	v_add_f32_e32 v148, 1.0, v148
	v_rcp_f32_e32 v148, v148
	s_nop 0
	v_mul_f32_e32 v146, v146, v148
	v_cvt_f32_i32_e32 v149, v9
	v_cvt_f32_i32_e32 v148, v8
	v_mov_b32_e32 v200, v180
	v_mov_b32_e32 v201, v180
	v_pk_mul_f32 v[200:201], v[200:201], v[112:113]
	v_pk_mul_f32 v[148:149], v[200:201], v[148:149]
	v_mul_f32_e32 v158, 0xbfb8aa3b, v147
	v_exp_f32_e32 v158, v158
	v_mul_f32_e32 v147, v219, v147
	v_add_f32_e32 v158, 1.0, v158
	v_rcp_f32_e32 v158, v158
	s_nop 0
	v_mul_f32_e32 v147, v147, v158
	v_mul_f32_e32 v158, 0xbfb8aa3b, v148
	v_exp_f32_e32 v158, v158
	v_mul_f32_e32 v148, v219, v148
	v_add_f32_e32 v158, 1.0, v158
	v_rcp_f32_e32 v158, v158
	s_nop 0
	v_mul_f32_e32 v148, v148, v158
	v_mul_f32_e32 v158, 0xbfb8aa3b, v149
	v_exp_f32_e32 v158, v158
	v_mul_f32_e32 v149, v219, v149
	v_add_f32_e32 v158, 1.0, v158
	v_rcp_f32_e32 v158, v158
	s_nop 0
	v_mul_f32_e32 v149, v149, v158
	v_cvt_f32_i32_e32 v201, v3
	v_cvt_f32_i32_e32 v200, v2
	v_pk_mul_f32 v[202:203], v[180:181], v[106:107]
	v_pk_mul_f32 v[200:201], v[202:203], v[200:201]
	v_mul_f32_e32 v158, 0xbfb8aa3b, v200
	v_exp_f32_e32 v158, v158
	v_mul_f32_e32 v181, v219, v200
	v_add_f32_e32 v158, 1.0, v158
	v_rcp_f32_e32 v158, v158
	s_nop 0
	v_mul_f32_e32 v200, v181, v158
	v_cvt_f32_i32_e32 v203, v5
	v_cvt_f32_i32_e32 v202, v4
	v_mov_b32_e32 v181, v180
	v_pk_mul_f32 v[220:221], v[180:181], v[108:109]
	v_pk_mul_f32 v[202:203], v[220:221], v[202:203]
	v_mul_f32_e32 v158, 0xbfb8aa3b, v201
	v_exp_f32_e32 v158, v158
	v_mul_f32_e32 v181, v219, v201
	v_add_f32_e32 v158, 1.0, v158
	v_rcp_f32_e32 v158, v158
	s_nop 0
	v_mul_f32_e32 v201, v181, v158
	v_mul_f32_e32 v158, 0xbfb8aa3b, v202
	v_exp_f32_e32 v158, v158
	v_mul_f32_e32 v181, v219, v202
	v_add_f32_e32 v158, 1.0, v158
	v_rcp_f32_e32 v158, v158
	s_nop 0
	v_mul_f32_e32 v202, v181, v158
	v_mul_f32_e32 v158, 0xbfb8aa3b, v203
	v_exp_f32_e32 v158, v158
	v_mul_f32_e32 v181, v219, v203
	v_add_f32_e32 v158, 1.0, v158
	v_rcp_f32_e32 v158, v158
	s_nop 0
	v_mul_f32_e32 v203, v181, v158
	v_cvt_pk_bf16_f32 v146, v146, v147
	v_cvt_pk_bf16_f32 v147, v148, v149
	v_cvt_pk_bf16_f32 v148, v200, v201
	v_cvt_pk_bf16_f32 v149, v202, v203
	v_lshl_add_u64 v[198:199], v[198:199], 0, s[10:11]
	s_branch .LBB0_354
.Lepi_t5:
	s_mov_b64 s[68:69], s[24:25]
	v_mov_b64_e32 v[196:197], v[166:167]
	s_cmp_eq_u32 s59, 3
	s_cselect_b64 s[10:11], -1, 0
	v_cvt_f32_i32_e32 v147, v143
	v_cvt_f32_i32_e32 v146, v142
	s_waitcnt vmcnt(0)
	v_pk_mul_f32 v[148:149], v[194:195], v[130:131] op_sel_hi:[0,1]
	v_cndmask_b32_e64 v219, 1.0, v217, s[10:11]
	v_pk_mul_f32 v[146:147], v[148:149], v[146:147]
	v_cvt_f32_i32_e32 v149, v145
	v_cvt_f32_i32_e32 v148, v144
	v_mov_b32_e32 v195, v194
	v_pk_mul_f32 v[196:197], v[194:195], v[132:133] op_sel_hi:[0,1]
	v_pk_mul_f32 v[148:149], v[196:197], v[148:149]
	v_cvt_f32_i32_e32 v197, v139
	v_cvt_f32_i32_e32 v196, v138
	v_pk_mul_f32 v[198:199], v[194:195], v[126:127]
	v_pk_mul_f32 v[198:199], v[198:199], v[196:197]
	v_cvt_f32_i32_e32 v197, v141
	v_cvt_f32_i32_e32 v196, v140
	v_mov_b32_e32 v200, v194
	v_mov_b32_e32 v201, v194
	v_pk_mul_f32 v[200:201], v[200:201], v[128:129]
	v_pk_mul_f32 v[200:201], v[200:201], v[196:197]
	s_lshl_b32 s16, s57, 13
	v_lshlrev_b32_e32 v158, 1, v162
	v_cvt_pk_bf16_f32 v146, v146, v147
	v_cvt_pk_bf16_f32 v147, v148, v149
	v_cvt_pk_bf16_f32 v148, v198, v199
	v_lshl_add_u64 v[198:199], v[178:179], 0, s[16:17]
	v_lshl_add_u64 v[196:197], s[68:69], 0, v[158:159]
	v_lshlrev_b64 v[198:199], 8, v[198:199]
	v_lshl_add_u64 v[198:199], v[196:197], 0, v[198:199]
	v_cvt_pk_bf16_f32 v149, v200, v201
	global_store_dwordx4 v[198:199], v[146:149], off
	s_nop 1
	v_cvt_f32_i32_e32 v147, v135
	v_cvt_f32_i32_e32 v146, v134
	v_pk_mul_f32 v[148:149], v[194:195], v[110:111]
	v_pk_mul_f32 v[146:147], v[148:149], v[146:147]
	v_cvt_f32_i32_e32 v149, v137
	v_cvt_f32_i32_e32 v148, v136
	v_mov_b32_e32 v198, v194
	v_mov_b32_e32 v199, v194
	v_pk_mul_f32 v[198:199], v[198:199], v[112:113]
	v_pk_mul_f32 v[148:149], v[198:199], v[148:149]
	v_cvt_f32_i32_e32 v199, v123
	v_cvt_f32_i32_e32 v198, v122
	v_pk_mul_f32 v[200:201], v[194:195], v[106:107]
	v_pk_mul_f32 v[198:199], v[200:201], v[198:199]
	v_cvt_f32_i32_e32 v201, v125
	v_cvt_f32_i32_e32 v200, v124
	v_mov_b32_e32 v195, v194
	v_pk_mul_f32 v[202:203], v[194:195], v[108:109]
	v_pk_mul_f32 v[200:201], v[202:203], v[200:201]
	s_or_b32 s10, s16, 0x2000
	s_mov_b32 s11, s17
	v_cvt_pk_bf16_f32 v146, v146, v147
	v_cvt_pk_bf16_f32 v147, v148, v149
	v_cvt_pk_bf16_f32 v148, v198, v199
	v_lshl_add_u64 v[198:199], v[178:179], 0, s[10:11]
	v_lshlrev_b64 v[198:199], 8, v[198:199]
	v_lshl_add_u64 v[198:199], v[196:197], 0, v[198:199]
	v_cvt_pk_bf16_f32 v149, v200, v201
	global_store_dwordx4 v[198:199], v[146:149], off
	s_nop 1
	v_cvt_f32_i32_e32 v147, v119
	v_cvt_f32_i32_e32 v146, v118
	v_pk_mul_f32 v[148:149], v[192:193], v[130:131] op_sel_hi:[0,1]
	v_pk_mul_f32 v[148:149], v[148:149], v[146:147]
	v_cvt_f32_i32_e32 v147, v121
	v_cvt_f32_i32_e32 v146, v120
	v_mov_b32_e32 v193, v192
	v_pk_mul_f32 v[198:199], v[192:193], v[132:133] op_sel_hi:[0,1]
	v_pk_mul_f32 v[198:199], v[198:199], v[146:147]
	v_cvt_f32_i32_e32 v147, v115
	v_cvt_f32_i32_e32 v146, v114
	v_pk_mul_f32 v[200:201], v[192:193], v[126:127]
	v_pk_mul_f32 v[200:201], v[200:201], v[146:147]
	v_cvt_f32_i32_e32 v147, v117
	v_cvt_f32_i32_e32 v146, v116
	v_mov_b32_e32 v202, v192
	v_mov_b32_e32 v203, v192
	v_pk_mul_f32 v[202:203], v[202:203], v[128:129]
	v_pk_mul_f32 v[202:203], v[202:203], v[146:147]
	v_or_b32_e32 v146, 16, v178
	v_mov_b32_e32 v147, v179
	v_cvt_pk_bf16_f32 v220, v148, v149
	v_lshl_add_u64 v[148:149], v[146:147], 0, s[16:17]
	v_lshlrev_b64 v[148:149], 8, v[148:149]
	v_lshl_add_u64 v[148:149], v[196:197], 0, v[148:149]
	v_cvt_pk_bf16_f32 v221, v198, v199
	v_cvt_pk_bf16_f32 v222, v200, v201
	v_cvt_pk_bf16_f32 v223, v202, v203
	global_store_dwordx4 v[148:149], v[220:223], off
	s_nop 1
	v_cvt_f32_i32_e32 v149, v103
	v_cvt_f32_i32_e32 v148, v102
	v_pk_mul_f32 v[198:199], v[192:193], v[110:111]
	v_pk_mul_f32 v[148:149], v[198:199], v[148:149]
	v_cvt_f32_i32_e32 v199, v105
	v_cvt_f32_i32_e32 v198, v104
	v_mov_b32_e32 v200, v192
	v_mov_b32_e32 v201, v192
	v_pk_mul_f32 v[200:201], v[200:201], v[112:113]
	v_pk_mul_f32 v[198:199], v[200:201], v[198:199]
	v_cvt_f32_i32_e32 v201, v99
	v_cvt_f32_i32_e32 v200, v98
	v_pk_mul_f32 v[202:203], v[192:193], v[106:107]
	v_pk_mul_f32 v[200:201], v[202:203], v[200:201]
	v_cvt_f32_i32_e32 v203, v101
	v_cvt_f32_i32_e32 v202, v100
	v_mov_b32_e32 v193, v192
	v_pk_mul_f32 v[220:221], v[192:193], v[108:109]
	v_pk_mul_f32 v[202:203], v[220:221], v[202:203]
	v_lshl_add_u64 v[146:147], v[146:147], 0, s[10:11]
	v_lshlrev_b64 v[146:147], 8, v[146:147]
	v_lshl_add_u64 v[146:147], v[196:197], 0, v[146:147]
	v_cvt_pk_bf16_f32 v220, v148, v149
	v_cvt_pk_bf16_f32 v221, v198, v199
	v_cvt_pk_bf16_f32 v222, v200, v201
	v_cvt_pk_bf16_f32 v223, v202, v203
	global_store_dwordx4 v[146:147], v[220:223], off
	s_nop 1
	v_cvt_f32_i32_e32 v147, v95
	v_cvt_f32_i32_e32 v146, v94
	v_pk_mul_f32 v[148:149], v[190:191], v[130:131] op_sel_hi:[0,1]
	v_pk_mul_f32 v[148:149], v[148:149], v[146:147]
	v_cvt_f32_i32_e32 v147, v97
	v_cvt_f32_i32_e32 v146, v96
	v_mov_b32_e32 v191, v190
	v_pk_mul_f32 v[198:199], v[190:191], v[132:133] op_sel_hi:[0,1]
	v_pk_mul_f32 v[198:199], v[198:199], v[146:147]
	v_cvt_f32_i32_e32 v147, v91
	v_cvt_f32_i32_e32 v146, v90
	v_pk_mul_f32 v[200:201], v[190:191], v[126:127]
	v_pk_mul_f32 v[200:201], v[200:201], v[146:147]
	v_cvt_f32_i32_e32 v147, v93
	v_cvt_f32_i32_e32 v146, v92
	v_mov_b32_e32 v202, v190
	v_mov_b32_e32 v203, v190
	v_pk_mul_f32 v[202:203], v[202:203], v[128:129]
	v_pk_mul_f32 v[202:203], v[202:203], v[146:147]
	v_or_b32_e32 v146, 32, v178
	v_mov_b32_e32 v147, v179
	v_cvt_pk_bf16_f32 v220, v148, v149
	v_lshl_add_u64 v[148:149], v[146:147], 0, s[16:17]
	v_lshlrev_b64 v[148:149], 8, v[148:149]
	v_lshl_add_u64 v[148:149], v[196:197], 0, v[148:149]
	v_cvt_pk_bf16_f32 v221, v198, v199
	v_cvt_pk_bf16_f32 v222, v200, v201
	v_cvt_pk_bf16_f32 v223, v202, v203
	global_store_dwordx4 v[148:149], v[220:223], off
	s_nop 1
	v_cvt_f32_i32_e32 v149, v87
	v_cvt_f32_i32_e32 v148, v86
	v_pk_mul_f32 v[198:199], v[190:191], v[110:111]
	v_pk_mul_f32 v[148:149], v[198:199], v[148:149]
	v_cvt_f32_i32_e32 v199, v89
	v_cvt_f32_i32_e32 v198, v88
	v_mov_b32_e32 v200, v190
	v_mov_b32_e32 v201, v190
	v_pk_mul_f32 v[200:201], v[200:201], v[112:113]
	v_pk_mul_f32 v[198:199], v[200:201], v[198:199]
	v_cvt_f32_i32_e32 v201, v83
	v_cvt_f32_i32_e32 v200, v82
	v_pk_mul_f32 v[202:203], v[190:191], v[106:107]
	v_pk_mul_f32 v[200:201], v[202:203], v[200:201]
	v_cvt_f32_i32_e32 v203, v85
	v_cvt_f32_i32_e32 v202, v84
	v_mov_b32_e32 v191, v190
	v_pk_mul_f32 v[220:221], v[190:191], v[108:109]
	v_pk_mul_f32 v[202:203], v[220:221], v[202:203]
	v_lshl_add_u64 v[146:147], v[146:147], 0, s[10:11]
	v_lshlrev_b64 v[146:147], 8, v[146:147]
	v_lshl_add_u64 v[146:147], v[196:197], 0, v[146:147]
	v_cvt_pk_bf16_f32 v220, v148, v149
	v_cvt_pk_bf16_f32 v221, v198, v199
	v_cvt_pk_bf16_f32 v222, v200, v201
	v_cvt_pk_bf16_f32 v223, v202, v203
	global_store_dwordx4 v[146:147], v[220:223], off
	s_nop 1
	v_cvt_f32_i32_e32 v147, v79
	v_cvt_f32_i32_e32 v146, v78
	v_pk_mul_f32 v[148:149], v[188:189], v[130:131] op_sel_hi:[0,1]
	v_pk_mul_f32 v[148:149], v[148:149], v[146:147]
	v_cvt_f32_i32_e32 v147, v81
	v_cvt_f32_i32_e32 v146, v80
	v_mov_b32_e32 v189, v188
	v_pk_mul_f32 v[198:199], v[188:189], v[132:133] op_sel_hi:[0,1]
	v_pk_mul_f32 v[198:199], v[198:199], v[146:147]
	v_cvt_f32_i32_e32 v147, v75
	v_cvt_f32_i32_e32 v146, v74
	v_pk_mul_f32 v[200:201], v[188:189], v[126:127]
	v_pk_mul_f32 v[200:201], v[200:201], v[146:147]
	v_cvt_f32_i32_e32 v147, v77
	v_cvt_f32_i32_e32 v146, v76
	v_mov_b32_e32 v202, v188
	v_mov_b32_e32 v203, v188
	v_pk_mul_f32 v[202:203], v[202:203], v[128:129]
	v_pk_mul_f32 v[202:203], v[202:203], v[146:147]
	v_or_b32_e32 v146, 48, v178
	v_mov_b32_e32 v147, v179
	v_cvt_pk_bf16_f32 v220, v148, v149
	v_lshl_add_u64 v[148:149], v[146:147], 0, s[16:17]
	v_lshlrev_b64 v[148:149], 8, v[148:149]
	v_lshl_add_u64 v[148:149], v[196:197], 0, v[148:149]
	v_cvt_pk_bf16_f32 v221, v198, v199
	v_cvt_pk_bf16_f32 v222, v200, v201
	v_cvt_pk_bf16_f32 v223, v202, v203
	global_store_dwordx4 v[148:149], v[220:223], off
	s_nop 1
	v_cvt_f32_i32_e32 v149, v71
	v_cvt_f32_i32_e32 v148, v70
	v_pk_mul_f32 v[198:199], v[188:189], v[110:111]
	v_pk_mul_f32 v[148:149], v[198:199], v[148:149]
	v_cvt_f32_i32_e32 v199, v73
	v_cvt_f32_i32_e32 v198, v72
	v_mov_b32_e32 v200, v188
	v_mov_b32_e32 v201, v188
	v_pk_mul_f32 v[200:201], v[200:201], v[112:113]
	v_pk_mul_f32 v[198:199], v[200:201], v[198:199]
	v_cvt_f32_i32_e32 v201, v67
	v_cvt_f32_i32_e32 v200, v66
	v_pk_mul_f32 v[202:203], v[188:189], v[106:107]
	v_pk_mul_f32 v[200:201], v[202:203], v[200:201]
	v_cvt_f32_i32_e32 v203, v69
	v_cvt_f32_i32_e32 v202, v68
	v_mov_b32_e32 v189, v188
	v_pk_mul_f32 v[220:221], v[188:189], v[108:109]
	v_pk_mul_f32 v[202:203], v[220:221], v[202:203]
	v_lshl_add_u64 v[146:147], v[146:147], 0, s[10:11]
	v_lshlrev_b64 v[146:147], 8, v[146:147]
	v_lshl_add_u64 v[146:147], v[196:197], 0, v[146:147]
	v_cvt_pk_bf16_f32 v220, v148, v149
	v_cvt_pk_bf16_f32 v221, v198, v199
	v_cvt_pk_bf16_f32 v222, v200, v201
	v_cvt_pk_bf16_f32 v223, v202, v203
	global_store_dwordx4 v[146:147], v[220:223], off
	s_nop 1
	v_cvt_f32_i32_e32 v147, v63
	v_cvt_f32_i32_e32 v146, v62
	v_pk_mul_f32 v[148:149], v[186:187], v[130:131] op_sel_hi:[0,1]
	v_pk_mul_f32 v[148:149], v[148:149], v[146:147]
	v_cvt_f32_i32_e32 v147, v65
	v_cvt_f32_i32_e32 v146, v64
	v_mov_b32_e32 v187, v186
	v_pk_mul_f32 v[198:199], v[186:187], v[132:133] op_sel_hi:[0,1]
	v_pk_mul_f32 v[198:199], v[198:199], v[146:147]
	v_cvt_f32_i32_e32 v147, v59
	v_cvt_f32_i32_e32 v146, v58
	v_pk_mul_f32 v[200:201], v[186:187], v[126:127]
	v_pk_mul_f32 v[200:201], v[200:201], v[146:147]
	v_cvt_f32_i32_e32 v147, v61
	v_cvt_f32_i32_e32 v146, v60
	v_mov_b32_e32 v202, v186
	v_mov_b32_e32 v203, v186
	v_pk_mul_f32 v[202:203], v[202:203], v[128:129]
	v_pk_mul_f32 v[202:203], v[202:203], v[146:147]
	v_lshl_add_u64 v[146:147], v[178:179], 0, s[34:35]
	v_cvt_pk_bf16_f32 v220, v148, v149
	v_lshl_add_u64 v[148:149], v[146:147], 0, s[16:17]
	v_lshlrev_b64 v[148:149], 8, v[148:149]
	v_lshl_add_u64 v[148:149], v[196:197], 0, v[148:149]
	v_cvt_pk_bf16_f32 v221, v198, v199
	v_cvt_pk_bf16_f32 v222, v200, v201
	v_cvt_pk_bf16_f32 v223, v202, v203
	global_store_dwordx4 v[148:149], v[220:223], off
	s_nop 1
	v_cvt_f32_i32_e32 v149, v55
	v_cvt_f32_i32_e32 v148, v54
	v_pk_mul_f32 v[198:199], v[186:187], v[110:111]
	v_pk_mul_f32 v[148:149], v[198:199], v[148:149]
	v_cvt_f32_i32_e32 v199, v57
	v_cvt_f32_i32_e32 v198, v56
	v_mov_b32_e32 v200, v186
	v_mov_b32_e32 v201, v186
	v_pk_mul_f32 v[200:201], v[200:201], v[112:113]
	v_pk_mul_f32 v[198:199], v[200:201], v[198:199]
	v_cvt_f32_i32_e32 v201, v51
	v_cvt_f32_i32_e32 v200, v50
	v_pk_mul_f32 v[202:203], v[186:187], v[106:107]
	v_pk_mul_f32 v[200:201], v[202:203], v[200:201]
	v_cvt_f32_i32_e32 v203, v53
	v_cvt_f32_i32_e32 v202, v52
	v_mov_b32_e32 v187, v186
	v_pk_mul_f32 v[220:221], v[186:187], v[108:109]
	v_pk_mul_f32 v[202:203], v[220:221], v[202:203]
	v_lshl_add_u64 v[146:147], v[146:147], 0, s[10:11]
	v_lshlrev_b64 v[146:147], 8, v[146:147]
	v_lshl_add_u64 v[146:147], v[196:197], 0, v[146:147]
	v_cvt_pk_bf16_f32 v220, v148, v149
	v_cvt_pk_bf16_f32 v221, v198, v199
	v_cvt_pk_bf16_f32 v222, v200, v201
	v_cvt_pk_bf16_f32 v223, v202, v203
	global_store_dwordx4 v[146:147], v[220:223], off
	s_nop 1
	v_cvt_f32_i32_e32 v147, v47
	v_cvt_f32_i32_e32 v146, v46
	v_pk_mul_f32 v[148:149], v[184:185], v[130:131] op_sel_hi:[0,1]
	v_pk_mul_f32 v[148:149], v[148:149], v[146:147]
	v_cvt_f32_i32_e32 v147, v49
	v_cvt_f32_i32_e32 v146, v48
	v_mov_b32_e32 v185, v184
	v_pk_mul_f32 v[198:199], v[184:185], v[132:133] op_sel_hi:[0,1]
	v_pk_mul_f32 v[198:199], v[198:199], v[146:147]
	v_cvt_f32_i32_e32 v147, v43
	v_cvt_f32_i32_e32 v146, v42
	v_pk_mul_f32 v[200:201], v[184:185], v[126:127]
	v_pk_mul_f32 v[200:201], v[200:201], v[146:147]
	v_cvt_f32_i32_e32 v147, v45
	v_cvt_f32_i32_e32 v146, v44
	v_mov_b32_e32 v202, v184
	v_mov_b32_e32 v203, v184
	v_pk_mul_f32 v[202:203], v[202:203], v[128:129]
	v_pk_mul_f32 v[202:203], v[202:203], v[146:147]
	v_lshl_add_u64 v[146:147], v[178:179], 0, s[42:43]
	v_cvt_pk_bf16_f32 v220, v148, v149
	v_lshl_add_u64 v[148:149], v[146:147], 0, s[16:17]
	v_lshlrev_b64 v[148:149], 8, v[148:149]
	v_lshl_add_u64 v[148:149], v[196:197], 0, v[148:149]
	v_cvt_pk_bf16_f32 v221, v198, v199
	v_cvt_pk_bf16_f32 v222, v200, v201
	v_cvt_pk_bf16_f32 v223, v202, v203
	global_store_dwordx4 v[148:149], v[220:223], off
	s_nop 1
	v_cvt_f32_i32_e32 v149, v39
	v_cvt_f32_i32_e32 v148, v38
	v_pk_mul_f32 v[198:199], v[184:185], v[110:111]
	v_pk_mul_f32 v[148:149], v[198:199], v[148:149]
	v_cvt_f32_i32_e32 v199, v41
	v_cvt_f32_i32_e32 v198, v40
	v_mov_b32_e32 v200, v184
	v_mov_b32_e32 v201, v184
	v_pk_mul_f32 v[200:201], v[200:201], v[112:113]
	v_pk_mul_f32 v[198:199], v[200:201], v[198:199]
	v_cvt_f32_i32_e32 v201, v35
	v_cvt_f32_i32_e32 v200, v34
	v_pk_mul_f32 v[202:203], v[184:185], v[106:107]
	v_pk_mul_f32 v[200:201], v[202:203], v[200:201]
	v_cvt_f32_i32_e32 v203, v37
	v_cvt_f32_i32_e32 v202, v36
	v_mov_b32_e32 v185, v184
	v_pk_mul_f32 v[220:221], v[184:185], v[108:109]
	v_pk_mul_f32 v[202:203], v[220:221], v[202:203]
	v_lshl_add_u64 v[146:147], v[146:147], 0, s[10:11]
	v_lshlrev_b64 v[146:147], 8, v[146:147]
	v_lshl_add_u64 v[146:147], v[196:197], 0, v[146:147]
	v_cvt_pk_bf16_f32 v220, v148, v149
	v_cvt_pk_bf16_f32 v221, v198, v199
	v_cvt_pk_bf16_f32 v222, v200, v201
	v_cvt_pk_bf16_f32 v223, v202, v203
	global_store_dwordx4 v[146:147], v[220:223], off
	s_nop 1
	v_cvt_f32_i32_e32 v147, v31
	v_cvt_f32_i32_e32 v146, v30
	v_pk_mul_f32 v[148:149], v[182:183], v[130:131] op_sel_hi:[0,1]
	v_pk_mul_f32 v[148:149], v[148:149], v[146:147]
	v_cvt_f32_i32_e32 v147, v33
	v_cvt_f32_i32_e32 v146, v32
	v_mov_b32_e32 v183, v182
	v_pk_mul_f32 v[198:199], v[182:183], v[132:133] op_sel_hi:[0,1]
	v_pk_mul_f32 v[198:199], v[198:199], v[146:147]
	v_cvt_f32_i32_e32 v147, v27
	v_cvt_f32_i32_e32 v146, v26
	v_pk_mul_f32 v[200:201], v[182:183], v[126:127]
	v_pk_mul_f32 v[200:201], v[200:201], v[146:147]
	v_cvt_f32_i32_e32 v147, v29
	v_cvt_f32_i32_e32 v146, v28
	v_mov_b32_e32 v202, v182
	v_mov_b32_e32 v203, v182
	v_pk_mul_f32 v[202:203], v[202:203], v[128:129]
	v_pk_mul_f32 v[202:203], v[202:203], v[146:147]
	v_lshl_add_u64 v[146:147], v[178:179], 0, s[52:53]
	v_cvt_pk_bf16_f32 v220, v148, v149
	v_lshl_add_u64 v[148:149], v[146:147], 0, s[16:17]
	v_lshlrev_b64 v[148:149], 8, v[148:149]
	v_lshl_add_u64 v[148:149], v[196:197], 0, v[148:149]
	v_cvt_pk_bf16_f32 v221, v198, v199
	v_cvt_pk_bf16_f32 v222, v200, v201
	v_cvt_pk_bf16_f32 v223, v202, v203
	global_store_dwordx4 v[148:149], v[220:223], off
	s_nop 1
	v_cvt_f32_i32_e32 v149, v23
	v_cvt_f32_i32_e32 v148, v22
	v_pk_mul_f32 v[198:199], v[182:183], v[110:111]
	v_pk_mul_f32 v[148:149], v[198:199], v[148:149]
	v_cvt_f32_i32_e32 v199, v25
	v_cvt_f32_i32_e32 v198, v24
	v_mov_b32_e32 v200, v182
	v_mov_b32_e32 v201, v182
	v_pk_mul_f32 v[200:201], v[200:201], v[112:113]
	v_pk_mul_f32 v[198:199], v[200:201], v[198:199]
	v_cvt_f32_i32_e32 v201, v19
	v_cvt_f32_i32_e32 v200, v18
	v_pk_mul_f32 v[202:203], v[182:183], v[106:107]
	v_pk_mul_f32 v[200:201], v[202:203], v[200:201]
	v_cvt_f32_i32_e32 v203, v21
	v_cvt_f32_i32_e32 v202, v20
	v_mov_b32_e32 v183, v182
	v_pk_mul_f32 v[220:221], v[182:183], v[108:109]
	v_pk_mul_f32 v[202:203], v[220:221], v[202:203]
	v_lshl_add_u64 v[146:147], v[146:147], 0, s[10:11]
	v_lshlrev_b64 v[146:147], 8, v[146:147]
	v_lshl_add_u64 v[146:147], v[196:197], 0, v[146:147]
	v_cvt_pk_bf16_f32 v220, v148, v149
	v_cvt_pk_bf16_f32 v221, v198, v199
	v_cvt_pk_bf16_f32 v222, v200, v201
	v_cvt_pk_bf16_f32 v223, v202, v203
	global_store_dwordx4 v[146:147], v[220:223], off
	s_nop 1
	v_cvt_f32_i32_e32 v147, v15
	v_cvt_f32_i32_e32 v146, v14
	v_pk_mul_f32 v[148:149], v[130:131], v[180:181] op_sel_hi:[1,0]
	v_pk_mul_f32 v[146:147], v[148:149], v[146:147]
	v_cvt_f32_i32_e32 v149, v17
	v_cvt_f32_i32_e32 v148, v16
	v_mov_b32_e32 v181, v180
	v_pk_mul_f32 v[198:199], v[132:133], v[180:181] op_sel_hi:[1,0]
	v_pk_mul_f32 v[148:149], v[198:199], v[148:149]
	v_cvt_f32_i32_e32 v199, v11
	v_cvt_f32_i32_e32 v198, v10
	v_pk_mul_f32 v[200:201], v[180:181], v[126:127]
	v_pk_mul_f32 v[200:201], v[200:201], v[198:199]
	v_cvt_f32_i32_e32 v199, v13
	v_cvt_f32_i32_e32 v198, v12
	v_mov_b32_e32 v202, v180
	v_mov_b32_e32 v203, v180
	v_pk_mul_f32 v[202:203], v[202:203], v[128:129]
	v_pk_mul_f32 v[202:203], v[202:203], v[198:199]
	v_lshl_add_u64 v[198:199], v[178:179], 0, s[54:55]
	v_cvt_pk_bf16_f32 v146, v146, v147
	v_cvt_pk_bf16_f32 v147, v148, v149
	v_cvt_pk_bf16_f32 v148, v200, v201
	v_lshl_add_u64 v[200:201], v[198:199], 0, s[16:17]
	v_lshlrev_b64 v[200:201], 8, v[200:201]
	v_lshl_add_u64 v[200:201], v[196:197], 0, v[200:201]
	v_cvt_pk_bf16_f32 v149, v202, v203
	global_store_dwordx4 v[200:201], v[146:149], off
	s_nop 1
	v_cvt_f32_i32_e32 v147, v7
	v_cvt_f32_i32_e32 v146, v6
	v_pk_mul_f32 v[148:149], v[180:181], v[110:111]
	v_pk_mul_f32 v[146:147], v[148:149], v[146:147]
	v_cvt_f32_i32_e32 v149, v9
	v_cvt_f32_i32_e32 v148, v8
	v_mov_b32_e32 v200, v180
	v_mov_b32_e32 v201, v180
	v_pk_mul_f32 v[200:201], v[200:201], v[112:113]
	v_pk_mul_f32 v[148:149], v[200:201], v[148:149]
	v_cvt_f32_i32_e32 v201, v3
	v_cvt_f32_i32_e32 v200, v2
	v_pk_mul_f32 v[202:203], v[180:181], v[106:107]
	v_pk_mul_f32 v[200:201], v[202:203], v[200:201]
	v_cvt_f32_i32_e32 v203, v5
	v_cvt_f32_i32_e32 v202, v4
	v_mov_b32_e32 v181, v180
	v_pk_mul_f32 v[220:221], v[180:181], v[108:109]
	v_pk_mul_f32 v[202:203], v[220:221], v[202:203]
	v_cvt_pk_bf16_f32 v146, v146, v147
	v_cvt_pk_bf16_f32 v147, v148, v149
	v_cvt_pk_bf16_f32 v148, v200, v201
	v_cvt_pk_bf16_f32 v149, v202, v203
	v_lshl_add_u64 v[198:199], v[198:199], 0, s[10:11]
	s_branch .LBB0_354
.Lepi_lo:
	s_cmp_eq_u32 s59, 2
	s_cbranch_scc1 .Lepi_t2
	s_mov_b64 s[68:69], s[22:23]
	v_mov_b64_e32 v[196:197], v[166:167]
	s_cmp_eq_u32 s59, 3
	s_cselect_b64 s[10:11], -1, 0
	v_cvt_f32_i32_e32 v147, v143
	v_cvt_f32_i32_e32 v146, v142
	s_waitcnt vmcnt(0)
	v_pk_mul_f32 v[148:149], v[194:195], v[130:131] op_sel_hi:[0,1]
	v_cndmask_b32_e64 v219, 1.0, v217, s[10:11]
	v_pk_mul_f32 v[146:147], v[148:149], v[146:147]
	v_mul_f32_e32 v148, 0xbfb8aa3b, v146
	v_exp_f32_e32 v148, v148
	v_mul_f32_e32 v146, v219, v146
	v_add_f32_e32 v148, 1.0, v148
	v_rcp_f32_e32 v148, v148
	s_nop 0
	v_mul_f32_e32 v146, v146, v148
	v_cvt_f32_i32_e32 v149, v145
	v_cvt_f32_i32_e32 v148, v144
	v_mov_b32_e32 v195, v194
	v_pk_mul_f32 v[196:197], v[194:195], v[132:133] op_sel_hi:[0,1]
	v_pk_mul_f32 v[148:149], v[196:197], v[148:149]
	v_mul_f32_e32 v158, 0xbfb8aa3b, v147
	v_exp_f32_e32 v158, v158
	v_mul_f32_e32 v147, v219, v147
	v_add_f32_e32 v158, 1.0, v158
	v_rcp_f32_e32 v158, v158
	s_nop 0
	v_mul_f32_e32 v147, v147, v158
	v_mul_f32_e32 v158, 0xbfb8aa3b, v148
	v_exp_f32_e32 v158, v158
	v_mul_f32_e32 v148, v219, v148
	v_add_f32_e32 v158, 1.0, v158
	v_rcp_f32_e32 v158, v158
	s_nop 0
	v_mul_f32_e32 v148, v148, v158
	v_mul_f32_e32 v158, 0xbfb8aa3b, v149
	v_exp_f32_e32 v158, v158
	v_mul_f32_e32 v149, v219, v149
	v_add_f32_e32 v158, 1.0, v158
	v_rcp_f32_e32 v158, v158
	s_nop 0
	v_mul_f32_e32 v149, v149, v158
	v_cvt_f32_i32_e32 v197, v139
	v_cvt_f32_i32_e32 v196, v138
	v_pk_mul_f32 v[198:199], v[194:195], v[126:127]
	v_pk_mul_f32 v[198:199], v[198:199], v[196:197]
	v_mul_f32_e32 v158, 0xbfb8aa3b, v198
	v_exp_f32_e32 v158, v158
	v_mul_f32_e32 v181, v219, v198
	v_add_f32_e32 v158, 1.0, v158
	v_rcp_f32_e32 v158, v158
	s_nop 0
	v_mul_f32_e32 v198, v181, v158
	v_cvt_f32_i32_e32 v197, v141
	v_cvt_f32_i32_e32 v196, v140
	v_mov_b32_e32 v200, v194
	v_mov_b32_e32 v201, v194
	v_pk_mul_f32 v[200:201], v[200:201], v[128:129]
	v_pk_mul_f32 v[200:201], v[200:201], v[196:197]
	v_mul_f32_e32 v158, 0xbfb8aa3b, v199
	v_exp_f32_e32 v158, v158
	v_mul_f32_e32 v181, v219, v199
	v_add_f32_e32 v158, 1.0, v158
	v_rcp_f32_e32 v158, v158
	s_nop 0
	v_mul_f32_e32 v199, v181, v158
	v_mul_f32_e32 v158, 0xbfb8aa3b, v200
	v_exp_f32_e32 v158, v158
	v_mul_f32_e32 v181, v219, v200
	v_add_f32_e32 v158, 1.0, v158
	v_rcp_f32_e32 v158, v158
	s_nop 0
	v_mul_f32_e32 v200, v181, v158
	v_mul_f32_e32 v158, 0xbfb8aa3b, v201
	v_exp_f32_e32 v158, v158
	v_mul_f32_e32 v181, v219, v201
	v_add_f32_e32 v158, 1.0, v158
	v_rcp_f32_e32 v158, v158
	s_nop 0
	v_mul_f32_e32 v201, v181, v158
	s_lshl_b32 s16, s57, 13
	v_lshlrev_b32_e32 v158, 1, v162
	v_cvt_pk_bf16_f32 v146, v146, v147
	v_cvt_pk_bf16_f32 v147, v148, v149
	v_cvt_pk_bf16_f32 v148, v198, v199
	v_lshl_add_u64 v[198:199], v[178:179], 0, s[16:17]
	v_lshl_add_u64 v[196:197], s[68:69], 0, v[158:159]
	v_lshlrev_b64 v[198:199], 8, v[198:199]
	v_lshl_add_u64 v[198:199], v[196:197], 0, v[198:199]
	v_cvt_pk_bf16_f32 v149, v200, v201
	global_store_dwordx4 v[198:199], v[146:149], off
	s_nop 1
	v_cvt_f32_i32_e32 v147, v135
	v_cvt_f32_i32_e32 v146, v134
	v_pk_mul_f32 v[148:149], v[194:195], v[110:111]
	v_pk_mul_f32 v[146:147], v[148:149], v[146:147]
	v_mul_f32_e32 v148, 0xbfb8aa3b, v146
	v_exp_f32_e32 v148, v148
	v_mul_f32_e32 v146, v219, v146
	v_add_f32_e32 v148, 1.0, v148
	v_rcp_f32_e32 v148, v148
	s_nop 0
	v_mul_f32_e32 v146, v146, v148
	v_cvt_f32_i32_e32 v149, v137
	v_cvt_f32_i32_e32 v148, v136
	v_mov_b32_e32 v198, v194
	v_mov_b32_e32 v199, v194
	v_pk_mul_f32 v[198:199], v[198:199], v[112:113]
	v_pk_mul_f32 v[148:149], v[198:199], v[148:149]
	v_mul_f32_e32 v158, 0xbfb8aa3b, v147
	v_exp_f32_e32 v158, v158
	v_mul_f32_e32 v147, v219, v147
	v_add_f32_e32 v158, 1.0, v158
	v_rcp_f32_e32 v158, v158
	s_nop 0
	v_mul_f32_e32 v147, v147, v158
	v_mul_f32_e32 v158, 0xbfb8aa3b, v148
	v_exp_f32_e32 v158, v158
	v_mul_f32_e32 v148, v219, v148
	v_add_f32_e32 v158, 1.0, v158
	v_rcp_f32_e32 v158, v158
	s_nop 0
	v_mul_f32_e32 v148, v148, v158
	v_mul_f32_e32 v158, 0xbfb8aa3b, v149
	v_exp_f32_e32 v158, v158
	v_mul_f32_e32 v149, v219, v149
	v_add_f32_e32 v158, 1.0, v158
	v_rcp_f32_e32 v158, v158
	s_nop 0
	v_mul_f32_e32 v149, v149, v158
	v_cvt_f32_i32_e32 v199, v123
	v_cvt_f32_i32_e32 v198, v122
	v_pk_mul_f32 v[200:201], v[194:195], v[106:107]
	v_pk_mul_f32 v[198:199], v[200:201], v[198:199]
	v_mul_f32_e32 v158, 0xbfb8aa3b, v198
	v_exp_f32_e32 v158, v158
	v_mul_f32_e32 v181, v219, v198
	v_add_f32_e32 v158, 1.0, v158
	v_rcp_f32_e32 v158, v158
	s_nop 0
	v_mul_f32_e32 v198, v181, v158
	v_cvt_f32_i32_e32 v201, v125
	v_cvt_f32_i32_e32 v200, v124
	v_mov_b32_e32 v195, v194
	v_pk_mul_f32 v[202:203], v[194:195], v[108:109]
	v_pk_mul_f32 v[200:201], v[202:203], v[200:201]
	v_mul_f32_e32 v158, 0xbfb8aa3b, v199
	v_exp_f32_e32 v158, v158
	v_mul_f32_e32 v181, v219, v199
	v_add_f32_e32 v158, 1.0, v158
	v_rcp_f32_e32 v158, v158
	s_nop 0
	v_mul_f32_e32 v199, v181, v158
	v_mul_f32_e32 v158, 0xbfb8aa3b, v200
	v_exp_f32_e32 v158, v158
	v_mul_f32_e32 v181, v219, v200
	v_add_f32_e32 v158, 1.0, v158
	v_rcp_f32_e32 v158, v158
	s_nop 0
	v_mul_f32_e32 v200, v181, v158
	v_mul_f32_e32 v158, 0xbfb8aa3b, v201
	v_exp_f32_e32 v158, v158
	v_mul_f32_e32 v181, v219, v201
	v_add_f32_e32 v158, 1.0, v158
	v_rcp_f32_e32 v158, v158
	s_nop 0
	v_mul_f32_e32 v201, v181, v158
	s_or_b32 s10, s16, 0x2000
	s_mov_b32 s11, s17
	v_cvt_pk_bf16_f32 v146, v146, v147
	v_cvt_pk_bf16_f32 v147, v148, v149
	v_cvt_pk_bf16_f32 v148, v198, v199
	v_lshl_add_u64 v[198:199], v[178:179], 0, s[10:11]
	v_lshlrev_b64 v[198:199], 8, v[198:199]
	v_lshl_add_u64 v[198:199], v[196:197], 0, v[198:199]
	v_cvt_pk_bf16_f32 v149, v200, v201
	global_store_dwordx4 v[198:199], v[146:149], off
	s_nop 1
	v_cvt_f32_i32_e32 v147, v119
	v_cvt_f32_i32_e32 v146, v118
	v_pk_mul_f32 v[148:149], v[192:193], v[130:131] op_sel_hi:[0,1]
	v_pk_mul_f32 v[148:149], v[148:149], v[146:147]
	v_mul_f32_e32 v146, 0xbfb8aa3b, v148
	v_exp_f32_e32 v146, v146
	v_mul_f32_e32 v147, v219, v148
	v_add_f32_e32 v146, 1.0, v146
	v_rcp_f32_e32 v146, v146
	s_nop 0
	v_mul_f32_e32 v148, v147, v146
	v_cvt_f32_i32_e32 v147, v121
	v_cvt_f32_i32_e32 v146, v120
	v_mov_b32_e32 v193, v192
	v_pk_mul_f32 v[198:199], v[192:193], v[132:133] op_sel_hi:[0,1]
	v_pk_mul_f32 v[198:199], v[198:199], v[146:147]
	v_mul_f32_e32 v146, 0xbfb8aa3b, v149
	v_exp_f32_e32 v146, v146
	v_mul_f32_e32 v147, v219, v149
	v_add_f32_e32 v146, 1.0, v146
	v_rcp_f32_e32 v146, v146
	s_nop 0
	v_mul_f32_e32 v149, v147, v146
	v_mul_f32_e32 v146, 0xbfb8aa3b, v198
	v_exp_f32_e32 v146, v146
	v_mul_f32_e32 v147, v219, v198
	v_add_f32_e32 v146, 1.0, v146
	v_rcp_f32_e32 v146, v146
	s_nop 0
	v_mul_f32_e32 v198, v147, v146
	v_mul_f32_e32 v146, 0xbfb8aa3b, v199
	v_exp_f32_e32 v146, v146
	v_mul_f32_e32 v147, v219, v199
	v_add_f32_e32 v146, 1.0, v146
	v_rcp_f32_e32 v146, v146
	s_nop 0
	v_mul_f32_e32 v199, v147, v146
	v_cvt_f32_i32_e32 v147, v115
	v_cvt_f32_i32_e32 v146, v114
	v_pk_mul_f32 v[200:201], v[192:193], v[126:127]
	v_pk_mul_f32 v[200:201], v[200:201], v[146:147]
	v_mul_f32_e32 v146, 0xbfb8aa3b, v200
	v_exp_f32_e32 v146, v146
	v_mul_f32_e32 v147, v219, v200
	v_add_f32_e32 v146, 1.0, v146
	v_rcp_f32_e32 v146, v146
	s_nop 0
	v_mul_f32_e32 v200, v147, v146
	v_cvt_f32_i32_e32 v147, v117
	v_cvt_f32_i32_e32 v146, v116
	v_mov_b32_e32 v202, v192
	v_mov_b32_e32 v203, v192
	v_pk_mul_f32 v[202:203], v[202:203], v[128:129]
	v_pk_mul_f32 v[202:203], v[202:203], v[146:147]
	v_mul_f32_e32 v146, 0xbfb8aa3b, v201
	v_exp_f32_e32 v146, v146
	v_mul_f32_e32 v147, v219, v201
	v_add_f32_e32 v146, 1.0, v146
	v_rcp_f32_e32 v146, v146
	s_nop 0
	v_mul_f32_e32 v201, v147, v146
	v_mul_f32_e32 v146, 0xbfb8aa3b, v202
	v_exp_f32_e32 v146, v146
	v_mul_f32_e32 v147, v219, v202
	v_add_f32_e32 v146, 1.0, v146
	v_rcp_f32_e32 v146, v146
	s_nop 0
	v_mul_f32_e32 v202, v147, v146
	v_mul_f32_e32 v146, 0xbfb8aa3b, v203
	v_exp_f32_e32 v146, v146
	v_mul_f32_e32 v147, v219, v203
	v_add_f32_e32 v146, 1.0, v146
	v_rcp_f32_e32 v146, v146
	s_nop 0
	v_mul_f32_e32 v203, v147, v146
	v_or_b32_e32 v146, 16, v178
	v_mov_b32_e32 v147, v179
	v_cvt_pk_bf16_f32 v220, v148, v149
	v_lshl_add_u64 v[148:149], v[146:147], 0, s[16:17]
	v_lshlrev_b64 v[148:149], 8, v[148:149]
	v_lshl_add_u64 v[148:149], v[196:197], 0, v[148:149]
	v_cvt_pk_bf16_f32 v221, v198, v199
	v_cvt_pk_bf16_f32 v222, v200, v201
	v_cvt_pk_bf16_f32 v223, v202, v203
	global_store_dwordx4 v[148:149], v[220:223], off
	s_nop 1
	v_cvt_f32_i32_e32 v149, v103
	v_cvt_f32_i32_e32 v148, v102
	v_pk_mul_f32 v[198:199], v[192:193], v[110:111]
	v_pk_mul_f32 v[148:149], v[198:199], v[148:149]
	v_mul_f32_e32 v158, 0xbfb8aa3b, v148
	v_exp_f32_e32 v158, v158
	v_mul_f32_e32 v148, v219, v148
	v_add_f32_e32 v158, 1.0, v158
	v_rcp_f32_e32 v158, v158
	s_nop 0
	v_mul_f32_e32 v148, v148, v158
	v_cvt_f32_i32_e32 v199, v105
	v_cvt_f32_i32_e32 v198, v104
	v_mov_b32_e32 v200, v192
	v_mov_b32_e32 v201, v192
	v_pk_mul_f32 v[200:201], v[200:201], v[112:113]
	v_pk_mul_f32 v[198:199], v[200:201], v[198:199]
	v_mul_f32_e32 v158, 0xbfb8aa3b, v149
	v_exp_f32_e32 v158, v158
	v_mul_f32_e32 v149, v219, v149
	v_add_f32_e32 v158, 1.0, v158
	v_rcp_f32_e32 v158, v158
	s_nop 0
	v_mul_f32_e32 v149, v149, v158
	v_mul_f32_e32 v158, 0xbfb8aa3b, v198
	v_exp_f32_e32 v158, v158
	v_mul_f32_e32 v181, v219, v198
	v_add_f32_e32 v158, 1.0, v158
	v_rcp_f32_e32 v158, v158
	s_nop 0
	v_mul_f32_e32 v198, v181, v158
	v_mul_f32_e32 v158, 0xbfb8aa3b, v199
	v_exp_f32_e32 v158, v158
	v_mul_f32_e32 v181, v219, v199
	v_add_f32_e32 v158, 1.0, v158
	v_rcp_f32_e32 v158, v158
	s_nop 0
	v_mul_f32_e32 v199, v181, v158
	v_cvt_f32_i32_e32 v201, v99
	v_cvt_f32_i32_e32 v200, v98
	v_pk_mul_f32 v[202:203], v[192:193], v[106:107]
	v_pk_mul_f32 v[200:201], v[202:203], v[200:201]
	v_mul_f32_e32 v158, 0xbfb8aa3b, v200
	v_exp_f32_e32 v158, v158
	v_mul_f32_e32 v181, v219, v200
	v_add_f32_e32 v158, 1.0, v158
	v_rcp_f32_e32 v158, v158
	s_nop 0
	v_mul_f32_e32 v200, v181, v158
	v_cvt_f32_i32_e32 v203, v101
	v_cvt_f32_i32_e32 v202, v100
	v_mov_b32_e32 v193, v192
	v_pk_mul_f32 v[220:221], v[192:193], v[108:109]
	v_pk_mul_f32 v[202:203], v[220:221], v[202:203]
	v_mul_f32_e32 v158, 0xbfb8aa3b, v201
	v_exp_f32_e32 v158, v158
	v_mul_f32_e32 v181, v219, v201
	v_add_f32_e32 v158, 1.0, v158
	v_rcp_f32_e32 v158, v158
	s_nop 0
	v_mul_f32_e32 v201, v181, v158
	v_mul_f32_e32 v158, 0xbfb8aa3b, v202
	v_exp_f32_e32 v158, v158
	v_mul_f32_e32 v181, v219, v202
	v_add_f32_e32 v158, 1.0, v158
	v_rcp_f32_e32 v158, v158
	s_nop 0
	v_mul_f32_e32 v202, v181, v158
	v_mul_f32_e32 v158, 0xbfb8aa3b, v203
	v_exp_f32_e32 v158, v158
	v_mul_f32_e32 v181, v219, v203
	v_add_f32_e32 v158, 1.0, v158
	v_rcp_f32_e32 v158, v158
	s_nop 0
	v_mul_f32_e32 v203, v181, v158
	v_lshl_add_u64 v[146:147], v[146:147], 0, s[10:11]
	v_lshlrev_b64 v[146:147], 8, v[146:147]
	v_lshl_add_u64 v[146:147], v[196:197], 0, v[146:147]
	v_cvt_pk_bf16_f32 v220, v148, v149
	v_cvt_pk_bf16_f32 v221, v198, v199
	v_cvt_pk_bf16_f32 v222, v200, v201
	v_cvt_pk_bf16_f32 v223, v202, v203
	global_store_dwordx4 v[146:147], v[220:223], off
	s_nop 1
	v_cvt_f32_i32_e32 v147, v95
	v_cvt_f32_i32_e32 v146, v94
	v_pk_mul_f32 v[148:149], v[190:191], v[130:131] op_sel_hi:[0,1]
	v_pk_mul_f32 v[148:149], v[148:149], v[146:147]
	v_mul_f32_e32 v146, 0xbfb8aa3b, v148
	v_exp_f32_e32 v146, v146
	v_mul_f32_e32 v147, v219, v148
	v_add_f32_e32 v146, 1.0, v146
	v_rcp_f32_e32 v146, v146
	s_nop 0
	v_mul_f32_e32 v148, v147, v146
	v_cvt_f32_i32_e32 v147, v97
	v_cvt_f32_i32_e32 v146, v96
	v_mov_b32_e32 v191, v190
	v_pk_mul_f32 v[198:199], v[190:191], v[132:133] op_sel_hi:[0,1]
	v_pk_mul_f32 v[198:199], v[198:199], v[146:147]
	v_mul_f32_e32 v146, 0xbfb8aa3b, v149
	v_exp_f32_e32 v146, v146
	v_mul_f32_e32 v147, v219, v149
	v_add_f32_e32 v146, 1.0, v146
	v_rcp_f32_e32 v146, v146
	s_nop 0
	v_mul_f32_e32 v149, v147, v146
	v_mul_f32_e32 v146, 0xbfb8aa3b, v198
	v_exp_f32_e32 v146, v146
	v_mul_f32_e32 v147, v219, v198
	v_add_f32_e32 v146, 1.0, v146
	v_rcp_f32_e32 v146, v146
	s_nop 0
	v_mul_f32_e32 v198, v147, v146
	v_mul_f32_e32 v146, 0xbfb8aa3b, v199
	v_exp_f32_e32 v146, v146
	v_mul_f32_e32 v147, v219, v199
	v_add_f32_e32 v146, 1.0, v146
	v_rcp_f32_e32 v146, v146
	s_nop 0
	v_mul_f32_e32 v199, v147, v146
	v_cvt_f32_i32_e32 v147, v91
	v_cvt_f32_i32_e32 v146, v90
	v_pk_mul_f32 v[200:201], v[190:191], v[126:127]
	v_pk_mul_f32 v[200:201], v[200:201], v[146:147]
	v_mul_f32_e32 v146, 0xbfb8aa3b, v200
	v_exp_f32_e32 v146, v146
	v_mul_f32_e32 v147, v219, v200
	v_add_f32_e32 v146, 1.0, v146
	v_rcp_f32_e32 v146, v146
	s_nop 0
	v_mul_f32_e32 v200, v147, v146
	v_cvt_f32_i32_e32 v147, v93
	v_cvt_f32_i32_e32 v146, v92
	v_mov_b32_e32 v202, v190
	v_mov_b32_e32 v203, v190
	v_pk_mul_f32 v[202:203], v[202:203], v[128:129]
	v_pk_mul_f32 v[202:203], v[202:203], v[146:147]
	v_mul_f32_e32 v146, 0xbfb8aa3b, v201
	v_exp_f32_e32 v146, v146
	v_mul_f32_e32 v147, v219, v201
	v_add_f32_e32 v146, 1.0, v146
	v_rcp_f32_e32 v146, v146
	s_nop 0
	v_mul_f32_e32 v201, v147, v146
	v_mul_f32_e32 v146, 0xbfb8aa3b, v202
	v_exp_f32_e32 v146, v146
	v_mul_f32_e32 v147, v219, v202
	v_add_f32_e32 v146, 1.0, v146
	v_rcp_f32_e32 v146, v146
	s_nop 0
	v_mul_f32_e32 v202, v147, v146
	v_mul_f32_e32 v146, 0xbfb8aa3b, v203
	v_exp_f32_e32 v146, v146
	v_mul_f32_e32 v147, v219, v203
	v_add_f32_e32 v146, 1.0, v146
	v_rcp_f32_e32 v146, v146
	s_nop 0
	v_mul_f32_e32 v203, v147, v146
	v_or_b32_e32 v146, 32, v178
	v_mov_b32_e32 v147, v179
	v_cvt_pk_bf16_f32 v220, v148, v149
	v_lshl_add_u64 v[148:149], v[146:147], 0, s[16:17]
	v_lshlrev_b64 v[148:149], 8, v[148:149]
	v_lshl_add_u64 v[148:149], v[196:197], 0, v[148:149]
	v_cvt_pk_bf16_f32 v221, v198, v199
	v_cvt_pk_bf16_f32 v222, v200, v201
	v_cvt_pk_bf16_f32 v223, v202, v203
	global_store_dwordx4 v[148:149], v[220:223], off
	s_nop 1
	v_cvt_f32_i32_e32 v149, v87
	v_cvt_f32_i32_e32 v148, v86
	v_pk_mul_f32 v[198:199], v[190:191], v[110:111]
	v_pk_mul_f32 v[148:149], v[198:199], v[148:149]
	v_mul_f32_e32 v158, 0xbfb8aa3b, v148
	v_exp_f32_e32 v158, v158
	v_mul_f32_e32 v148, v219, v148
	v_add_f32_e32 v158, 1.0, v158
	v_rcp_f32_e32 v158, v158
	s_nop 0
	v_mul_f32_e32 v148, v148, v158
	v_cvt_f32_i32_e32 v199, v89
	v_cvt_f32_i32_e32 v198, v88
	v_mov_b32_e32 v200, v190
	v_mov_b32_e32 v201, v190
	v_pk_mul_f32 v[200:201], v[200:201], v[112:113]
	v_pk_mul_f32 v[198:199], v[200:201], v[198:199]
	v_mul_f32_e32 v158, 0xbfb8aa3b, v149
	v_exp_f32_e32 v158, v158
	v_mul_f32_e32 v149, v219, v149
	v_add_f32_e32 v158, 1.0, v158
	v_rcp_f32_e32 v158, v158
	s_nop 0
	v_mul_f32_e32 v149, v149, v158
	v_mul_f32_e32 v158, 0xbfb8aa3b, v198
	v_exp_f32_e32 v158, v158
	v_mul_f32_e32 v181, v219, v198
	v_add_f32_e32 v158, 1.0, v158
	v_rcp_f32_e32 v158, v158
	s_nop 0
	v_mul_f32_e32 v198, v181, v158
	v_mul_f32_e32 v158, 0xbfb8aa3b, v199
	v_exp_f32_e32 v158, v158
	v_mul_f32_e32 v181, v219, v199
	v_add_f32_e32 v158, 1.0, v158
	v_rcp_f32_e32 v158, v158
	s_nop 0
	v_mul_f32_e32 v199, v181, v158
	v_cvt_f32_i32_e32 v201, v83
	v_cvt_f32_i32_e32 v200, v82
	v_pk_mul_f32 v[202:203], v[190:191], v[106:107]
	v_pk_mul_f32 v[200:201], v[202:203], v[200:201]
	v_mul_f32_e32 v158, 0xbfb8aa3b, v200
	v_exp_f32_e32 v158, v158
	v_mul_f32_e32 v181, v219, v200
	v_add_f32_e32 v158, 1.0, v158
	v_rcp_f32_e32 v158, v158
	s_nop 0
	v_mul_f32_e32 v200, v181, v158
	v_cvt_f32_i32_e32 v203, v85
	v_cvt_f32_i32_e32 v202, v84
	v_mov_b32_e32 v191, v190
	v_pk_mul_f32 v[220:221], v[190:191], v[108:109]
	v_pk_mul_f32 v[202:203], v[220:221], v[202:203]
	v_mul_f32_e32 v158, 0xbfb8aa3b, v201
	v_exp_f32_e32 v158, v158
	v_mul_f32_e32 v181, v219, v201
	v_add_f32_e32 v158, 1.0, v158
	v_rcp_f32_e32 v158, v158
	s_nop 0
	v_mul_f32_e32 v201, v181, v158
	v_mul_f32_e32 v158, 0xbfb8aa3b, v202
	v_exp_f32_e32 v158, v158
	v_mul_f32_e32 v181, v219, v202
	v_add_f32_e32 v158, 1.0, v158
	v_rcp_f32_e32 v158, v158
	s_nop 0
	v_mul_f32_e32 v202, v181, v158
	v_mul_f32_e32 v158, 0xbfb8aa3b, v203
	v_exp_f32_e32 v158, v158
	v_mul_f32_e32 v181, v219, v203
	v_add_f32_e32 v158, 1.0, v158
	v_rcp_f32_e32 v158, v158
	s_nop 0
	v_mul_f32_e32 v203, v181, v158
	v_lshl_add_u64 v[146:147], v[146:147], 0, s[10:11]
	v_lshlrev_b64 v[146:147], 8, v[146:147]
	v_lshl_add_u64 v[146:147], v[196:197], 0, v[146:147]
	v_cvt_pk_bf16_f32 v220, v148, v149
	v_cvt_pk_bf16_f32 v221, v198, v199
	v_cvt_pk_bf16_f32 v222, v200, v201
	v_cvt_pk_bf16_f32 v223, v202, v203
	global_store_dwordx4 v[146:147], v[220:223], off
	s_nop 1
	v_cvt_f32_i32_e32 v147, v79
	v_cvt_f32_i32_e32 v146, v78
	v_pk_mul_f32 v[148:149], v[188:189], v[130:131] op_sel_hi:[0,1]
	v_pk_mul_f32 v[148:149], v[148:149], v[146:147]
	v_mul_f32_e32 v146, 0xbfb8aa3b, v148
	v_exp_f32_e32 v146, v146
	v_mul_f32_e32 v147, v219, v148
	v_add_f32_e32 v146, 1.0, v146
	v_rcp_f32_e32 v146, v146
	s_nop 0
	v_mul_f32_e32 v148, v147, v146
	v_cvt_f32_i32_e32 v147, v81
	v_cvt_f32_i32_e32 v146, v80
	v_mov_b32_e32 v189, v188
	v_pk_mul_f32 v[198:199], v[188:189], v[132:133] op_sel_hi:[0,1]
	v_pk_mul_f32 v[198:199], v[198:199], v[146:147]
	v_mul_f32_e32 v146, 0xbfb8aa3b, v149
	v_exp_f32_e32 v146, v146
	v_mul_f32_e32 v147, v219, v149
	v_add_f32_e32 v146, 1.0, v146
	v_rcp_f32_e32 v146, v146
	s_nop 0
	v_mul_f32_e32 v149, v147, v146
	v_mul_f32_e32 v146, 0xbfb8aa3b, v198
	v_exp_f32_e32 v146, v146
	v_mul_f32_e32 v147, v219, v198
	v_add_f32_e32 v146, 1.0, v146
	v_rcp_f32_e32 v146, v146
	s_nop 0
	v_mul_f32_e32 v198, v147, v146
	v_mul_f32_e32 v146, 0xbfb8aa3b, v199
	v_exp_f32_e32 v146, v146
	v_mul_f32_e32 v147, v219, v199
	v_add_f32_e32 v146, 1.0, v146
	v_rcp_f32_e32 v146, v146
	s_nop 0
	v_mul_f32_e32 v199, v147, v146
	v_cvt_f32_i32_e32 v147, v75
	v_cvt_f32_i32_e32 v146, v74
	v_pk_mul_f32 v[200:201], v[188:189], v[126:127]
	v_pk_mul_f32 v[200:201], v[200:201], v[146:147]
	v_mul_f32_e32 v146, 0xbfb8aa3b, v200
	v_exp_f32_e32 v146, v146
	v_mul_f32_e32 v147, v219, v200
	v_add_f32_e32 v146, 1.0, v146
	v_rcp_f32_e32 v146, v146
	s_nop 0
	v_mul_f32_e32 v200, v147, v146
	v_cvt_f32_i32_e32 v147, v77
	v_cvt_f32_i32_e32 v146, v76
	v_mov_b32_e32 v202, v188
	v_mov_b32_e32 v203, v188
	v_pk_mul_f32 v[202:203], v[202:203], v[128:129]
	v_pk_mul_f32 v[202:203], v[202:203], v[146:147]
	v_mul_f32_e32 v146, 0xbfb8aa3b, v201
	v_exp_f32_e32 v146, v146
	v_mul_f32_e32 v147, v219, v201
	v_add_f32_e32 v146, 1.0, v146
	v_rcp_f32_e32 v146, v146
	s_nop 0
	v_mul_f32_e32 v201, v147, v146
	v_mul_f32_e32 v146, 0xbfb8aa3b, v202
	v_exp_f32_e32 v146, v146
	v_mul_f32_e32 v147, v219, v202
	v_add_f32_e32 v146, 1.0, v146
	v_rcp_f32_e32 v146, v146
	s_nop 0
	v_mul_f32_e32 v202, v147, v146
	v_mul_f32_e32 v146, 0xbfb8aa3b, v203
	v_exp_f32_e32 v146, v146
	v_mul_f32_e32 v147, v219, v203
	v_add_f32_e32 v146, 1.0, v146
	v_rcp_f32_e32 v146, v146
	s_nop 0
	v_mul_f32_e32 v203, v147, v146
	v_or_b32_e32 v146, 48, v178
	v_mov_b32_e32 v147, v179
	v_cvt_pk_bf16_f32 v220, v148, v149
	v_lshl_add_u64 v[148:149], v[146:147], 0, s[16:17]
	v_lshlrev_b64 v[148:149], 8, v[148:149]
	v_lshl_add_u64 v[148:149], v[196:197], 0, v[148:149]
	v_cvt_pk_bf16_f32 v221, v198, v199
	v_cvt_pk_bf16_f32 v222, v200, v201
	v_cvt_pk_bf16_f32 v223, v202, v203
	global_store_dwordx4 v[148:149], v[220:223], off
	s_nop 1
	v_cvt_f32_i32_e32 v149, v71
	v_cvt_f32_i32_e32 v148, v70
	v_pk_mul_f32 v[198:199], v[188:189], v[110:111]
	v_pk_mul_f32 v[148:149], v[198:199], v[148:149]
	v_mul_f32_e32 v158, 0xbfb8aa3b, v148
	v_exp_f32_e32 v158, v158
	v_mul_f32_e32 v148, v219, v148
	v_add_f32_e32 v158, 1.0, v158
	v_rcp_f32_e32 v158, v158
	s_nop 0
	v_mul_f32_e32 v148, v148, v158
	v_cvt_f32_i32_e32 v199, v73
	v_cvt_f32_i32_e32 v198, v72
	v_mov_b32_e32 v200, v188
	v_mov_b32_e32 v201, v188
	v_pk_mul_f32 v[200:201], v[200:201], v[112:113]
	v_pk_mul_f32 v[198:199], v[200:201], v[198:199]
	v_mul_f32_e32 v158, 0xbfb8aa3b, v149
	v_exp_f32_e32 v158, v158
	v_mul_f32_e32 v149, v219, v149
	v_add_f32_e32 v158, 1.0, v158
	v_rcp_f32_e32 v158, v158
	s_nop 0
	v_mul_f32_e32 v149, v149, v158
	v_mul_f32_e32 v158, 0xbfb8aa3b, v198
	v_exp_f32_e32 v158, v158
	v_mul_f32_e32 v181, v219, v198
	v_add_f32_e32 v158, 1.0, v158
	v_rcp_f32_e32 v158, v158
	s_nop 0
	v_mul_f32_e32 v198, v181, v158
	v_mul_f32_e32 v158, 0xbfb8aa3b, v199
	v_exp_f32_e32 v158, v158
	v_mul_f32_e32 v181, v219, v199
	v_add_f32_e32 v158, 1.0, v158
	v_rcp_f32_e32 v158, v158
	s_nop 0
	v_mul_f32_e32 v199, v181, v158
	v_cvt_f32_i32_e32 v201, v67
	v_cvt_f32_i32_e32 v200, v66
	v_pk_mul_f32 v[202:203], v[188:189], v[106:107]
	v_pk_mul_f32 v[200:201], v[202:203], v[200:201]
	v_mul_f32_e32 v158, 0xbfb8aa3b, v200
	v_exp_f32_e32 v158, v158
	v_mul_f32_e32 v181, v219, v200
	v_add_f32_e32 v158, 1.0, v158
	v_rcp_f32_e32 v158, v158
	s_nop 0
	v_mul_f32_e32 v200, v181, v158
	v_cvt_f32_i32_e32 v203, v69
	v_cvt_f32_i32_e32 v202, v68
	v_mov_b32_e32 v189, v188
	v_pk_mul_f32 v[220:221], v[188:189], v[108:109]
	v_pk_mul_f32 v[202:203], v[220:221], v[202:203]
	v_mul_f32_e32 v158, 0xbfb8aa3b, v201
	v_exp_f32_e32 v158, v158
	v_mul_f32_e32 v181, v219, v201
	v_add_f32_e32 v158, 1.0, v158
	v_rcp_f32_e32 v158, v158
	s_nop 0
	v_mul_f32_e32 v201, v181, v158
	v_mul_f32_e32 v158, 0xbfb8aa3b, v202
	v_exp_f32_e32 v158, v158
	v_mul_f32_e32 v181, v219, v202
	v_add_f32_e32 v158, 1.0, v158
	v_rcp_f32_e32 v158, v158
	s_nop 0
	v_mul_f32_e32 v202, v181, v158
	v_mul_f32_e32 v158, 0xbfb8aa3b, v203
	v_exp_f32_e32 v158, v158
	v_mul_f32_e32 v181, v219, v203
	v_add_f32_e32 v158, 1.0, v158
	v_rcp_f32_e32 v158, v158
	s_nop 0
	v_mul_f32_e32 v203, v181, v158
	v_lshl_add_u64 v[146:147], v[146:147], 0, s[10:11]
	v_lshlrev_b64 v[146:147], 8, v[146:147]
	v_lshl_add_u64 v[146:147], v[196:197], 0, v[146:147]
	v_cvt_pk_bf16_f32 v220, v148, v149
	v_cvt_pk_bf16_f32 v221, v198, v199
	v_cvt_pk_bf16_f32 v222, v200, v201
	v_cvt_pk_bf16_f32 v223, v202, v203
	global_store_dwordx4 v[146:147], v[220:223], off
	s_nop 1
	v_cvt_f32_i32_e32 v147, v63
	v_cvt_f32_i32_e32 v146, v62
	v_pk_mul_f32 v[148:149], v[186:187], v[130:131] op_sel_hi:[0,1]
	v_pk_mul_f32 v[148:149], v[148:149], v[146:147]
	v_mul_f32_e32 v146, 0xbfb8aa3b, v148
	v_exp_f32_e32 v146, v146
	v_mul_f32_e32 v147, v219, v148
	v_add_f32_e32 v146, 1.0, v146
	v_rcp_f32_e32 v146, v146
	s_nop 0
	v_mul_f32_e32 v148, v147, v146
	v_cvt_f32_i32_e32 v147, v65
	v_cvt_f32_i32_e32 v146, v64
	v_mov_b32_e32 v187, v186
	v_pk_mul_f32 v[198:199], v[186:187], v[132:133] op_sel_hi:[0,1]
	v_pk_mul_f32 v[198:199], v[198:199], v[146:147]
	v_mul_f32_e32 v146, 0xbfb8aa3b, v149
	v_exp_f32_e32 v146, v146
	v_mul_f32_e32 v147, v219, v149
	v_add_f32_e32 v146, 1.0, v146
	v_rcp_f32_e32 v146, v146
	s_nop 0
	v_mul_f32_e32 v149, v147, v146
	v_mul_f32_e32 v146, 0xbfb8aa3b, v198
	v_exp_f32_e32 v146, v146
	v_mul_f32_e32 v147, v219, v198
	v_add_f32_e32 v146, 1.0, v146
	v_rcp_f32_e32 v146, v146
	s_nop 0
	v_mul_f32_e32 v198, v147, v146
	v_mul_f32_e32 v146, 0xbfb8aa3b, v199
	v_exp_f32_e32 v146, v146
	v_mul_f32_e32 v147, v219, v199
	v_add_f32_e32 v146, 1.0, v146
	v_rcp_f32_e32 v146, v146
	s_nop 0
	v_mul_f32_e32 v199, v147, v146
	v_cvt_f32_i32_e32 v147, v59
	v_cvt_f32_i32_e32 v146, v58
	v_pk_mul_f32 v[200:201], v[186:187], v[126:127]
	v_pk_mul_f32 v[200:201], v[200:201], v[146:147]
	v_mul_f32_e32 v146, 0xbfb8aa3b, v200
	v_exp_f32_e32 v146, v146
	v_mul_f32_e32 v147, v219, v200
	v_add_f32_e32 v146, 1.0, v146
	v_rcp_f32_e32 v146, v146
	s_nop 0
	v_mul_f32_e32 v200, v147, v146
	v_cvt_f32_i32_e32 v147, v61
	v_cvt_f32_i32_e32 v146, v60
	v_mov_b32_e32 v202, v186
	v_mov_b32_e32 v203, v186
	v_pk_mul_f32 v[202:203], v[202:203], v[128:129]
	v_pk_mul_f32 v[202:203], v[202:203], v[146:147]
	v_mul_f32_e32 v146, 0xbfb8aa3b, v201
	v_exp_f32_e32 v146, v146
	v_mul_f32_e32 v147, v219, v201
	v_add_f32_e32 v146, 1.0, v146
	v_rcp_f32_e32 v146, v146
	s_nop 0
	v_mul_f32_e32 v201, v147, v146
	v_mul_f32_e32 v146, 0xbfb8aa3b, v202
	v_exp_f32_e32 v146, v146
	v_mul_f32_e32 v147, v219, v202
	v_add_f32_e32 v146, 1.0, v146
	v_rcp_f32_e32 v146, v146
	s_nop 0
	v_mul_f32_e32 v202, v147, v146
	v_mul_f32_e32 v146, 0xbfb8aa3b, v203
	v_exp_f32_e32 v146, v146
	v_mul_f32_e32 v147, v219, v203
	v_add_f32_e32 v146, 1.0, v146
	v_rcp_f32_e32 v146, v146
	s_nop 0
	v_mul_f32_e32 v203, v147, v146
	v_lshl_add_u64 v[146:147], v[178:179], 0, s[34:35]
	v_cvt_pk_bf16_f32 v220, v148, v149
	v_lshl_add_u64 v[148:149], v[146:147], 0, s[16:17]
	v_lshlrev_b64 v[148:149], 8, v[148:149]
	v_lshl_add_u64 v[148:149], v[196:197], 0, v[148:149]
	v_cvt_pk_bf16_f32 v221, v198, v199
	v_cvt_pk_bf16_f32 v222, v200, v201
	v_cvt_pk_bf16_f32 v223, v202, v203
	global_store_dwordx4 v[148:149], v[220:223], off
	s_nop 1
	v_cvt_f32_i32_e32 v149, v55
	v_cvt_f32_i32_e32 v148, v54
	v_pk_mul_f32 v[198:199], v[186:187], v[110:111]
	v_pk_mul_f32 v[148:149], v[198:199], v[148:149]
	v_mul_f32_e32 v158, 0xbfb8aa3b, v148
	v_exp_f32_e32 v158, v158
	v_mul_f32_e32 v148, v219, v148
	v_add_f32_e32 v158, 1.0, v158
	v_rcp_f32_e32 v158, v158
	s_nop 0
	v_mul_f32_e32 v148, v148, v158
	v_cvt_f32_i32_e32 v199, v57
	v_cvt_f32_i32_e32 v198, v56
	v_mov_b32_e32 v200, v186
	v_mov_b32_e32 v201, v186
	v_pk_mul_f32 v[200:201], v[200:201], v[112:113]
	v_pk_mul_f32 v[198:199], v[200:201], v[198:199]
	v_mul_f32_e32 v158, 0xbfb8aa3b, v149
	v_exp_f32_e32 v158, v158
	v_mul_f32_e32 v149, v219, v149
	v_add_f32_e32 v158, 1.0, v158
	v_rcp_f32_e32 v158, v158
	s_nop 0
	v_mul_f32_e32 v149, v149, v158
	v_mul_f32_e32 v158, 0xbfb8aa3b, v198
	v_exp_f32_e32 v158, v158
	v_mul_f32_e32 v181, v219, v198
	v_add_f32_e32 v158, 1.0, v158
	v_rcp_f32_e32 v158, v158
	s_nop 0
	v_mul_f32_e32 v198, v181, v158
	v_mul_f32_e32 v158, 0xbfb8aa3b, v199
	v_exp_f32_e32 v158, v158
	v_mul_f32_e32 v181, v219, v199
	v_add_f32_e32 v158, 1.0, v158
	v_rcp_f32_e32 v158, v158
	s_nop 0
	v_mul_f32_e32 v199, v181, v158
	v_cvt_f32_i32_e32 v201, v51
	v_cvt_f32_i32_e32 v200, v50
	v_pk_mul_f32 v[202:203], v[186:187], v[106:107]
	v_pk_mul_f32 v[200:201], v[202:203], v[200:201]
	v_mul_f32_e32 v158, 0xbfb8aa3b, v200
	v_exp_f32_e32 v158, v158
	v_mul_f32_e32 v181, v219, v200
	v_add_f32_e32 v158, 1.0, v158
	v_rcp_f32_e32 v158, v158
	s_nop 0
	v_mul_f32_e32 v200, v181, v158
	v_cvt_f32_i32_e32 v203, v53
	v_cvt_f32_i32_e32 v202, v52
	v_mov_b32_e32 v187, v186
	v_pk_mul_f32 v[220:221], v[186:187], v[108:109]
	v_pk_mul_f32 v[202:203], v[220:221], v[202:203]
	v_mul_f32_e32 v158, 0xbfb8aa3b, v201
	v_exp_f32_e32 v158, v158
	v_mul_f32_e32 v181, v219, v201
	v_add_f32_e32 v158, 1.0, v158
	v_rcp_f32_e32 v158, v158
	s_nop 0
	v_mul_f32_e32 v201, v181, v158
	v_mul_f32_e32 v158, 0xbfb8aa3b, v202
	v_exp_f32_e32 v158, v158
	v_mul_f32_e32 v181, v219, v202
	v_add_f32_e32 v158, 1.0, v158
	v_rcp_f32_e32 v158, v158
	s_nop 0
	v_mul_f32_e32 v202, v181, v158
	v_mul_f32_e32 v158, 0xbfb8aa3b, v203
	v_exp_f32_e32 v158, v158
	v_mul_f32_e32 v181, v219, v203
	v_add_f32_e32 v158, 1.0, v158
	v_rcp_f32_e32 v158, v158
	s_nop 0
	v_mul_f32_e32 v203, v181, v158
	v_lshl_add_u64 v[146:147], v[146:147], 0, s[10:11]
	v_lshlrev_b64 v[146:147], 8, v[146:147]
	v_lshl_add_u64 v[146:147], v[196:197], 0, v[146:147]
	v_cvt_pk_bf16_f32 v220, v148, v149
	v_cvt_pk_bf16_f32 v221, v198, v199
	v_cvt_pk_bf16_f32 v222, v200, v201
	v_cvt_pk_bf16_f32 v223, v202, v203
	global_store_dwordx4 v[146:147], v[220:223], off
	s_nop 1
	v_cvt_f32_i32_e32 v147, v47
	v_cvt_f32_i32_e32 v146, v46
	v_pk_mul_f32 v[148:149], v[184:185], v[130:131] op_sel_hi:[0,1]
	v_pk_mul_f32 v[148:149], v[148:149], v[146:147]
	v_mul_f32_e32 v146, 0xbfb8aa3b, v148
	v_exp_f32_e32 v146, v146
	v_mul_f32_e32 v147, v219, v148
	v_add_f32_e32 v146, 1.0, v146
	v_rcp_f32_e32 v146, v146
	s_nop 0
	v_mul_f32_e32 v148, v147, v146
	v_cvt_f32_i32_e32 v147, v49
	v_cvt_f32_i32_e32 v146, v48
	v_mov_b32_e32 v185, v184
	v_pk_mul_f32 v[198:199], v[184:185], v[132:133] op_sel_hi:[0,1]
	v_pk_mul_f32 v[198:199], v[198:199], v[146:147]
	v_mul_f32_e32 v146, 0xbfb8aa3b, v149
	v_exp_f32_e32 v146, v146
	v_mul_f32_e32 v147, v219, v149
	v_add_f32_e32 v146, 1.0, v146
	v_rcp_f32_e32 v146, v146
	s_nop 0
	v_mul_f32_e32 v149, v147, v146
	v_mul_f32_e32 v146, 0xbfb8aa3b, v198
	v_exp_f32_e32 v146, v146
	v_mul_f32_e32 v147, v219, v198
	v_add_f32_e32 v146, 1.0, v146
	v_rcp_f32_e32 v146, v146
	s_nop 0
	v_mul_f32_e32 v198, v147, v146
	v_mul_f32_e32 v146, 0xbfb8aa3b, v199
	v_exp_f32_e32 v146, v146
	v_mul_f32_e32 v147, v219, v199
	v_add_f32_e32 v146, 1.0, v146
	v_rcp_f32_e32 v146, v146
	s_nop 0
	v_mul_f32_e32 v199, v147, v146
	v_cvt_f32_i32_e32 v147, v43
	v_cvt_f32_i32_e32 v146, v42
	v_pk_mul_f32 v[200:201], v[184:185], v[126:127]
	v_pk_mul_f32 v[200:201], v[200:201], v[146:147]
	v_mul_f32_e32 v146, 0xbfb8aa3b, v200
	v_exp_f32_e32 v146, v146
	v_mul_f32_e32 v147, v219, v200
	v_add_f32_e32 v146, 1.0, v146
	v_rcp_f32_e32 v146, v146
	s_nop 0
	v_mul_f32_e32 v200, v147, v146
	v_cvt_f32_i32_e32 v147, v45
	v_cvt_f32_i32_e32 v146, v44
	v_mov_b32_e32 v202, v184
	v_mov_b32_e32 v203, v184
	v_pk_mul_f32 v[202:203], v[202:203], v[128:129]
	v_pk_mul_f32 v[202:203], v[202:203], v[146:147]
	v_mul_f32_e32 v146, 0xbfb8aa3b, v201
	v_exp_f32_e32 v146, v146
	v_mul_f32_e32 v147, v219, v201
	v_add_f32_e32 v146, 1.0, v146
	v_rcp_f32_e32 v146, v146
	s_nop 0
	v_mul_f32_e32 v201, v147, v146
	v_mul_f32_e32 v146, 0xbfb8aa3b, v202
	v_exp_f32_e32 v146, v146
	v_mul_f32_e32 v147, v219, v202
	v_add_f32_e32 v146, 1.0, v146
	v_rcp_f32_e32 v146, v146
	s_nop 0
	v_mul_f32_e32 v202, v147, v146
	v_mul_f32_e32 v146, 0xbfb8aa3b, v203
	v_exp_f32_e32 v146, v146
	v_mul_f32_e32 v147, v219, v203
	v_add_f32_e32 v146, 1.0, v146
	v_rcp_f32_e32 v146, v146
	s_nop 0
	v_mul_f32_e32 v203, v147, v146
	v_lshl_add_u64 v[146:147], v[178:179], 0, s[42:43]
	v_cvt_pk_bf16_f32 v220, v148, v149
	v_lshl_add_u64 v[148:149], v[146:147], 0, s[16:17]
	v_lshlrev_b64 v[148:149], 8, v[148:149]
	v_lshl_add_u64 v[148:149], v[196:197], 0, v[148:149]
	v_cvt_pk_bf16_f32 v221, v198, v199
	v_cvt_pk_bf16_f32 v222, v200, v201
	v_cvt_pk_bf16_f32 v223, v202, v203
	global_store_dwordx4 v[148:149], v[220:223], off
	s_nop 1
	v_cvt_f32_i32_e32 v149, v39
	v_cvt_f32_i32_e32 v148, v38
	v_pk_mul_f32 v[198:199], v[184:185], v[110:111]
	v_pk_mul_f32 v[148:149], v[198:199], v[148:149]
	v_mul_f32_e32 v158, 0xbfb8aa3b, v148
	v_exp_f32_e32 v158, v158
	v_mul_f32_e32 v148, v219, v148
	v_add_f32_e32 v158, 1.0, v158
	v_rcp_f32_e32 v158, v158
	s_nop 0
	v_mul_f32_e32 v148, v148, v158
	v_cvt_f32_i32_e32 v199, v41
	v_cvt_f32_i32_e32 v198, v40
	v_mov_b32_e32 v200, v184
	v_mov_b32_e32 v201, v184
	v_pk_mul_f32 v[200:201], v[200:201], v[112:113]
	v_pk_mul_f32 v[198:199], v[200:201], v[198:199]
	v_mul_f32_e32 v158, 0xbfb8aa3b, v149
	v_exp_f32_e32 v158, v158
	v_mul_f32_e32 v149, v219, v149
	v_add_f32_e32 v158, 1.0, v158
	v_rcp_f32_e32 v158, v158
	s_nop 0
	v_mul_f32_e32 v149, v149, v158
	v_mul_f32_e32 v158, 0xbfb8aa3b, v198
	v_exp_f32_e32 v158, v158
	v_mul_f32_e32 v181, v219, v198
	v_add_f32_e32 v158, 1.0, v158
	v_rcp_f32_e32 v158, v158
	s_nop 0
	v_mul_f32_e32 v198, v181, v158
	v_mul_f32_e32 v158, 0xbfb8aa3b, v199
	v_exp_f32_e32 v158, v158
	v_mul_f32_e32 v181, v219, v199
	v_add_f32_e32 v158, 1.0, v158
	v_rcp_f32_e32 v158, v158
	s_nop 0
	v_mul_f32_e32 v199, v181, v158
	v_cvt_f32_i32_e32 v201, v35
	v_cvt_f32_i32_e32 v200, v34
	v_pk_mul_f32 v[202:203], v[184:185], v[106:107]
	v_pk_mul_f32 v[200:201], v[202:203], v[200:201]
	v_mul_f32_e32 v158, 0xbfb8aa3b, v200
	v_exp_f32_e32 v158, v158
	v_mul_f32_e32 v181, v219, v200
	v_add_f32_e32 v158, 1.0, v158
	v_rcp_f32_e32 v158, v158
	s_nop 0
	v_mul_f32_e32 v200, v181, v158
	v_cvt_f32_i32_e32 v203, v37
	v_cvt_f32_i32_e32 v202, v36
	v_mov_b32_e32 v185, v184
	v_pk_mul_f32 v[220:221], v[184:185], v[108:109]
	v_pk_mul_f32 v[202:203], v[220:221], v[202:203]
	v_mul_f32_e32 v158, 0xbfb8aa3b, v201
	v_exp_f32_e32 v158, v158
	v_mul_f32_e32 v181, v219, v201
	v_add_f32_e32 v158, 1.0, v158
	v_rcp_f32_e32 v158, v158
	s_nop 0
	v_mul_f32_e32 v201, v181, v158
	v_mul_f32_e32 v158, 0xbfb8aa3b, v202
	v_exp_f32_e32 v158, v158
	v_mul_f32_e32 v181, v219, v202
	v_add_f32_e32 v158, 1.0, v158
	v_rcp_f32_e32 v158, v158
	s_nop 0
	v_mul_f32_e32 v202, v181, v158
	v_mul_f32_e32 v158, 0xbfb8aa3b, v203
	v_exp_f32_e32 v158, v158
	v_mul_f32_e32 v181, v219, v203
	v_add_f32_e32 v158, 1.0, v158
	v_rcp_f32_e32 v158, v158
	s_nop 0
	v_mul_f32_e32 v203, v181, v158
	v_lshl_add_u64 v[146:147], v[146:147], 0, s[10:11]
	v_lshlrev_b64 v[146:147], 8, v[146:147]
	v_lshl_add_u64 v[146:147], v[196:197], 0, v[146:147]
	v_cvt_pk_bf16_f32 v220, v148, v149
	v_cvt_pk_bf16_f32 v221, v198, v199
	v_cvt_pk_bf16_f32 v222, v200, v201
	v_cvt_pk_bf16_f32 v223, v202, v203
	global_store_dwordx4 v[146:147], v[220:223], off
	s_nop 1
	v_cvt_f32_i32_e32 v147, v31
	v_cvt_f32_i32_e32 v146, v30
	v_pk_mul_f32 v[148:149], v[182:183], v[130:131] op_sel_hi:[0,1]
	v_pk_mul_f32 v[148:149], v[148:149], v[146:147]
	v_mul_f32_e32 v146, 0xbfb8aa3b, v148
	v_exp_f32_e32 v146, v146
	v_mul_f32_e32 v147, v219, v148
	v_add_f32_e32 v146, 1.0, v146
	v_rcp_f32_e32 v146, v146
	s_nop 0
	v_mul_f32_e32 v148, v147, v146
	v_cvt_f32_i32_e32 v147, v33
	v_cvt_f32_i32_e32 v146, v32
	v_mov_b32_e32 v183, v182
	v_pk_mul_f32 v[198:199], v[182:183], v[132:133] op_sel_hi:[0,1]
	v_pk_mul_f32 v[198:199], v[198:199], v[146:147]
	v_mul_f32_e32 v146, 0xbfb8aa3b, v149
	v_exp_f32_e32 v146, v146
	v_mul_f32_e32 v147, v219, v149
	v_add_f32_e32 v146, 1.0, v146
	v_rcp_f32_e32 v146, v146
	s_nop 0
	v_mul_f32_e32 v149, v147, v146
	v_mul_f32_e32 v146, 0xbfb8aa3b, v198
	v_exp_f32_e32 v146, v146
	v_mul_f32_e32 v147, v219, v198
	v_add_f32_e32 v146, 1.0, v146
	v_rcp_f32_e32 v146, v146
	s_nop 0
	v_mul_f32_e32 v198, v147, v146
	v_mul_f32_e32 v146, 0xbfb8aa3b, v199
	v_exp_f32_e32 v146, v146
	v_mul_f32_e32 v147, v219, v199
	v_add_f32_e32 v146, 1.0, v146
	v_rcp_f32_e32 v146, v146
	s_nop 0
	v_mul_f32_e32 v199, v147, v146
	v_cvt_f32_i32_e32 v147, v27
	v_cvt_f32_i32_e32 v146, v26
	v_pk_mul_f32 v[200:201], v[182:183], v[126:127]
	v_pk_mul_f32 v[200:201], v[200:201], v[146:147]
	v_mul_f32_e32 v146, 0xbfb8aa3b, v200
	v_exp_f32_e32 v146, v146
	v_mul_f32_e32 v147, v219, v200
	v_add_f32_e32 v146, 1.0, v146
	v_rcp_f32_e32 v146, v146
	s_nop 0
	v_mul_f32_e32 v200, v147, v146
	v_cvt_f32_i32_e32 v147, v29
	v_cvt_f32_i32_e32 v146, v28
	v_mov_b32_e32 v202, v182
	v_mov_b32_e32 v203, v182
	v_pk_mul_f32 v[202:203], v[202:203], v[128:129]
	v_pk_mul_f32 v[202:203], v[202:203], v[146:147]
	v_mul_f32_e32 v146, 0xbfb8aa3b, v201
	v_exp_f32_e32 v146, v146
	v_mul_f32_e32 v147, v219, v201
	v_add_f32_e32 v146, 1.0, v146
	v_rcp_f32_e32 v146, v146
	s_nop 0
	v_mul_f32_e32 v201, v147, v146
	v_mul_f32_e32 v146, 0xbfb8aa3b, v202
	v_exp_f32_e32 v146, v146
	v_mul_f32_e32 v147, v219, v202
	v_add_f32_e32 v146, 1.0, v146
	v_rcp_f32_e32 v146, v146
	s_nop 0
	v_mul_f32_e32 v202, v147, v146
	v_mul_f32_e32 v146, 0xbfb8aa3b, v203
	v_exp_f32_e32 v146, v146
	v_mul_f32_e32 v147, v219, v203
	v_add_f32_e32 v146, 1.0, v146
	v_rcp_f32_e32 v146, v146
	s_nop 0
	v_mul_f32_e32 v203, v147, v146
	v_lshl_add_u64 v[146:147], v[178:179], 0, s[52:53]
	v_cvt_pk_bf16_f32 v220, v148, v149
	v_lshl_add_u64 v[148:149], v[146:147], 0, s[16:17]
	v_lshlrev_b64 v[148:149], 8, v[148:149]
	v_lshl_add_u64 v[148:149], v[196:197], 0, v[148:149]
	v_cvt_pk_bf16_f32 v221, v198, v199
	v_cvt_pk_bf16_f32 v222, v200, v201
	v_cvt_pk_bf16_f32 v223, v202, v203
	global_store_dwordx4 v[148:149], v[220:223], off
	s_nop 1
	v_cvt_f32_i32_e32 v149, v23
	v_cvt_f32_i32_e32 v148, v22
	v_pk_mul_f32 v[198:199], v[182:183], v[110:111]
	v_pk_mul_f32 v[148:149], v[198:199], v[148:149]
	v_mul_f32_e32 v158, 0xbfb8aa3b, v148
	v_exp_f32_e32 v158, v158
	v_mul_f32_e32 v148, v219, v148
	v_add_f32_e32 v158, 1.0, v158
	v_rcp_f32_e32 v158, v158
	s_nop 0
	v_mul_f32_e32 v148, v148, v158
	v_cvt_f32_i32_e32 v199, v25
	v_cvt_f32_i32_e32 v198, v24
	v_mov_b32_e32 v200, v182
	v_mov_b32_e32 v201, v182
	v_pk_mul_f32 v[200:201], v[200:201], v[112:113]
	v_pk_mul_f32 v[198:199], v[200:201], v[198:199]
	v_mul_f32_e32 v158, 0xbfb8aa3b, v149
	v_exp_f32_e32 v158, v158
	v_mul_f32_e32 v149, v219, v149
	v_add_f32_e32 v158, 1.0, v158
	v_rcp_f32_e32 v158, v158
	s_nop 0
	v_mul_f32_e32 v149, v149, v158
	v_mul_f32_e32 v158, 0xbfb8aa3b, v198
	v_exp_f32_e32 v158, v158
	v_mul_f32_e32 v181, v219, v198
	v_add_f32_e32 v158, 1.0, v158
	v_rcp_f32_e32 v158, v158
	s_nop 0
	v_mul_f32_e32 v198, v181, v158
	v_mul_f32_e32 v158, 0xbfb8aa3b, v199
	v_exp_f32_e32 v158, v158
	v_mul_f32_e32 v181, v219, v199
	v_add_f32_e32 v158, 1.0, v158
	v_rcp_f32_e32 v158, v158
	s_nop 0
	v_mul_f32_e32 v199, v181, v158
	v_cvt_f32_i32_e32 v201, v19
	v_cvt_f32_i32_e32 v200, v18
	v_pk_mul_f32 v[202:203], v[182:183], v[106:107]
	v_pk_mul_f32 v[200:201], v[202:203], v[200:201]
	v_mul_f32_e32 v158, 0xbfb8aa3b, v200
	v_exp_f32_e32 v158, v158
	v_mul_f32_e32 v181, v219, v200
	v_add_f32_e32 v158, 1.0, v158
	v_rcp_f32_e32 v158, v158
	s_nop 0
	v_mul_f32_e32 v200, v181, v158
	v_cvt_f32_i32_e32 v203, v21
	v_cvt_f32_i32_e32 v202, v20
	v_mov_b32_e32 v183, v182
	v_pk_mul_f32 v[220:221], v[182:183], v[108:109]
	v_pk_mul_f32 v[202:203], v[220:221], v[202:203]
	v_mul_f32_e32 v158, 0xbfb8aa3b, v201
	v_exp_f32_e32 v158, v158
	v_mul_f32_e32 v181, v219, v201
	v_add_f32_e32 v158, 1.0, v158
	v_rcp_f32_e32 v158, v158
	s_nop 0
	v_mul_f32_e32 v201, v181, v158
	v_mul_f32_e32 v158, 0xbfb8aa3b, v202
	v_exp_f32_e32 v158, v158
	v_mul_f32_e32 v181, v219, v202
	v_add_f32_e32 v158, 1.0, v158
	v_rcp_f32_e32 v158, v158
	s_nop 0
	v_mul_f32_e32 v202, v181, v158
	v_mul_f32_e32 v158, 0xbfb8aa3b, v203
	v_exp_f32_e32 v158, v158
	v_mul_f32_e32 v181, v219, v203
	v_add_f32_e32 v158, 1.0, v158
	v_rcp_f32_e32 v158, v158
	s_nop 0
	v_mul_f32_e32 v203, v181, v158
	v_lshl_add_u64 v[146:147], v[146:147], 0, s[10:11]
	v_lshlrev_b64 v[146:147], 8, v[146:147]
	v_lshl_add_u64 v[146:147], v[196:197], 0, v[146:147]
	v_cvt_pk_bf16_f32 v220, v148, v149
	v_cvt_pk_bf16_f32 v221, v198, v199
	v_cvt_pk_bf16_f32 v222, v200, v201
	v_cvt_pk_bf16_f32 v223, v202, v203
	global_store_dwordx4 v[146:147], v[220:223], off
	s_nop 1
	v_cvt_f32_i32_e32 v147, v15
	v_cvt_f32_i32_e32 v146, v14
	v_pk_mul_f32 v[148:149], v[130:131], v[180:181] op_sel_hi:[1,0]
	v_pk_mul_f32 v[146:147], v[148:149], v[146:147]
	v_mul_f32_e32 v148, 0xbfb8aa3b, v146
	v_exp_f32_e32 v148, v148
	v_mul_f32_e32 v146, v219, v146
	v_add_f32_e32 v148, 1.0, v148
	v_rcp_f32_e32 v148, v148
	s_nop 0
	v_mul_f32_e32 v146, v146, v148
	v_cvt_f32_i32_e32 v149, v17
	v_cvt_f32_i32_e32 v148, v16
	v_mov_b32_e32 v181, v180
	v_pk_mul_f32 v[198:199], v[132:133], v[180:181] op_sel_hi:[1,0]
	v_pk_mul_f32 v[148:149], v[198:199], v[148:149]
	v_mul_f32_e32 v158, 0xbfb8aa3b, v147
	v_exp_f32_e32 v158, v158
	v_mul_f32_e32 v147, v219, v147
	v_add_f32_e32 v158, 1.0, v158
	v_rcp_f32_e32 v158, v158
	s_nop 0
	v_mul_f32_e32 v147, v147, v158
	v_mul_f32_e32 v158, 0xbfb8aa3b, v148
	v_exp_f32_e32 v158, v158
	v_mul_f32_e32 v148, v219, v148
	v_add_f32_e32 v158, 1.0, v158
	v_rcp_f32_e32 v158, v158
	s_nop 0
	v_mul_f32_e32 v148, v148, v158
	v_mul_f32_e32 v158, 0xbfb8aa3b, v149
	v_exp_f32_e32 v158, v158
	v_mul_f32_e32 v149, v219, v149
	v_add_f32_e32 v158, 1.0, v158
	v_rcp_f32_e32 v158, v158
	s_nop 0
	v_mul_f32_e32 v149, v149, v158
	v_cvt_f32_i32_e32 v199, v11
	v_cvt_f32_i32_e32 v198, v10
	v_pk_mul_f32 v[200:201], v[180:181], v[126:127]
	v_pk_mul_f32 v[200:201], v[200:201], v[198:199]
	v_mul_f32_e32 v158, 0xbfb8aa3b, v200
	v_exp_f32_e32 v158, v158
	v_mul_f32_e32 v183, v219, v200
	v_add_f32_e32 v158, 1.0, v158
	v_rcp_f32_e32 v158, v158
	s_nop 0
	v_mul_f32_e32 v200, v183, v158
	v_cvt_f32_i32_e32 v199, v13
	v_cvt_f32_i32_e32 v198, v12
	v_mov_b32_e32 v202, v180
	v_mov_b32_e32 v203, v180
	v_pk_mul_f32 v[202:203], v[202:203], v[128:129]
	v_pk_mul_f32 v[202:203], v[202:203], v[198:199]
	v_mul_f32_e32 v158, 0xbfb8aa3b, v201
	v_exp_f32_e32 v158, v158
	v_mul_f32_e32 v183, v219, v201
	v_add_f32_e32 v158, 1.0, v158
	v_rcp_f32_e32 v158, v158
	s_nop 0
	v_mul_f32_e32 v201, v183, v158
	v_mul_f32_e32 v158, 0xbfb8aa3b, v202
	v_exp_f32_e32 v158, v158
	v_mul_f32_e32 v183, v219, v202
	v_add_f32_e32 v158, 1.0, v158
	v_rcp_f32_e32 v158, v158
	s_nop 0
	v_mul_f32_e32 v202, v183, v158
	v_mul_f32_e32 v158, 0xbfb8aa3b, v203
	v_exp_f32_e32 v158, v158
	v_mul_f32_e32 v183, v219, v203
	v_add_f32_e32 v158, 1.0, v158
	v_rcp_f32_e32 v158, v158
	s_nop 0
	v_mul_f32_e32 v203, v183, v158
	v_lshl_add_u64 v[198:199], v[178:179], 0, s[54:55]
	v_cvt_pk_bf16_f32 v146, v146, v147
	v_cvt_pk_bf16_f32 v147, v148, v149
	v_cvt_pk_bf16_f32 v148, v200, v201
	v_lshl_add_u64 v[200:201], v[198:199], 0, s[16:17]
	v_lshlrev_b64 v[200:201], 8, v[200:201]
	v_lshl_add_u64 v[200:201], v[196:197], 0, v[200:201]
	v_cvt_pk_bf16_f32 v149, v202, v203
	global_store_dwordx4 v[200:201], v[146:149], off
	s_nop 1
	v_cvt_f32_i32_e32 v147, v7
	v_cvt_f32_i32_e32 v146, v6
	v_pk_mul_f32 v[148:149], v[180:181], v[110:111]
	v_pk_mul_f32 v[146:147], v[148:149], v[146:147]
	v_mul_f32_e32 v148, 0xbfb8aa3b, v146
	v_exp_f32_e32 v148, v148
	v_mul_f32_e32 v146, v219, v146
	v_add_f32_e32 v148, 1.0, v148
	v_rcp_f32_e32 v148, v148
	s_nop 0
	v_mul_f32_e32 v146, v146, v148
	v_cvt_f32_i32_e32 v149, v9
	v_cvt_f32_i32_e32 v148, v8
	v_mov_b32_e32 v200, v180
	v_mov_b32_e32 v201, v180
	v_pk_mul_f32 v[200:201], v[200:201], v[112:113]
	v_pk_mul_f32 v[148:149], v[200:201], v[148:149]
	v_mul_f32_e32 v158, 0xbfb8aa3b, v147
	v_exp_f32_e32 v158, v158
	v_mul_f32_e32 v147, v219, v147
	v_add_f32_e32 v158, 1.0, v158
	v_rcp_f32_e32 v158, v158
	s_nop 0
	v_mul_f32_e32 v147, v147, v158
	v_mul_f32_e32 v158, 0xbfb8aa3b, v148
	v_exp_f32_e32 v158, v158
	v_mul_f32_e32 v148, v219, v148
	v_add_f32_e32 v158, 1.0, v158
	v_rcp_f32_e32 v158, v158
	s_nop 0
	v_mul_f32_e32 v148, v148, v158
	v_mul_f32_e32 v158, 0xbfb8aa3b, v149
	v_exp_f32_e32 v158, v158
	v_mul_f32_e32 v149, v219, v149
	v_add_f32_e32 v158, 1.0, v158
	v_rcp_f32_e32 v158, v158
	s_nop 0
	v_mul_f32_e32 v149, v149, v158
	v_cvt_f32_i32_e32 v201, v3
	v_cvt_f32_i32_e32 v200, v2
	v_pk_mul_f32 v[202:203], v[180:181], v[106:107]
	v_pk_mul_f32 v[200:201], v[202:203], v[200:201]
	v_mul_f32_e32 v158, 0xbfb8aa3b, v200
	v_exp_f32_e32 v158, v158
	v_mul_f32_e32 v181, v219, v200
	v_add_f32_e32 v158, 1.0, v158
	v_rcp_f32_e32 v158, v158
	s_nop 0
	v_mul_f32_e32 v200, v181, v158
	v_cvt_f32_i32_e32 v203, v5
	v_cvt_f32_i32_e32 v202, v4
	v_mov_b32_e32 v181, v180
	v_pk_mul_f32 v[220:221], v[180:181], v[108:109]
	v_pk_mul_f32 v[202:203], v[220:221], v[202:203]
	v_mul_f32_e32 v158, 0xbfb8aa3b, v201
	v_exp_f32_e32 v158, v158
	v_mul_f32_e32 v181, v219, v201
	v_add_f32_e32 v158, 1.0, v158
	v_rcp_f32_e32 v158, v158
	s_nop 0
	v_mul_f32_e32 v201, v181, v158
	v_mul_f32_e32 v158, 0xbfb8aa3b, v202
	v_exp_f32_e32 v158, v158
	v_mul_f32_e32 v181, v219, v202
	v_add_f32_e32 v158, 1.0, v158
	v_rcp_f32_e32 v158, v158
	s_nop 0
	v_mul_f32_e32 v202, v181, v158
	v_mul_f32_e32 v158, 0xbfb8aa3b, v203
	v_exp_f32_e32 v158, v158
	v_mul_f32_e32 v181, v219, v203
	v_add_f32_e32 v158, 1.0, v158
	v_rcp_f32_e32 v158, v158
	s_nop 0
	v_mul_f32_e32 v203, v181, v158
	v_cvt_pk_bf16_f32 v146, v146, v147
	v_cvt_pk_bf16_f32 v147, v148, v149
	v_cvt_pk_bf16_f32 v148, v200, v201
	v_cvt_pk_bf16_f32 v149, v202, v203
	v_lshl_add_u64 v[198:199], v[198:199], 0, s[10:11]
	s_branch .LBB0_354
.Lepi_t2:
	s_mov_b64 s[68:69], s[22:23]
	s_mov_b64 s[68:69], s[20:21]
	v_mov_b64_e32 v[196:197], v[166:167]
	s_cmp_eq_u32 s59, 3
	s_cselect_b64 s[10:11], -1, 0
	v_cvt_f32_i32_e32 v147, v143
	v_cvt_f32_i32_e32 v146, v142
	s_waitcnt vmcnt(0)
	v_pk_mul_f32 v[148:149], v[194:195], v[130:131] op_sel_hi:[0,1]
	v_cndmask_b32_e64 v219, 1.0, v217, s[10:11]
	v_pk_mul_f32 v[146:147], v[148:149], v[146:147]
	v_cvt_f32_i32_e32 v149, v145
	v_cvt_f32_i32_e32 v148, v144
	v_mov_b32_e32 v195, v194
	v_pk_mul_f32 v[196:197], v[194:195], v[132:133] op_sel_hi:[0,1]
	v_pk_mul_f32 v[148:149], v[196:197], v[148:149]
	v_cvt_f32_i32_e32 v197, v139
	v_cvt_f32_i32_e32 v196, v138
	v_pk_mul_f32 v[198:199], v[194:195], v[126:127]
	v_pk_mul_f32 v[198:199], v[198:199], v[196:197]
	v_cvt_f32_i32_e32 v197, v141
	v_cvt_f32_i32_e32 v196, v140
	v_mov_b32_e32 v200, v194
	v_mov_b32_e32 v201, v194
	v_pk_mul_f32 v[200:201], v[200:201], v[128:129]
	v_pk_mul_f32 v[200:201], v[200:201], v[196:197]
	s_lshl_b32 s16, s57, 13
	v_lshlrev_b32_e32 v158, 1, v162
	v_cvt_pk_bf16_f32 v146, v146, v147
	v_cvt_pk_bf16_f32 v147, v148, v149
	v_cvt_pk_bf16_f32 v148, v198, v199
	v_lshl_add_u64 v[198:199], v[178:179], 0, s[16:17]
	v_lshl_add_u64 v[196:197], s[68:69], 0, v[158:159]
	v_lshlrev_b64 v[198:199], 8, v[198:199]
	v_lshl_add_u64 v[198:199], v[196:197], 0, v[198:199]
	v_cvt_pk_bf16_f32 v149, v200, v201
	global_store_dwordx4 v[198:199], v[146:149], off
	s_nop 1
	v_cvt_f32_i32_e32 v147, v135
	v_cvt_f32_i32_e32 v146, v134
	v_pk_mul_f32 v[148:149], v[194:195], v[110:111]
	v_pk_mul_f32 v[146:147], v[148:149], v[146:147]
	v_cvt_f32_i32_e32 v149, v137
	v_cvt_f32_i32_e32 v148, v136
	v_mov_b32_e32 v198, v194
	v_mov_b32_e32 v199, v194
	v_pk_mul_f32 v[198:199], v[198:199], v[112:113]
	v_pk_mul_f32 v[148:149], v[198:199], v[148:149]
	v_cvt_f32_i32_e32 v199, v123
	v_cvt_f32_i32_e32 v198, v122
	v_pk_mul_f32 v[200:201], v[194:195], v[106:107]
	v_pk_mul_f32 v[198:199], v[200:201], v[198:199]
	v_cvt_f32_i32_e32 v201, v125
	v_cvt_f32_i32_e32 v200, v124
	v_mov_b32_e32 v195, v194
	v_pk_mul_f32 v[202:203], v[194:195], v[108:109]
	v_pk_mul_f32 v[200:201], v[202:203], v[200:201]
	s_or_b32 s10, s16, 0x2000
	s_mov_b32 s11, s17
	v_cvt_pk_bf16_f32 v146, v146, v147
	v_cvt_pk_bf16_f32 v147, v148, v149
	v_cvt_pk_bf16_f32 v148, v198, v199
	v_lshl_add_u64 v[198:199], v[178:179], 0, s[10:11]
	v_lshlrev_b64 v[198:199], 8, v[198:199]
	v_lshl_add_u64 v[198:199], v[196:197], 0, v[198:199]
	v_cvt_pk_bf16_f32 v149, v200, v201
	global_store_dwordx4 v[198:199], v[146:149], off
	s_nop 1
	v_cvt_f32_i32_e32 v147, v119
	v_cvt_f32_i32_e32 v146, v118
	v_pk_mul_f32 v[148:149], v[192:193], v[130:131] op_sel_hi:[0,1]
	v_pk_mul_f32 v[148:149], v[148:149], v[146:147]
	v_cvt_f32_i32_e32 v147, v121
	v_cvt_f32_i32_e32 v146, v120
	v_mov_b32_e32 v193, v192
	v_pk_mul_f32 v[198:199], v[192:193], v[132:133] op_sel_hi:[0,1]
	v_pk_mul_f32 v[198:199], v[198:199], v[146:147]
	v_cvt_f32_i32_e32 v147, v115
	v_cvt_f32_i32_e32 v146, v114
	v_pk_mul_f32 v[200:201], v[192:193], v[126:127]
	v_pk_mul_f32 v[200:201], v[200:201], v[146:147]
	v_cvt_f32_i32_e32 v147, v117
	v_cvt_f32_i32_e32 v146, v116
	v_mov_b32_e32 v202, v192
	v_mov_b32_e32 v203, v192
	v_pk_mul_f32 v[202:203], v[202:203], v[128:129]
	v_pk_mul_f32 v[202:203], v[202:203], v[146:147]
	v_or_b32_e32 v146, 16, v178
	v_mov_b32_e32 v147, v179
	v_cvt_pk_bf16_f32 v220, v148, v149
	v_lshl_add_u64 v[148:149], v[146:147], 0, s[16:17]
	v_lshlrev_b64 v[148:149], 8, v[148:149]
	v_lshl_add_u64 v[148:149], v[196:197], 0, v[148:149]
	v_cvt_pk_bf16_f32 v221, v198, v199
	v_cvt_pk_bf16_f32 v222, v200, v201
	v_cvt_pk_bf16_f32 v223, v202, v203
	global_store_dwordx4 v[148:149], v[220:223], off
	s_nop 1
	v_cvt_f32_i32_e32 v149, v103
	v_cvt_f32_i32_e32 v148, v102
	v_pk_mul_f32 v[198:199], v[192:193], v[110:111]
	v_pk_mul_f32 v[148:149], v[198:199], v[148:149]
	v_cvt_f32_i32_e32 v199, v105
	v_cvt_f32_i32_e32 v198, v104
	v_mov_b32_e32 v200, v192
	v_mov_b32_e32 v201, v192
	v_pk_mul_f32 v[200:201], v[200:201], v[112:113]
	v_pk_mul_f32 v[198:199], v[200:201], v[198:199]
	v_cvt_f32_i32_e32 v201, v99
	v_cvt_f32_i32_e32 v200, v98
	v_pk_mul_f32 v[202:203], v[192:193], v[106:107]
	v_pk_mul_f32 v[200:201], v[202:203], v[200:201]
	v_cvt_f32_i32_e32 v203, v101
	v_cvt_f32_i32_e32 v202, v100
	v_mov_b32_e32 v193, v192
	v_pk_mul_f32 v[220:221], v[192:193], v[108:109]
	v_pk_mul_f32 v[202:203], v[220:221], v[202:203]
	v_lshl_add_u64 v[146:147], v[146:147], 0, s[10:11]
	v_lshlrev_b64 v[146:147], 8, v[146:147]
	v_lshl_add_u64 v[146:147], v[196:197], 0, v[146:147]
	v_cvt_pk_bf16_f32 v220, v148, v149
	v_cvt_pk_bf16_f32 v221, v198, v199
	v_cvt_pk_bf16_f32 v222, v200, v201
	v_cvt_pk_bf16_f32 v223, v202, v203
	global_store_dwordx4 v[146:147], v[220:223], off
	s_nop 1
	v_cvt_f32_i32_e32 v147, v95
	v_cvt_f32_i32_e32 v146, v94
	v_pk_mul_f32 v[148:149], v[190:191], v[130:131] op_sel_hi:[0,1]
	v_pk_mul_f32 v[148:149], v[148:149], v[146:147]
	v_cvt_f32_i32_e32 v147, v97
	v_cvt_f32_i32_e32 v146, v96
	v_mov_b32_e32 v191, v190
	v_pk_mul_f32 v[198:199], v[190:191], v[132:133] op_sel_hi:[0,1]
	v_pk_mul_f32 v[198:199], v[198:199], v[146:147]
	v_cvt_f32_i32_e32 v147, v91
	v_cvt_f32_i32_e32 v146, v90
	v_pk_mul_f32 v[200:201], v[190:191], v[126:127]
	v_pk_mul_f32 v[200:201], v[200:201], v[146:147]
	v_cvt_f32_i32_e32 v147, v93
	v_cvt_f32_i32_e32 v146, v92
	v_mov_b32_e32 v202, v190
	v_mov_b32_e32 v203, v190
	v_pk_mul_f32 v[202:203], v[202:203], v[128:129]
	v_pk_mul_f32 v[202:203], v[202:203], v[146:147]
	v_or_b32_e32 v146, 32, v178
	v_mov_b32_e32 v147, v179
	v_cvt_pk_bf16_f32 v220, v148, v149
	v_lshl_add_u64 v[148:149], v[146:147], 0, s[16:17]
	v_lshlrev_b64 v[148:149], 8, v[148:149]
	v_lshl_add_u64 v[148:149], v[196:197], 0, v[148:149]
	v_cvt_pk_bf16_f32 v221, v198, v199
	v_cvt_pk_bf16_f32 v222, v200, v201
	v_cvt_pk_bf16_f32 v223, v202, v203
	global_store_dwordx4 v[148:149], v[220:223], off
	s_nop 1
	v_cvt_f32_i32_e32 v149, v87
	v_cvt_f32_i32_e32 v148, v86
	v_pk_mul_f32 v[198:199], v[190:191], v[110:111]
	v_pk_mul_f32 v[148:149], v[198:199], v[148:149]
	v_cvt_f32_i32_e32 v199, v89
	v_cvt_f32_i32_e32 v198, v88
	v_mov_b32_e32 v200, v190
	v_mov_b32_e32 v201, v190
	v_pk_mul_f32 v[200:201], v[200:201], v[112:113]
	v_pk_mul_f32 v[198:199], v[200:201], v[198:199]
	v_cvt_f32_i32_e32 v201, v83
	v_cvt_f32_i32_e32 v200, v82
	v_pk_mul_f32 v[202:203], v[190:191], v[106:107]
	v_pk_mul_f32 v[200:201], v[202:203], v[200:201]
	v_cvt_f32_i32_e32 v203, v85
	v_cvt_f32_i32_e32 v202, v84
	v_mov_b32_e32 v191, v190
	v_pk_mul_f32 v[220:221], v[190:191], v[108:109]
	v_pk_mul_f32 v[202:203], v[220:221], v[202:203]
	v_lshl_add_u64 v[146:147], v[146:147], 0, s[10:11]
	v_lshlrev_b64 v[146:147], 8, v[146:147]
	v_lshl_add_u64 v[146:147], v[196:197], 0, v[146:147]
	v_cvt_pk_bf16_f32 v220, v148, v149
	v_cvt_pk_bf16_f32 v221, v198, v199
	v_cvt_pk_bf16_f32 v222, v200, v201
	v_cvt_pk_bf16_f32 v223, v202, v203
	global_store_dwordx4 v[146:147], v[220:223], off
	s_nop 1
	v_cvt_f32_i32_e32 v147, v79
	v_cvt_f32_i32_e32 v146, v78
	v_pk_mul_f32 v[148:149], v[188:189], v[130:131] op_sel_hi:[0,1]
	v_pk_mul_f32 v[148:149], v[148:149], v[146:147]
	v_cvt_f32_i32_e32 v147, v81
	v_cvt_f32_i32_e32 v146, v80
	v_mov_b32_e32 v189, v188
	v_pk_mul_f32 v[198:199], v[188:189], v[132:133] op_sel_hi:[0,1]
	v_pk_mul_f32 v[198:199], v[198:199], v[146:147]
	v_cvt_f32_i32_e32 v147, v75
	v_cvt_f32_i32_e32 v146, v74
	v_pk_mul_f32 v[200:201], v[188:189], v[126:127]
	v_pk_mul_f32 v[200:201], v[200:201], v[146:147]
	v_cvt_f32_i32_e32 v147, v77
	v_cvt_f32_i32_e32 v146, v76
	v_mov_b32_e32 v202, v188
	v_mov_b32_e32 v203, v188
	v_pk_mul_f32 v[202:203], v[202:203], v[128:129]
	v_pk_mul_f32 v[202:203], v[202:203], v[146:147]
	v_or_b32_e32 v146, 48, v178
	v_mov_b32_e32 v147, v179
	v_cvt_pk_bf16_f32 v220, v148, v149
	v_lshl_add_u64 v[148:149], v[146:147], 0, s[16:17]
	v_lshlrev_b64 v[148:149], 8, v[148:149]
	v_lshl_add_u64 v[148:149], v[196:197], 0, v[148:149]
	v_cvt_pk_bf16_f32 v221, v198, v199
	v_cvt_pk_bf16_f32 v222, v200, v201
	v_cvt_pk_bf16_f32 v223, v202, v203
	global_store_dwordx4 v[148:149], v[220:223], off
	s_nop 1
	v_cvt_f32_i32_e32 v149, v71
	v_cvt_f32_i32_e32 v148, v70
	v_pk_mul_f32 v[198:199], v[188:189], v[110:111]
	v_pk_mul_f32 v[148:149], v[198:199], v[148:149]
	v_cvt_f32_i32_e32 v199, v73
	v_cvt_f32_i32_e32 v198, v72
	v_mov_b32_e32 v200, v188
	v_mov_b32_e32 v201, v188
	v_pk_mul_f32 v[200:201], v[200:201], v[112:113]
	v_pk_mul_f32 v[198:199], v[200:201], v[198:199]
	v_cvt_f32_i32_e32 v201, v67
	v_cvt_f32_i32_e32 v200, v66
	v_pk_mul_f32 v[202:203], v[188:189], v[106:107]
	v_pk_mul_f32 v[200:201], v[202:203], v[200:201]
	v_cvt_f32_i32_e32 v203, v69
	v_cvt_f32_i32_e32 v202, v68
	v_mov_b32_e32 v189, v188
	v_pk_mul_f32 v[220:221], v[188:189], v[108:109]
	v_pk_mul_f32 v[202:203], v[220:221], v[202:203]
	v_lshl_add_u64 v[146:147], v[146:147], 0, s[10:11]
	v_lshlrev_b64 v[146:147], 8, v[146:147]
	v_lshl_add_u64 v[146:147], v[196:197], 0, v[146:147]
	v_cvt_pk_bf16_f32 v220, v148, v149
	v_cvt_pk_bf16_f32 v221, v198, v199
	v_cvt_pk_bf16_f32 v222, v200, v201
	v_cvt_pk_bf16_f32 v223, v202, v203
	global_store_dwordx4 v[146:147], v[220:223], off
	s_nop 1
	v_cvt_f32_i32_e32 v147, v63
	v_cvt_f32_i32_e32 v146, v62
	v_pk_mul_f32 v[148:149], v[186:187], v[130:131] op_sel_hi:[0,1]
	v_pk_mul_f32 v[148:149], v[148:149], v[146:147]
	v_cvt_f32_i32_e32 v147, v65
	v_cvt_f32_i32_e32 v146, v64
	v_mov_b32_e32 v187, v186
	v_pk_mul_f32 v[198:199], v[186:187], v[132:133] op_sel_hi:[0,1]
	v_pk_mul_f32 v[198:199], v[198:199], v[146:147]
	v_cvt_f32_i32_e32 v147, v59
	v_cvt_f32_i32_e32 v146, v58
	v_pk_mul_f32 v[200:201], v[186:187], v[126:127]
	v_pk_mul_f32 v[200:201], v[200:201], v[146:147]
	v_cvt_f32_i32_e32 v147, v61
	v_cvt_f32_i32_e32 v146, v60
	v_mov_b32_e32 v202, v186
	v_mov_b32_e32 v203, v186
	v_pk_mul_f32 v[202:203], v[202:203], v[128:129]
	v_pk_mul_f32 v[202:203], v[202:203], v[146:147]
	v_lshl_add_u64 v[146:147], v[178:179], 0, s[34:35]
	v_cvt_pk_bf16_f32 v220, v148, v149
	v_lshl_add_u64 v[148:149], v[146:147], 0, s[16:17]
	v_lshlrev_b64 v[148:149], 8, v[148:149]
	v_lshl_add_u64 v[148:149], v[196:197], 0, v[148:149]
	v_cvt_pk_bf16_f32 v221, v198, v199
	v_cvt_pk_bf16_f32 v222, v200, v201
	v_cvt_pk_bf16_f32 v223, v202, v203
	global_store_dwordx4 v[148:149], v[220:223], off
	s_nop 1
	v_cvt_f32_i32_e32 v149, v55
	v_cvt_f32_i32_e32 v148, v54
	v_pk_mul_f32 v[198:199], v[186:187], v[110:111]
	v_pk_mul_f32 v[148:149], v[198:199], v[148:149]
	v_cvt_f32_i32_e32 v199, v57
	v_cvt_f32_i32_e32 v198, v56
	v_mov_b32_e32 v200, v186
	v_mov_b32_e32 v201, v186
	v_pk_mul_f32 v[200:201], v[200:201], v[112:113]
	v_pk_mul_f32 v[198:199], v[200:201], v[198:199]
	v_cvt_f32_i32_e32 v201, v51
	v_cvt_f32_i32_e32 v200, v50
	v_pk_mul_f32 v[202:203], v[186:187], v[106:107]
	v_pk_mul_f32 v[200:201], v[202:203], v[200:201]
	v_cvt_f32_i32_e32 v203, v53
	v_cvt_f32_i32_e32 v202, v52
	v_mov_b32_e32 v187, v186
	v_pk_mul_f32 v[220:221], v[186:187], v[108:109]
	v_pk_mul_f32 v[202:203], v[220:221], v[202:203]
	v_lshl_add_u64 v[146:147], v[146:147], 0, s[10:11]
	v_lshlrev_b64 v[146:147], 8, v[146:147]
	v_lshl_add_u64 v[146:147], v[196:197], 0, v[146:147]
	v_cvt_pk_bf16_f32 v220, v148, v149
	v_cvt_pk_bf16_f32 v221, v198, v199
	v_cvt_pk_bf16_f32 v222, v200, v201
	v_cvt_pk_bf16_f32 v223, v202, v203
	global_store_dwordx4 v[146:147], v[220:223], off
	s_nop 1
	v_cvt_f32_i32_e32 v147, v47
	v_cvt_f32_i32_e32 v146, v46
	v_pk_mul_f32 v[148:149], v[184:185], v[130:131] op_sel_hi:[0,1]
	v_pk_mul_f32 v[148:149], v[148:149], v[146:147]
	v_cvt_f32_i32_e32 v147, v49
	v_cvt_f32_i32_e32 v146, v48
	v_mov_b32_e32 v185, v184
	v_pk_mul_f32 v[198:199], v[184:185], v[132:133] op_sel_hi:[0,1]
	v_pk_mul_f32 v[198:199], v[198:199], v[146:147]
	v_cvt_f32_i32_e32 v147, v43
	v_cvt_f32_i32_e32 v146, v42
	v_pk_mul_f32 v[200:201], v[184:185], v[126:127]
	v_pk_mul_f32 v[200:201], v[200:201], v[146:147]
	v_cvt_f32_i32_e32 v147, v45
	v_cvt_f32_i32_e32 v146, v44
	v_mov_b32_e32 v202, v184
	v_mov_b32_e32 v203, v184
	v_pk_mul_f32 v[202:203], v[202:203], v[128:129]
	v_pk_mul_f32 v[202:203], v[202:203], v[146:147]
	v_lshl_add_u64 v[146:147], v[178:179], 0, s[42:43]
	v_cvt_pk_bf16_f32 v220, v148, v149
	v_lshl_add_u64 v[148:149], v[146:147], 0, s[16:17]
	v_lshlrev_b64 v[148:149], 8, v[148:149]
	v_lshl_add_u64 v[148:149], v[196:197], 0, v[148:149]
	v_cvt_pk_bf16_f32 v221, v198, v199
	v_cvt_pk_bf16_f32 v222, v200, v201
	v_cvt_pk_bf16_f32 v223, v202, v203
	global_store_dwordx4 v[148:149], v[220:223], off
	s_nop 1
	v_cvt_f32_i32_e32 v149, v39
	v_cvt_f32_i32_e32 v148, v38
	v_pk_mul_f32 v[198:199], v[184:185], v[110:111]
	v_pk_mul_f32 v[148:149], v[198:199], v[148:149]
	v_cvt_f32_i32_e32 v199, v41
	v_cvt_f32_i32_e32 v198, v40
	v_mov_b32_e32 v200, v184
	v_mov_b32_e32 v201, v184
	v_pk_mul_f32 v[200:201], v[200:201], v[112:113]
	v_pk_mul_f32 v[198:199], v[200:201], v[198:199]
	v_cvt_f32_i32_e32 v201, v35
	v_cvt_f32_i32_e32 v200, v34
	v_pk_mul_f32 v[202:203], v[184:185], v[106:107]
	v_pk_mul_f32 v[200:201], v[202:203], v[200:201]
	v_cvt_f32_i32_e32 v203, v37
	v_cvt_f32_i32_e32 v202, v36
	v_mov_b32_e32 v185, v184
	v_pk_mul_f32 v[220:221], v[184:185], v[108:109]
	v_pk_mul_f32 v[202:203], v[220:221], v[202:203]
	v_lshl_add_u64 v[146:147], v[146:147], 0, s[10:11]
	v_lshlrev_b64 v[146:147], 8, v[146:147]
	v_lshl_add_u64 v[146:147], v[196:197], 0, v[146:147]
	v_cvt_pk_bf16_f32 v220, v148, v149
	v_cvt_pk_bf16_f32 v221, v198, v199
	v_cvt_pk_bf16_f32 v222, v200, v201
	v_cvt_pk_bf16_f32 v223, v202, v203
	global_store_dwordx4 v[146:147], v[220:223], off
	s_nop 1
	v_cvt_f32_i32_e32 v147, v31
	v_cvt_f32_i32_e32 v146, v30
	v_pk_mul_f32 v[148:149], v[182:183], v[130:131] op_sel_hi:[0,1]
	v_pk_mul_f32 v[148:149], v[148:149], v[146:147]
	v_cvt_f32_i32_e32 v147, v33
	v_cvt_f32_i32_e32 v146, v32
	v_mov_b32_e32 v183, v182
	v_pk_mul_f32 v[198:199], v[182:183], v[132:133] op_sel_hi:[0,1]
	v_pk_mul_f32 v[198:199], v[198:199], v[146:147]
	v_cvt_f32_i32_e32 v147, v27
	v_cvt_f32_i32_e32 v146, v26
	v_pk_mul_f32 v[200:201], v[182:183], v[126:127]
	v_pk_mul_f32 v[200:201], v[200:201], v[146:147]
	v_cvt_f32_i32_e32 v147, v29
	v_cvt_f32_i32_e32 v146, v28
	v_mov_b32_e32 v202, v182
	v_mov_b32_e32 v203, v182
	v_pk_mul_f32 v[202:203], v[202:203], v[128:129]
	v_pk_mul_f32 v[202:203], v[202:203], v[146:147]
	v_lshl_add_u64 v[146:147], v[178:179], 0, s[52:53]
	v_cvt_pk_bf16_f32 v220, v148, v149
	v_lshl_add_u64 v[148:149], v[146:147], 0, s[16:17]
	v_lshlrev_b64 v[148:149], 8, v[148:149]
	v_lshl_add_u64 v[148:149], v[196:197], 0, v[148:149]
	v_cvt_pk_bf16_f32 v221, v198, v199
	v_cvt_pk_bf16_f32 v222, v200, v201
	v_cvt_pk_bf16_f32 v223, v202, v203
	global_store_dwordx4 v[148:149], v[220:223], off
	s_nop 1
	v_cvt_f32_i32_e32 v149, v23
	v_cvt_f32_i32_e32 v148, v22
	v_pk_mul_f32 v[198:199], v[182:183], v[110:111]
	v_pk_mul_f32 v[148:149], v[198:199], v[148:149]
	v_cvt_f32_i32_e32 v199, v25
	v_cvt_f32_i32_e32 v198, v24
	v_mov_b32_e32 v200, v182
	v_mov_b32_e32 v201, v182
	v_pk_mul_f32 v[200:201], v[200:201], v[112:113]
	v_pk_mul_f32 v[198:199], v[200:201], v[198:199]
	v_cvt_f32_i32_e32 v201, v19
	v_cvt_f32_i32_e32 v200, v18
	v_pk_mul_f32 v[202:203], v[182:183], v[106:107]
	v_pk_mul_f32 v[200:201], v[202:203], v[200:201]
	v_cvt_f32_i32_e32 v203, v21
	v_cvt_f32_i32_e32 v202, v20
	v_mov_b32_e32 v183, v182
	v_pk_mul_f32 v[220:221], v[182:183], v[108:109]
	v_pk_mul_f32 v[202:203], v[220:221], v[202:203]
	v_lshl_add_u64 v[146:147], v[146:147], 0, s[10:11]
	v_lshlrev_b64 v[146:147], 8, v[146:147]
	v_lshl_add_u64 v[146:147], v[196:197], 0, v[146:147]
	v_cvt_pk_bf16_f32 v220, v148, v149
	v_cvt_pk_bf16_f32 v221, v198, v199
	v_cvt_pk_bf16_f32 v222, v200, v201
	v_cvt_pk_bf16_f32 v223, v202, v203
	global_store_dwordx4 v[146:147], v[220:223], off
	s_nop 1
	v_cvt_f32_i32_e32 v147, v15
	v_cvt_f32_i32_e32 v146, v14
	v_pk_mul_f32 v[148:149], v[130:131], v[180:181] op_sel_hi:[1,0]
	v_pk_mul_f32 v[146:147], v[148:149], v[146:147]
	v_cvt_f32_i32_e32 v149, v17
	v_cvt_f32_i32_e32 v148, v16
	v_mov_b32_e32 v181, v180
	v_pk_mul_f32 v[198:199], v[132:133], v[180:181] op_sel_hi:[1,0]
	v_pk_mul_f32 v[148:149], v[198:199], v[148:149]
	v_cvt_f32_i32_e32 v199, v11
	v_cvt_f32_i32_e32 v198, v10
	v_pk_mul_f32 v[200:201], v[180:181], v[126:127]
	v_pk_mul_f32 v[200:201], v[200:201], v[198:199]
	v_cvt_f32_i32_e32 v199, v13
	v_cvt_f32_i32_e32 v198, v12
	v_mov_b32_e32 v202, v180
	v_mov_b32_e32 v203, v180
	v_pk_mul_f32 v[202:203], v[202:203], v[128:129]
	v_pk_mul_f32 v[202:203], v[202:203], v[198:199]
	v_lshl_add_u64 v[198:199], v[178:179], 0, s[54:55]
	v_cvt_pk_bf16_f32 v146, v146, v147
	v_cvt_pk_bf16_f32 v147, v148, v149
	v_cvt_pk_bf16_f32 v148, v200, v201
	v_lshl_add_u64 v[200:201], v[198:199], 0, s[16:17]
	v_lshlrev_b64 v[200:201], 8, v[200:201]
	v_lshl_add_u64 v[200:201], v[196:197], 0, v[200:201]
	v_cvt_pk_bf16_f32 v149, v202, v203
	global_store_dwordx4 v[200:201], v[146:149], off
	s_nop 1
	v_cvt_f32_i32_e32 v147, v7
	v_cvt_f32_i32_e32 v146, v6
	v_pk_mul_f32 v[148:149], v[180:181], v[110:111]
	v_pk_mul_f32 v[146:147], v[148:149], v[146:147]
	v_cvt_f32_i32_e32 v149, v9
	v_cvt_f32_i32_e32 v148, v8
	v_mov_b32_e32 v200, v180
	v_mov_b32_e32 v201, v180
	v_pk_mul_f32 v[200:201], v[200:201], v[112:113]
	v_pk_mul_f32 v[148:149], v[200:201], v[148:149]
	v_cvt_f32_i32_e32 v201, v3
	v_cvt_f32_i32_e32 v200, v2
	v_pk_mul_f32 v[202:203], v[180:181], v[106:107]
	v_pk_mul_f32 v[200:201], v[202:203], v[200:201]
	v_cvt_f32_i32_e32 v203, v5
	v_cvt_f32_i32_e32 v202, v4
	v_mov_b32_e32 v181, v180
	v_pk_mul_f32 v[220:221], v[180:181], v[108:109]
	v_pk_mul_f32 v[202:203], v[220:221], v[202:203]
	v_cvt_pk_bf16_f32 v146, v146, v147
	v_cvt_pk_bf16_f32 v147, v148, v149
	v_cvt_pk_bf16_f32 v148, v200, v201
	v_cvt_pk_bf16_f32 v149, v202, v203
	v_lshl_add_u64 v[198:199], v[198:199], 0, s[10:11]
	s_branch .LBB0_354
